# layer-1 kernel hand-written: 512 persistent workers, 4 row slots per wave swept by column window with fp16 fma_mix, clock-paced so all waves stay in the same window (L2 reuse); k_l2 window-sorted CSR
# speedup vs baseline: 1.0274x; 1.0099x over previous
_Z6k_spmmILb0ELi0EEvPKiPK15HIP_vector_typeIiLj2EEPKvPKfPKDF16_S9_S9_iPfPDF16_PhSC_PKhS9_SG_S9_S9_i:
	s_cmpk_ge_u32 s2, 512
	s_cbranch_scc1 .Lsw_exit
	s_load_dwordx8 s[4:11], s[0:1], 0x0
	s_load_dwordx4 s[12:15], s[0:1], 0x20
	s_load_dwordx2 s[16:17], s[0:1], 0x30
	s_load_dword s18, s[0:1], 0x38
	s_load_dwordx4 s[20:23], s[0:1], 0x48
	s_load_dwordx2 s[24:25], s[0:1], 0x58
	s_load_dword s27, s[0:1], 0x88
	v_and_b32_e32 v1, 15, v0
	v_lshlrev_b32_e32 v2, 4, v1
	v_bfe_u32 v3, v0, 4, 5
	v_lshlrev_b32_e32 v4, 3, v0
	v_add_u32_e32 v4, 0x8000, v4
	v_lshrrev_b32_e32 v5, 4, v0
	v_lshlrev_b32_e32 v5, 7, v5
	v_add_u32_e32 v5, 0x8000, v5
	v_and_b32_e32 v6, 48, v0
	s_waitcnt lgkmcnt(0)
	v_add_u32_e32 v104, 0, v0
	v_cmp_gt_u32_e32 vcc, s27, v104
	v_lshlrev_b32_e32 v104, 2, v104
	s_and_saveexec_b64 s[36:37], vcc
	global_load_dword v56, v104, s[10:11]
	s_mov_b64 exec, s[36:37]
	v_add_u32_e32 v104, 512, v0
	v_cmp_gt_u32_e32 vcc, s27, v104
	v_lshlrev_b32_e32 v104, 2, v104
	s_and_saveexec_b64 s[36:37], vcc
	global_load_dword v57, v104, s[10:11]
	s_mov_b64 exec, s[36:37]
	v_add_u32_e32 v104, 1024, v0
	v_cmp_gt_u32_e32 vcc, s27, v104
	v_lshlrev_b32_e32 v104, 2, v104
	s_and_saveexec_b64 s[36:37], vcc
	global_load_dword v58, v104, s[10:11]
	s_mov_b64 exec, s[36:37]
	v_add_u32_e32 v104, 1536, v0
	v_cmp_gt_u32_e32 vcc, s27, v104
	v_lshlrev_b32_e32 v104, 2, v104
	s_and_saveexec_b64 s[36:37], vcc
	global_load_dword v59, v104, s[10:11]
	s_mov_b64 exec, s[36:37]
	v_add_u32_e32 v104, 2048, v0
	v_cmp_gt_u32_e32 vcc, s27, v104
	v_lshlrev_b32_e32 v104, 2, v104
	s_and_saveexec_b64 s[36:37], vcc
	global_load_dword v60, v104, s[10:11]
	s_mov_b64 exec, s[36:37]
	v_add_u32_e32 v104, 2560, v0
	v_cmp_gt_u32_e32 vcc, s27, v104
	v_lshlrev_b32_e32 v104, 2, v104
	s_and_saveexec_b64 s[36:37], vcc
	global_load_dword v61, v104, s[10:11]
	s_mov_b64 exec, s[36:37]
	v_add_u32_e32 v104, 3072, v0
	v_cmp_gt_u32_e32 vcc, s27, v104
	v_lshlrev_b32_e32 v104, 2, v104
	s_and_saveexec_b64 s[36:37], vcc
	global_load_dword v62, v104, s[10:11]
	s_mov_b64 exec, s[36:37]
	v_add_u32_e32 v104, 3584, v0
	v_cmp_gt_u32_e32 vcc, s27, v104
	v_lshlrev_b32_e32 v104, 2, v104
	s_and_saveexec_b64 s[36:37], vcc
	global_load_dword v63, v104, s[10:11]
	s_mov_b64 exec, s[36:37]
	v_add_u32_e32 v104, 4096, v0
	v_cmp_gt_u32_e32 vcc, s27, v104
	v_lshlrev_b32_e32 v104, 2, v104
	s_and_saveexec_b64 s[36:37], vcc
	global_load_dword v64, v104, s[10:11]
	s_mov_b64 exec, s[36:37]
	v_add_u32_e32 v104, 4608, v0
	v_cmp_gt_u32_e32 vcc, s27, v104
	v_lshlrev_b32_e32 v104, 2, v104
	s_and_saveexec_b64 s[36:37], vcc
	global_load_dword v65, v104, s[10:11]
	s_mov_b64 exec, s[36:37]
	v_add_u32_e32 v104, 5120, v0
	v_cmp_gt_u32_e32 vcc, s27, v104
	v_lshlrev_b32_e32 v104, 2, v104
	s_and_saveexec_b64 s[36:37], vcc
	global_load_dword v66, v104, s[10:11]
	s_mov_b64 exec, s[36:37]
	v_add_u32_e32 v104, 5632, v0
	v_cmp_gt_u32_e32 vcc, s27, v104
	v_lshlrev_b32_e32 v104, 2, v104
	s_and_saveexec_b64 s[36:37], vcc
	global_load_dword v67, v104, s[10:11]
	s_mov_b64 exec, s[36:37]
	v_add_u32_e32 v104, 6144, v0
	v_cmp_gt_u32_e32 vcc, s27, v104
	v_lshlrev_b32_e32 v104, 2, v104
	s_and_saveexec_b64 s[36:37], vcc
	global_load_dword v68, v104, s[10:11]
	s_mov_b64 exec, s[36:37]
	v_add_u32_e32 v104, 6656, v0
	v_cmp_gt_u32_e32 vcc, s27, v104
	v_lshlrev_b32_e32 v104, 2, v104
	s_and_saveexec_b64 s[36:37], vcc
	global_load_dword v69, v104, s[10:11]
	s_mov_b64 exec, s[36:37]
	v_add_u32_e32 v104, 7168, v0
	v_cmp_gt_u32_e32 vcc, s27, v104
	v_lshlrev_b32_e32 v104, 2, v104
	s_and_saveexec_b64 s[36:37], vcc
	global_load_dword v70, v104, s[10:11]
	s_mov_b64 exec, s[36:37]
	v_add_u32_e32 v104, 7680, v0
	v_cmp_gt_u32_e32 vcc, s27, v104
	v_lshlrev_b32_e32 v104, 2, v104
	s_and_saveexec_b64 s[36:37], vcc
	global_load_dword v71, v104, s[10:11]
	s_mov_b64 exec, s[36:37]
	s_waitcnt vmcnt(0)
	v_add_u32_e32 v104, 0, v0
	v_cmp_gt_u32_e32 vcc, s27, v104
	v_lshlrev_b32_e32 v104, 2, v104
	s_and_saveexec_b64 s[36:37], vcc
	ds_write_b32 v104, v56
	s_mov_b64 exec, s[36:37]
	v_add_u32_e32 v104, 512, v0
	v_cmp_gt_u32_e32 vcc, s27, v104
	v_lshlrev_b32_e32 v104, 2, v104
	s_and_saveexec_b64 s[36:37], vcc
	ds_write_b32 v104, v57
	s_mov_b64 exec, s[36:37]
	v_add_u32_e32 v104, 1024, v0
	v_cmp_gt_u32_e32 vcc, s27, v104
	v_lshlrev_b32_e32 v104, 2, v104
	s_and_saveexec_b64 s[36:37], vcc
	ds_write_b32 v104, v58
	s_mov_b64 exec, s[36:37]
	v_add_u32_e32 v104, 1536, v0
	v_cmp_gt_u32_e32 vcc, s27, v104
	v_lshlrev_b32_e32 v104, 2, v104
	s_and_saveexec_b64 s[36:37], vcc
	ds_write_b32 v104, v59
	s_mov_b64 exec, s[36:37]
	v_add_u32_e32 v104, 2048, v0
	v_cmp_gt_u32_e32 vcc, s27, v104
	v_lshlrev_b32_e32 v104, 2, v104
	s_and_saveexec_b64 s[36:37], vcc
	ds_write_b32 v104, v60
	s_mov_b64 exec, s[36:37]
	v_add_u32_e32 v104, 2560, v0
	v_cmp_gt_u32_e32 vcc, s27, v104
	v_lshlrev_b32_e32 v104, 2, v104
	s_and_saveexec_b64 s[36:37], vcc
	ds_write_b32 v104, v61
	s_mov_b64 exec, s[36:37]
	v_add_u32_e32 v104, 3072, v0
	v_cmp_gt_u32_e32 vcc, s27, v104
	v_lshlrev_b32_e32 v104, 2, v104
	s_and_saveexec_b64 s[36:37], vcc
	ds_write_b32 v104, v62
	s_mov_b64 exec, s[36:37]
	v_add_u32_e32 v104, 3584, v0
	v_cmp_gt_u32_e32 vcc, s27, v104
	v_lshlrev_b32_e32 v104, 2, v104
	s_and_saveexec_b64 s[36:37], vcc
	ds_write_b32 v104, v63
	s_mov_b64 exec, s[36:37]
	v_add_u32_e32 v104, 4096, v0
	v_cmp_gt_u32_e32 vcc, s27, v104
	v_lshlrev_b32_e32 v104, 2, v104
	s_and_saveexec_b64 s[36:37], vcc
	ds_write_b32 v104, v64
	s_mov_b64 exec, s[36:37]
	v_add_u32_e32 v104, 4608, v0
	v_cmp_gt_u32_e32 vcc, s27, v104
	v_lshlrev_b32_e32 v104, 2, v104
	s_and_saveexec_b64 s[36:37], vcc
	ds_write_b32 v104, v65
	s_mov_b64 exec, s[36:37]
	v_add_u32_e32 v104, 5120, v0
	v_cmp_gt_u32_e32 vcc, s27, v104
	v_lshlrev_b32_e32 v104, 2, v104
	s_and_saveexec_b64 s[36:37], vcc
	ds_write_b32 v104, v66
	s_mov_b64 exec, s[36:37]
	v_add_u32_e32 v104, 5632, v0
	v_cmp_gt_u32_e32 vcc, s27, v104
	v_lshlrev_b32_e32 v104, 2, v104
	s_and_saveexec_b64 s[36:37], vcc
	ds_write_b32 v104, v67
	s_mov_b64 exec, s[36:37]
	v_add_u32_e32 v104, 6144, v0
	v_cmp_gt_u32_e32 vcc, s27, v104
	v_lshlrev_b32_e32 v104, 2, v104
	s_and_saveexec_b64 s[36:37], vcc
	ds_write_b32 v104, v68
	s_mov_b64 exec, s[36:37]
	v_add_u32_e32 v104, 6656, v0
	v_cmp_gt_u32_e32 vcc, s27, v104
	v_lshlrev_b32_e32 v104, 2, v104
	s_and_saveexec_b64 s[36:37], vcc
	ds_write_b32 v104, v69
	s_mov_b64 exec, s[36:37]
	v_add_u32_e32 v104, 7168, v0
	v_cmp_gt_u32_e32 vcc, s27, v104
	v_lshlrev_b32_e32 v104, 2, v104
	s_and_saveexec_b64 s[36:37], vcc
	ds_write_b32 v104, v70
	s_mov_b64 exec, s[36:37]
	v_add_u32_e32 v104, 7680, v0
	v_cmp_gt_u32_e32 vcc, s27, v104
	v_lshlrev_b32_e32 v104, 2, v104
	s_and_saveexec_b64 s[36:37], vcc
	ds_write_b32 v104, v71
	s_mov_b64 exec, s[36:37]
	s_waitcnt lgkmcnt(0)
	s_barrier
	s_add_u32 s35, s27, 511
	s_lshr_b32 s35, s35, 9
	s_add_u32 s35, s35, 7
	s_lshr_b32 s35, s35, 3
	s_lshl_b32 s35, s35, 1
	s_mov_b32 s26, 0
.Lsw_sweep:
	s_lshr_b32 s40, s26, 1
	s_lshl_b32 s40, s40, 2
	s_and_b32 s41, s26, 1
	s_add_u32 s40, s40, s41
	s_lshl_b32 s40, s40, 1
	s_lshl_b32 s40, s40, 9
	s_add_u32 s40, s40, s2
	s_sub_u32 s41, s27, s40
	s_sub_u32 s41, s41, 1
	s_cmp_lt_u32 s40, s27
	s_cselect_b64 s[42:43], -1, 0
	v_lshl_add_u32 v56, s41, 5, v3
	v_cmp_gt_i32_e32 vcc, s18, v56
	s_and_b64 s[44:45], vcc, s[42:43]
	v_lshlrev_b32_e32 v60, 2, v56
	v_mov_b32_e32 v64, 0
	v_mov_b32_e32 v65, 0
	s_lshr_b32 s40, s26, 1
	s_lshl_b32 s40, s40, 2
	s_and_b32 s41, s26, 1
	s_add_u32 s40, s40, s41
	s_lshl_b32 s40, s40, 1
	s_or_b32 s40, s40, 1
	s_lshl_b32 s40, s40, 9
	s_add_u32 s40, s40, s2
	s_sub_u32 s41, s27, s40
	s_sub_u32 s41, s41, 1
	s_cmp_lt_u32 s40, s27
	s_cselect_b64 s[42:43], -1, 0
	v_lshl_add_u32 v56, s41, 5, v3
	v_cmp_gt_i32_e32 vcc, s18, v56
	s_and_b64 s[46:47], vcc, s[42:43]
	v_lshlrev_b32_e32 v61, 2, v56
	v_mov_b32_e32 v66, 0
	v_mov_b32_e32 v67, 0
	s_lshr_b32 s40, s26, 1
	s_lshl_b32 s40, s40, 2
	s_and_b32 s41, s26, 1
	s_add_u32 s40, s40, s41
	s_add_u32 s40, s40, 2
	s_lshl_b32 s40, s40, 1
	s_lshl_b32 s40, s40, 9
	s_add_u32 s40, s40, s2
	s_sub_u32 s41, s27, s40
	s_sub_u32 s41, s41, 1
	s_cmp_lt_u32 s40, s27
	s_cselect_b64 s[42:43], -1, 0
	v_lshl_add_u32 v56, s41, 5, v3
	v_cmp_gt_i32_e32 vcc, s18, v56
	s_and_b64 s[48:49], vcc, s[42:43]
	v_lshlrev_b32_e32 v62, 2, v56
	v_mov_b32_e32 v68, 0
	v_mov_b32_e32 v69, 0
	s_lshr_b32 s40, s26, 1
	s_lshl_b32 s40, s40, 2
	s_and_b32 s41, s26, 1
	s_add_u32 s40, s40, s41
	s_add_u32 s40, s40, 2
	s_lshl_b32 s40, s40, 1
	s_or_b32 s40, s40, 1
	s_lshl_b32 s40, s40, 9
	s_add_u32 s40, s40, s2
	s_sub_u32 s41, s27, s40
	s_sub_u32 s41, s41, 1
	s_cmp_lt_u32 s40, s27
	s_cselect_b64 s[42:43], -1, 0
	v_lshl_add_u32 v56, s41, 5, v3
	v_cmp_gt_i32_e32 vcc, s18, v56
	s_and_b64 s[50:51], vcc, s[42:43]
	v_lshlrev_b32_e32 v63, 2, v56
	v_mov_b32_e32 v70, 0
	v_mov_b32_e32 v71, 0
	s_mov_b64 s[36:37], exec
	s_and_b64 exec, exec, s[44:45]
	global_load_dwordx2 v[64:65], v60, s[4:5]
	s_mov_b64 exec, s[36:37]
	s_mov_b64 s[36:37], exec
	s_and_b64 exec, exec, s[46:47]
	global_load_dwordx2 v[66:67], v61, s[4:5]
	s_mov_b64 exec, s[36:37]
	s_mov_b64 s[36:37], exec
	s_and_b64 exec, exec, s[48:49]
	global_load_dwordx2 v[68:69], v62, s[4:5]
	s_mov_b64 exec, s[36:37]
	s_mov_b64 s[36:37], exec
	s_and_b64 exec, exec, s[50:51]
	global_load_dwordx2 v[70:71], v63, s[4:5]
	s_mov_b64 exec, s[36:37]
	s_waitcnt vmcnt(0)
	v_mov_b32_e32 v40, v64
	v_sub_u32_e32 v44, v65, v64
	v_mov_b32_e32 v8, 0
	v_mov_b32_e32 v9, 0
	v_mov_b32_e32 v10, 0
	v_mov_b32_e32 v11, 0
	v_mov_b32_e32 v12, 0
	v_mov_b32_e32 v13, 0
	v_mov_b32_e32 v14, 0
	v_mov_b32_e32 v15, 0
	v_mov_b32_e32 v41, v66
	v_sub_u32_e32 v45, v67, v66
	v_mov_b32_e32 v16, 0
	v_mov_b32_e32 v17, 0
	v_mov_b32_e32 v18, 0
	v_mov_b32_e32 v19, 0
	v_mov_b32_e32 v20, 0
	v_mov_b32_e32 v21, 0
	v_mov_b32_e32 v22, 0
	v_mov_b32_e32 v23, 0
	v_mov_b32_e32 v42, v68
	v_sub_u32_e32 v46, v69, v68
	v_mov_b32_e32 v24, 0
	v_mov_b32_e32 v25, 0
	v_mov_b32_e32 v26, 0
	v_mov_b32_e32 v27, 0
	v_mov_b32_e32 v28, 0
	v_mov_b32_e32 v29, 0
	v_mov_b32_e32 v30, 0
	v_mov_b32_e32 v31, 0
	v_mov_b32_e32 v43, v70
	v_sub_u32_e32 v47, v71, v70
	v_mov_b32_e32 v32, 0
	v_mov_b32_e32 v33, 0
	v_mov_b32_e32 v34, 0
	v_mov_b32_e32 v35, 0
	v_mov_b32_e32 v36, 0
	v_mov_b32_e32 v37, 0
	v_mov_b32_e32 v38, 0
	v_mov_b32_e32 v39, 0
	v_mov_b32_e32 v48, 0
	v_mov_b32_e32 v49, 0
	v_cmp_lt_u32_e32 vcc, v1, v44
	v_add_u32_e32 v56, v40, v1
	v_lshlrev_b32_e32 v56, 3, v56
	s_and_saveexec_b64 s[36:37], vcc
	global_load_dwordx2 v[48:49], v56, s[6:7]
	s_mov_b64 exec, s[36:37]
	v_mov_b32_e32 v50, 0
	v_mov_b32_e32 v51, 0
	v_cmp_lt_u32_e32 vcc, v1, v45
	v_add_u32_e32 v56, v41, v1
	v_lshlrev_b32_e32 v56, 3, v56
	s_and_saveexec_b64 s[36:37], vcc
	global_load_dwordx2 v[50:51], v56, s[6:7]
	s_mov_b64 exec, s[36:37]
	v_mov_b32_e32 v52, 0
	v_mov_b32_e32 v53, 0
	v_cmp_lt_u32_e32 vcc, v1, v46
	v_add_u32_e32 v56, v42, v1
	v_lshlrev_b32_e32 v56, 3, v56
	s_and_saveexec_b64 s[36:37], vcc
	global_load_dwordx2 v[52:53], v56, s[6:7]
	s_mov_b64 exec, s[36:37]
	v_mov_b32_e32 v54, 0
	v_mov_b32_e32 v55, 0
	v_cmp_lt_u32_e32 vcc, v1, v47
	v_add_u32_e32 v56, v43, v1
	v_lshlrev_b32_e32 v56, 3, v56
	s_and_saveexec_b64 s[36:37], vcc
	global_load_dwordx2 v[54:55], v56, s[6:7]
	s_mov_b64 exec, s[36:37]
	s_memrealtime s[62:63]
	s_mov_b32 s60, 0
	s_waitcnt lgkmcnt(0)
	s_mov_b32 s61, s62
	s_add_u32 s40, s18, 8191
	s_lshr_b32 s54, s40, 13
	s_sub_u32 s41, s54, 1
	s_and_b32 s40, s26, 1
	s_cmp_eq_u32 s40, 0
	s_cselect_b32 s55, 0, s41
	s_cselect_b32 s56, 1, -1
	s_mov_b32 s57, 0
.Lsw_win:
.Lsw_wk0:
	s_waitcnt vmcnt(0)
	v_lshrrev_b32_e32 v57, 13, v48
	v_cmp_eq_u32_e32 vcc, s55, v57
	v_cmp_lt_u32_e64 s[52:53], v1, v44
	s_and_b64 s[50:51], vcc, s[52:53]
	s_cmp_lg_u64 s[50:51], 0
	s_cbranch_scc0 .Lsw_wskip0
	v_lshrrev_b64 v[58:59], v6, s[50:51]
	v_lshrrev_b32_e32 v56, 5, v48
	v_not_b32_e32 v58, v58
	v_lshlrev_b32_e32 v56, 2, v56
	v_or_b32_e32 v58, 0x10000, v58
	ds_read_b32 v57, v56
	v_ffbl_b32_e32 v60, v58
	s_nop 0
	v_cmp_lt_u32_e32 vcc, v1, v60
	s_waitcnt lgkmcnt(0)
	v_mul_f32_e32 v59, v49, v57
	v_cndmask_b32_e32 v58, 0, v48, vcc
	v_cndmask_b32_e32 v59, 0, v59, vcc
	ds_write_b64 v4, v[58:59]
	v_add_u32_e32 v40, v40, v60
	v_sub_u32_e32 v44, v44, v60
	v_cmp_lt_u32_e32 vcc, v1, v44
	v_add_u32_e32 v56, v40, v1
	v_lshlrev_b32_e32 v56, 3, v56
	v_mov_b32_e32 v48, 0
	v_mov_b32_e32 v49, 0
	s_and_saveexec_b64 s[36:37], vcc
	global_load_dwordx2 v[48:49], v56, s[6:7]
	s_mov_b64 exec, s[36:37]
	v_readlane_b32 s40, v60, 0
	v_readlane_b32 s41, v60, 16
	v_readlane_b32 s42, v60, 32
	v_readlane_b32 s43, v60, 48
	s_nop 0
	s_max_u32 s40, s40, s41
	s_max_u32 s42, s42, s43
	s_max_u32 s40, s40, s42
	s_mov_b32 s58, s40
.Lsw_pace0:
	s_memrealtime s[62:63]
	s_mul_i32 s59, s60, 130
	s_waitcnt lgkmcnt(0)
	s_sub_u32 s62, s62, s61
	s_cmp_lt_u32 s62, s59
	s_cbranch_scc0 .Lsw_go0
	s_sleep 1
	s_branch .Lsw_pace0
.Lsw_go0:
	s_add_u32 s60, s60, 1
	s_cmp_gt_u32 s40, 8
	s_addc_u32 s60, s60, 0
	ds_read_b128 v[56:59], v5 offset:0
	ds_read_b128 v[60:63], v5 offset:16
	ds_read_b128 v[64:67], v5 offset:32
	ds_read_b128 v[68:71], v5 offset:48
	s_waitcnt lgkmcnt(0)
	v_lshl_or_b32 v104, v56, 8, v2
	global_load_dwordx4 v[72:75], v104, s[8:9]
	v_lshl_or_b32 v104, v58, 8, v2
	global_load_dwordx4 v[76:79], v104, s[8:9]
	v_lshl_or_b32 v104, v60, 8, v2
	global_load_dwordx4 v[80:83], v104, s[8:9]
	v_lshl_or_b32 v104, v62, 8, v2
	global_load_dwordx4 v[84:87], v104, s[8:9]
	v_lshl_or_b32 v104, v64, 8, v2
	global_load_dwordx4 v[88:91], v104, s[8:9]
	v_lshl_or_b32 v104, v66, 8, v2
	global_load_dwordx4 v[92:95], v104, s[8:9]
	v_lshl_or_b32 v104, v68, 8, v2
	global_load_dwordx4 v[96:99], v104, s[8:9]
	v_lshl_or_b32 v104, v70, 8, v2
	global_load_dwordx4 v[100:103], v104, s[8:9]
	s_waitcnt vmcnt(7)
	v_fma_mix_f32 v8, v57, v72, v8 op_sel_hi:[0,1,0]
	v_fma_mix_f32 v9, v57, v72, v9 op_sel:[0,1,0] op_sel_hi:[0,1,0]
	v_fma_mix_f32 v10, v57, v73, v10 op_sel_hi:[0,1,0]
	v_fma_mix_f32 v11, v57, v73, v11 op_sel:[0,1,0] op_sel_hi:[0,1,0]
	v_fma_mix_f32 v12, v57, v74, v12 op_sel_hi:[0,1,0]
	v_fma_mix_f32 v13, v57, v74, v13 op_sel:[0,1,0] op_sel_hi:[0,1,0]
	v_fma_mix_f32 v14, v57, v75, v14 op_sel_hi:[0,1,0]
	v_fma_mix_f32 v15, v57, v75, v15 op_sel:[0,1,0] op_sel_hi:[0,1,0]
	s_waitcnt vmcnt(6)
	v_fma_mix_f32 v8, v59, v76, v8 op_sel_hi:[0,1,0]
	v_fma_mix_f32 v9, v59, v76, v9 op_sel:[0,1,0] op_sel_hi:[0,1,0]
	v_fma_mix_f32 v10, v59, v77, v10 op_sel_hi:[0,1,0]
	v_fma_mix_f32 v11, v59, v77, v11 op_sel:[0,1,0] op_sel_hi:[0,1,0]
	v_fma_mix_f32 v12, v59, v78, v12 op_sel_hi:[0,1,0]
	v_fma_mix_f32 v13, v59, v78, v13 op_sel:[0,1,0] op_sel_hi:[0,1,0]
	v_fma_mix_f32 v14, v59, v79, v14 op_sel_hi:[0,1,0]
	v_fma_mix_f32 v15, v59, v79, v15 op_sel:[0,1,0] op_sel_hi:[0,1,0]
	s_waitcnt vmcnt(5)
	v_fma_mix_f32 v8, v61, v80, v8 op_sel_hi:[0,1,0]
	v_fma_mix_f32 v9, v61, v80, v9 op_sel:[0,1,0] op_sel_hi:[0,1,0]
	v_fma_mix_f32 v10, v61, v81, v10 op_sel_hi:[0,1,0]
	v_fma_mix_f32 v11, v61, v81, v11 op_sel:[0,1,0] op_sel_hi:[0,1,0]
	v_fma_mix_f32 v12, v61, v82, v12 op_sel_hi:[0,1,0]
	v_fma_mix_f32 v13, v61, v82, v13 op_sel:[0,1,0] op_sel_hi:[0,1,0]
	v_fma_mix_f32 v14, v61, v83, v14 op_sel_hi:[0,1,0]
	v_fma_mix_f32 v15, v61, v83, v15 op_sel:[0,1,0] op_sel_hi:[0,1,0]
	s_waitcnt vmcnt(4)
	v_fma_mix_f32 v8, v63, v84, v8 op_sel_hi:[0,1,0]
	v_fma_mix_f32 v9, v63, v84, v9 op_sel:[0,1,0] op_sel_hi:[0,1,0]
	v_fma_mix_f32 v10, v63, v85, v10 op_sel_hi:[0,1,0]
	v_fma_mix_f32 v11, v63, v85, v11 op_sel:[0,1,0] op_sel_hi:[0,1,0]
	v_fma_mix_f32 v12, v63, v86, v12 op_sel_hi:[0,1,0]
	v_fma_mix_f32 v13, v63, v86, v13 op_sel:[0,1,0] op_sel_hi:[0,1,0]
	v_fma_mix_f32 v14, v63, v87, v14 op_sel_hi:[0,1,0]
	v_fma_mix_f32 v15, v63, v87, v15 op_sel:[0,1,0] op_sel_hi:[0,1,0]
	s_waitcnt vmcnt(3)
	v_fma_mix_f32 v8, v65, v88, v8 op_sel_hi:[0,1,0]
	v_fma_mix_f32 v9, v65, v88, v9 op_sel:[0,1,0] op_sel_hi:[0,1,0]
	v_fma_mix_f32 v10, v65, v89, v10 op_sel_hi:[0,1,0]
	v_fma_mix_f32 v11, v65, v89, v11 op_sel:[0,1,0] op_sel_hi:[0,1,0]
	v_fma_mix_f32 v12, v65, v90, v12 op_sel_hi:[0,1,0]
	v_fma_mix_f32 v13, v65, v90, v13 op_sel:[0,1,0] op_sel_hi:[0,1,0]
	v_fma_mix_f32 v14, v65, v91, v14 op_sel_hi:[0,1,0]
	v_fma_mix_f32 v15, v65, v91, v15 op_sel:[0,1,0] op_sel_hi:[0,1,0]
	s_waitcnt vmcnt(2)
	v_fma_mix_f32 v8, v67, v92, v8 op_sel_hi:[0,1,0]
	v_fma_mix_f32 v9, v67, v92, v9 op_sel:[0,1,0] op_sel_hi:[0,1,0]
	v_fma_mix_f32 v10, v67, v93, v10 op_sel_hi:[0,1,0]
	v_fma_mix_f32 v11, v67, v93, v11 op_sel:[0,1,0] op_sel_hi:[0,1,0]
	v_fma_mix_f32 v12, v67, v94, v12 op_sel_hi:[0,1,0]
	v_fma_mix_f32 v13, v67, v94, v13 op_sel:[0,1,0] op_sel_hi:[0,1,0]
	v_fma_mix_f32 v14, v67, v95, v14 op_sel_hi:[0,1,0]
	v_fma_mix_f32 v15, v67, v95, v15 op_sel:[0,1,0] op_sel_hi:[0,1,0]
	s_waitcnt vmcnt(1)
	v_fma_mix_f32 v8, v69, v96, v8 op_sel_hi:[0,1,0]
	v_fma_mix_f32 v9, v69, v96, v9 op_sel:[0,1,0] op_sel_hi:[0,1,0]
	v_fma_mix_f32 v10, v69, v97, v10 op_sel_hi:[0,1,0]
	v_fma_mix_f32 v11, v69, v97, v11 op_sel:[0,1,0] op_sel_hi:[0,1,0]
	v_fma_mix_f32 v12, v69, v98, v12 op_sel_hi:[0,1,0]
	v_fma_mix_f32 v13, v69, v98, v13 op_sel:[0,1,0] op_sel_hi:[0,1,0]
	v_fma_mix_f32 v14, v69, v99, v14 op_sel_hi:[0,1,0]
	v_fma_mix_f32 v15, v69, v99, v15 op_sel:[0,1,0] op_sel_hi:[0,1,0]
	s_waitcnt vmcnt(0)
	v_fma_mix_f32 v8, v71, v100, v8 op_sel_hi:[0,1,0]
	v_fma_mix_f32 v9, v71, v100, v9 op_sel:[0,1,0] op_sel_hi:[0,1,0]
	v_fma_mix_f32 v10, v71, v101, v10 op_sel_hi:[0,1,0]
	v_fma_mix_f32 v11, v71, v101, v11 op_sel:[0,1,0] op_sel_hi:[0,1,0]
	v_fma_mix_f32 v12, v71, v102, v12 op_sel_hi:[0,1,0]
	v_fma_mix_f32 v13, v71, v102, v13 op_sel:[0,1,0] op_sel_hi:[0,1,0]
	v_fma_mix_f32 v14, v71, v103, v14 op_sel_hi:[0,1,0]
	v_fma_mix_f32 v15, v71, v103, v15 op_sel:[0,1,0] op_sel_hi:[0,1,0]
	s_cmp_le_u32 s40, 8
	s_cbranch_scc1 .Lsw_wg0
	ds_read_b128 v[56:59], v5 offset:64
	ds_read_b128 v[60:63], v5 offset:80
	ds_read_b128 v[64:67], v5 offset:96
	ds_read_b128 v[68:71], v5 offset:112
	s_waitcnt lgkmcnt(0)
	v_lshl_or_b32 v104, v56, 8, v2
	global_load_dwordx4 v[72:75], v104, s[8:9]
	v_lshl_or_b32 v104, v58, 8, v2
	global_load_dwordx4 v[76:79], v104, s[8:9]
	v_lshl_or_b32 v104, v60, 8, v2
	global_load_dwordx4 v[80:83], v104, s[8:9]
	v_lshl_or_b32 v104, v62, 8, v2
	global_load_dwordx4 v[84:87], v104, s[8:9]
	v_lshl_or_b32 v104, v64, 8, v2
	global_load_dwordx4 v[88:91], v104, s[8:9]
	v_lshl_or_b32 v104, v66, 8, v2
	global_load_dwordx4 v[92:95], v104, s[8:9]
	v_lshl_or_b32 v104, v68, 8, v2
	global_load_dwordx4 v[96:99], v104, s[8:9]
	v_lshl_or_b32 v104, v70, 8, v2
	global_load_dwordx4 v[100:103], v104, s[8:9]
	s_waitcnt vmcnt(7)
	v_fma_mix_f32 v8, v57, v72, v8 op_sel_hi:[0,1,0]
	v_fma_mix_f32 v9, v57, v72, v9 op_sel:[0,1,0] op_sel_hi:[0,1,0]
	v_fma_mix_f32 v10, v57, v73, v10 op_sel_hi:[0,1,0]
	v_fma_mix_f32 v11, v57, v73, v11 op_sel:[0,1,0] op_sel_hi:[0,1,0]
	v_fma_mix_f32 v12, v57, v74, v12 op_sel_hi:[0,1,0]
	v_fma_mix_f32 v13, v57, v74, v13 op_sel:[0,1,0] op_sel_hi:[0,1,0]
	v_fma_mix_f32 v14, v57, v75, v14 op_sel_hi:[0,1,0]
	v_fma_mix_f32 v15, v57, v75, v15 op_sel:[0,1,0] op_sel_hi:[0,1,0]
	s_waitcnt vmcnt(6)
	v_fma_mix_f32 v8, v59, v76, v8 op_sel_hi:[0,1,0]
	v_fma_mix_f32 v9, v59, v76, v9 op_sel:[0,1,0] op_sel_hi:[0,1,0]
	v_fma_mix_f32 v10, v59, v77, v10 op_sel_hi:[0,1,0]
	v_fma_mix_f32 v11, v59, v77, v11 op_sel:[0,1,0] op_sel_hi:[0,1,0]
	v_fma_mix_f32 v12, v59, v78, v12 op_sel_hi:[0,1,0]
	v_fma_mix_f32 v13, v59, v78, v13 op_sel:[0,1,0] op_sel_hi:[0,1,0]
	v_fma_mix_f32 v14, v59, v79, v14 op_sel_hi:[0,1,0]
	v_fma_mix_f32 v15, v59, v79, v15 op_sel:[0,1,0] op_sel_hi:[0,1,0]
	s_waitcnt vmcnt(5)
	v_fma_mix_f32 v8, v61, v80, v8 op_sel_hi:[0,1,0]
	v_fma_mix_f32 v9, v61, v80, v9 op_sel:[0,1,0] op_sel_hi:[0,1,0]
	v_fma_mix_f32 v10, v61, v81, v10 op_sel_hi:[0,1,0]
	v_fma_mix_f32 v11, v61, v81, v11 op_sel:[0,1,0] op_sel_hi:[0,1,0]
	v_fma_mix_f32 v12, v61, v82, v12 op_sel_hi:[0,1,0]
	v_fma_mix_f32 v13, v61, v82, v13 op_sel:[0,1,0] op_sel_hi:[0,1,0]
	v_fma_mix_f32 v14, v61, v83, v14 op_sel_hi:[0,1,0]
	v_fma_mix_f32 v15, v61, v83, v15 op_sel:[0,1,0] op_sel_hi:[0,1,0]
	s_waitcnt vmcnt(4)
	v_fma_mix_f32 v8, v63, v84, v8 op_sel_hi:[0,1,0]
	v_fma_mix_f32 v9, v63, v84, v9 op_sel:[0,1,0] op_sel_hi:[0,1,0]
	v_fma_mix_f32 v10, v63, v85, v10 op_sel_hi:[0,1,0]
	v_fma_mix_f32 v11, v63, v85, v11 op_sel:[0,1,0] op_sel_hi:[0,1,0]
	v_fma_mix_f32 v12, v63, v86, v12 op_sel_hi:[0,1,0]
	v_fma_mix_f32 v13, v63, v86, v13 op_sel:[0,1,0] op_sel_hi:[0,1,0]
	v_fma_mix_f32 v14, v63, v87, v14 op_sel_hi:[0,1,0]
	v_fma_mix_f32 v15, v63, v87, v15 op_sel:[0,1,0] op_sel_hi:[0,1,0]
	s_waitcnt vmcnt(3)
	v_fma_mix_f32 v8, v65, v88, v8 op_sel_hi:[0,1,0]
	v_fma_mix_f32 v9, v65, v88, v9 op_sel:[0,1,0] op_sel_hi:[0,1,0]
	v_fma_mix_f32 v10, v65, v89, v10 op_sel_hi:[0,1,0]
	v_fma_mix_f32 v11, v65, v89, v11 op_sel:[0,1,0] op_sel_hi:[0,1,0]
	v_fma_mix_f32 v12, v65, v90, v12 op_sel_hi:[0,1,0]
	v_fma_mix_f32 v13, v65, v90, v13 op_sel:[0,1,0] op_sel_hi:[0,1,0]
	v_fma_mix_f32 v14, v65, v91, v14 op_sel_hi:[0,1,0]
	v_fma_mix_f32 v15, v65, v91, v15 op_sel:[0,1,0] op_sel_hi:[0,1,0]
	s_waitcnt vmcnt(2)
	v_fma_mix_f32 v8, v67, v92, v8 op_sel_hi:[0,1,0]
	v_fma_mix_f32 v9, v67, v92, v9 op_sel:[0,1,0] op_sel_hi:[0,1,0]
	v_fma_mix_f32 v10, v67, v93, v10 op_sel_hi:[0,1,0]
	v_fma_mix_f32 v11, v67, v93, v11 op_sel:[0,1,0] op_sel_hi:[0,1,0]
	v_fma_mix_f32 v12, v67, v94, v12 op_sel_hi:[0,1,0]
	v_fma_mix_f32 v13, v67, v94, v13 op_sel:[0,1,0] op_sel_hi:[0,1,0]
	v_fma_mix_f32 v14, v67, v95, v14 op_sel_hi:[0,1,0]
	v_fma_mix_f32 v15, v67, v95, v15 op_sel:[0,1,0] op_sel_hi:[0,1,0]
	s_waitcnt vmcnt(1)
	v_fma_mix_f32 v8, v69, v96, v8 op_sel_hi:[0,1,0]
	v_fma_mix_f32 v9, v69, v96, v9 op_sel:[0,1,0] op_sel_hi:[0,1,0]
	v_fma_mix_f32 v10, v69, v97, v10 op_sel_hi:[0,1,0]
	v_fma_mix_f32 v11, v69, v97, v11 op_sel:[0,1,0] op_sel_hi:[0,1,0]
	v_fma_mix_f32 v12, v69, v98, v12 op_sel_hi:[0,1,0]
	v_fma_mix_f32 v13, v69, v98, v13 op_sel:[0,1,0] op_sel_hi:[0,1,0]
	v_fma_mix_f32 v14, v69, v99, v14 op_sel_hi:[0,1,0]
	v_fma_mix_f32 v15, v69, v99, v15 op_sel:[0,1,0] op_sel_hi:[0,1,0]
	s_waitcnt vmcnt(0)
	v_fma_mix_f32 v8, v71, v100, v8 op_sel_hi:[0,1,0]
	v_fma_mix_f32 v9, v71, v100, v9 op_sel:[0,1,0] op_sel_hi:[0,1,0]
	v_fma_mix_f32 v10, v71, v101, v10 op_sel_hi:[0,1,0]
	v_fma_mix_f32 v11, v71, v101, v11 op_sel:[0,1,0] op_sel_hi:[0,1,0]
	v_fma_mix_f32 v12, v71, v102, v12 op_sel_hi:[0,1,0]
	v_fma_mix_f32 v13, v71, v102, v13 op_sel:[0,1,0] op_sel_hi:[0,1,0]
	v_fma_mix_f32 v14, v71, v103, v14 op_sel_hi:[0,1,0]
	v_fma_mix_f32 v15, v71, v103, v15 op_sel:[0,1,0] op_sel_hi:[0,1,0]
.Lsw_wg0:
	s_cmp_eq_u32 s58, 16
	s_cbranch_scc1 .Lsw_wk0
.Lsw_wskip0:
.Lsw_wk1:
	s_waitcnt vmcnt(0)
	v_lshrrev_b32_e32 v57, 13, v50
	v_cmp_eq_u32_e32 vcc, s55, v57
	v_cmp_lt_u32_e64 s[52:53], v1, v45
	s_and_b64 s[50:51], vcc, s[52:53]
	s_cmp_lg_u64 s[50:51], 0
	s_cbranch_scc0 .Lsw_wskip1
	v_lshrrev_b64 v[58:59], v6, s[50:51]
	v_lshrrev_b32_e32 v56, 5, v50
	v_not_b32_e32 v58, v58
	v_lshlrev_b32_e32 v56, 2, v56
	v_or_b32_e32 v58, 0x10000, v58
	ds_read_b32 v57, v56
	v_ffbl_b32_e32 v60, v58
	s_nop 0
	v_cmp_lt_u32_e32 vcc, v1, v60
	s_waitcnt lgkmcnt(0)
	v_mul_f32_e32 v59, v51, v57
	v_cndmask_b32_e32 v58, 0, v50, vcc
	v_cndmask_b32_e32 v59, 0, v59, vcc
	ds_write_b64 v4, v[58:59]
	v_add_u32_e32 v41, v41, v60
	v_sub_u32_e32 v45, v45, v60
	v_cmp_lt_u32_e32 vcc, v1, v45
	v_add_u32_e32 v56, v41, v1
	v_lshlrev_b32_e32 v56, 3, v56
	v_mov_b32_e32 v50, 0
	v_mov_b32_e32 v51, 0
	s_and_saveexec_b64 s[36:37], vcc
	global_load_dwordx2 v[50:51], v56, s[6:7]
	s_mov_b64 exec, s[36:37]
	v_readlane_b32 s40, v60, 0
	v_readlane_b32 s41, v60, 16
	v_readlane_b32 s42, v60, 32
	v_readlane_b32 s43, v60, 48
	s_nop 0
	s_max_u32 s40, s40, s41
	s_max_u32 s42, s42, s43
	s_max_u32 s40, s40, s42
	s_mov_b32 s58, s40

.Lsw_go1:
	s_add_u32 s60, s60, 1
	s_cmp_gt_u32 s40, 8
	s_addc_u32 s60, s60, 0
	ds_read_b128 v[56:59], v5 offset:0
	ds_read_b128 v[60:63], v5 offset:16
	ds_read_b128 v[64:67], v5 offset:32
	ds_read_b128 v[68:71], v5 offset:48
	s_waitcnt lgkmcnt(0)
	v_lshl_or_b32 v104, v56, 8, v2
	global_load_dwordx4 v[72:75], v104, s[8:9]
	v_lshl_or_b32 v104, v58, 8, v2
	global_load_dwordx4 v[76:79], v104, s[8:9]
	v_lshl_or_b32 v104, v60, 8, v2
	global_load_dwordx4 v[80:83], v104, s[8:9]
	v_lshl_or_b32 v104, v62, 8, v2
	global_load_dwordx4 v[84:87], v104, s[8:9]
	v_lshl_or_b32 v104, v64, 8, v2
	global_load_dwordx4 v[88:91], v104, s[8:9]
	v_lshl_or_b32 v104, v66, 8, v2
	global_load_dwordx4 v[92:95], v104, s[8:9]
	v_lshl_or_b32 v104, v68, 8, v2
	global_load_dwordx4 v[96:99], v104, s[8:9]
	v_lshl_or_b32 v104, v70, 8, v2
	global_load_dwordx4 v[100:103], v104, s[8:9]
	s_waitcnt vmcnt(7)
	v_fma_mix_f32 v16, v57, v72, v16 op_sel_hi:[0,1,0]
	v_fma_mix_f32 v17, v57, v72, v17 op_sel:[0,1,0] op_sel_hi:[0,1,0]
	v_fma_mix_f32 v18, v57, v73, v18 op_sel_hi:[0,1,0]
	v_fma_mix_f32 v19, v57, v73, v19 op_sel:[0,1,0] op_sel_hi:[0,1,0]
	v_fma_mix_f32 v20, v57, v74, v20 op_sel_hi:[0,1,0]
	v_fma_mix_f32 v21, v57, v74, v21 op_sel:[0,1,0] op_sel_hi:[0,1,0]
	v_fma_mix_f32 v22, v57, v75, v22 op_sel_hi:[0,1,0]
	v_fma_mix_f32 v23, v57, v75, v23 op_sel:[0,1,0] op_sel_hi:[0,1,0]
	s_waitcnt vmcnt(6)
	v_fma_mix_f32 v16, v59, v76, v16 op_sel_hi:[0,1,0]
	v_fma_mix_f32 v17, v59, v76, v17 op_sel:[0,1,0] op_sel_hi:[0,1,0]
	v_fma_mix_f32 v18, v59, v77, v18 op_sel_hi:[0,1,0]
	v_fma_mix_f32 v19, v59, v77, v19 op_sel:[0,1,0] op_sel_hi:[0,1,0]
	v_fma_mix_f32 v20, v59, v78, v20 op_sel_hi:[0,1,0]
	v_fma_mix_f32 v21, v59, v78, v21 op_sel:[0,1,0] op_sel_hi:[0,1,0]
	v_fma_mix_f32 v22, v59, v79, v22 op_sel_hi:[0,1,0]
	v_fma_mix_f32 v23, v59, v79, v23 op_sel:[0,1,0] op_sel_hi:[0,1,0]
	s_waitcnt vmcnt(5)
	v_fma_mix_f32 v16, v61, v80, v16 op_sel_hi:[0,1,0]
	v_fma_mix_f32 v17, v61, v80, v17 op_sel:[0,1,0] op_sel_hi:[0,1,0]
	v_fma_mix_f32 v18, v61, v81, v18 op_sel_hi:[0,1,0]
	v_fma_mix_f32 v19, v61, v81, v19 op_sel:[0,1,0] op_sel_hi:[0,1,0]
	v_fma_mix_f32 v20, v61, v82, v20 op_sel_hi:[0,1,0]
	v_fma_mix_f32 v21, v61, v82, v21 op_sel:[0,1,0] op_sel_hi:[0,1,0]
	v_fma_mix_f32 v22, v61, v83, v22 op_sel_hi:[0,1,0]
	v_fma_mix_f32 v23, v61, v83, v23 op_sel:[0,1,0] op_sel_hi:[0,1,0]
	s_waitcnt vmcnt(4)
	v_fma_mix_f32 v16, v63, v84, v16 op_sel_hi:[0,1,0]
	v_fma_mix_f32 v17, v63, v84, v17 op_sel:[0,1,0] op_sel_hi:[0,1,0]
	v_fma_mix_f32 v18, v63, v85, v18 op_sel_hi:[0,1,0]
	v_fma_mix_f32 v19, v63, v85, v19 op_sel:[0,1,0] op_sel_hi:[0,1,0]
	v_fma_mix_f32 v20, v63, v86, v20 op_sel_hi:[0,1,0]
	v_fma_mix_f32 v21, v63, v86, v21 op_sel:[0,1,0] op_sel_hi:[0,1,0]
	v_fma_mix_f32 v22, v63, v87, v22 op_sel_hi:[0,1,0]
	v_fma_mix_f32 v23, v63, v87, v23 op_sel:[0,1,0] op_sel_hi:[0,1,0]
	s_waitcnt vmcnt(3)
	v_fma_mix_f32 v16, v65, v88, v16 op_sel_hi:[0,1,0]
	v_fma_mix_f32 v17, v65, v88, v17 op_sel:[0,1,0] op_sel_hi:[0,1,0]
	v_fma_mix_f32 v18, v65, v89, v18 op_sel_hi:[0,1,0]
	v_fma_mix_f32 v19, v65, v89, v19 op_sel:[0,1,0] op_sel_hi:[0,1,0]
	v_fma_mix_f32 v20, v65, v90, v20 op_sel_hi:[0,1,0]
	v_fma_mix_f32 v21, v65, v90, v21 op_sel:[0,1,0] op_sel_hi:[0,1,0]
	v_fma_mix_f32 v22, v65, v91, v22 op_sel_hi:[0,1,0]
	v_fma_mix_f32 v23, v65, v91, v23 op_sel:[0,1,0] op_sel_hi:[0,1,0]
	s_waitcnt vmcnt(2)
	v_fma_mix_f32 v16, v67, v92, v16 op_sel_hi:[0,1,0]
	v_fma_mix_f32 v17, v67, v92, v17 op_sel:[0,1,0] op_sel_hi:[0,1,0]
	v_fma_mix_f32 v18, v67, v93, v18 op_sel_hi:[0,1,0]
	v_fma_mix_f32 v19, v67, v93, v19 op_sel:[0,1,0] op_sel_hi:[0,1,0]
	v_fma_mix_f32 v20, v67, v94, v20 op_sel_hi:[0,1,0]
	v_fma_mix_f32 v21, v67, v94, v21 op_sel:[0,1,0] op_sel_hi:[0,1,0]
	v_fma_mix_f32 v22, v67, v95, v22 op_sel_hi:[0,1,0]
	v_fma_mix_f32 v23, v67, v95, v23 op_sel:[0,1,0] op_sel_hi:[0,1,0]
	s_waitcnt vmcnt(1)
	v_fma_mix_f32 v16, v69, v96, v16 op_sel_hi:[0,1,0]
	v_fma_mix_f32 v17, v69, v96, v17 op_sel:[0,1,0] op_sel_hi:[0,1,0]
	v_fma_mix_f32 v18, v69, v97, v18 op_sel_hi:[0,1,0]
	v_fma_mix_f32 v19, v69, v97, v19 op_sel:[0,1,0] op_sel_hi:[0,1,0]
	v_fma_mix_f32 v20, v69, v98, v20 op_sel_hi:[0,1,0]
	v_fma_mix_f32 v21, v69, v98, v21 op_sel:[0,1,0] op_sel_hi:[0,1,0]
	v_fma_mix_f32 v22, v69, v99, v22 op_sel_hi:[0,1,0]
	v_fma_mix_f32 v23, v69, v99, v23 op_sel:[0,1,0] op_sel_hi:[0,1,0]
	s_waitcnt vmcnt(0)
	v_fma_mix_f32 v16, v71, v100, v16 op_sel_hi:[0,1,0]
	v_fma_mix_f32 v17, v71, v100, v17 op_sel:[0,1,0] op_sel_hi:[0,1,0]
	v_fma_mix_f32 v18, v71, v101, v18 op_sel_hi:[0,1,0]
	v_fma_mix_f32 v19, v71, v101, v19 op_sel:[0,1,0] op_sel_hi:[0,1,0]
	v_fma_mix_f32 v20, v71, v102, v20 op_sel_hi:[0,1,0]
	v_fma_mix_f32 v21, v71, v102, v21 op_sel:[0,1,0] op_sel_hi:[0,1,0]
	v_fma_mix_f32 v22, v71, v103, v22 op_sel_hi:[0,1,0]
	v_fma_mix_f32 v23, v71, v103, v23 op_sel:[0,1,0] op_sel_hi:[0,1,0]
	s_cmp_le_u32 s40, 8
	s_cbranch_scc1 .Lsw_wg1
	ds_read_b128 v[56:59], v5 offset:64
	ds_read_b128 v[60:63], v5 offset:80
	ds_read_b128 v[64:67], v5 offset:96
	ds_read_b128 v[68:71], v5 offset:112
	s_waitcnt lgkmcnt(0)
	v_lshl_or_b32 v104, v56, 8, v2
	global_load_dwordx4 v[72:75], v104, s[8:9]
	v_lshl_or_b32 v104, v58, 8, v2
	global_load_dwordx4 v[76:79], v104, s[8:9]
	v_lshl_or_b32 v104, v60, 8, v2
	global_load_dwordx4 v[80:83], v104, s[8:9]
	v_lshl_or_b32 v104, v62, 8, v2
	global_load_dwordx4 v[84:87], v104, s[8:9]
	v_lshl_or_b32 v104, v64, 8, v2
	global_load_dwordx4 v[88:91], v104, s[8:9]
	v_lshl_or_b32 v104, v66, 8, v2
	global_load_dwordx4 v[92:95], v104, s[8:9]
	v_lshl_or_b32 v104, v68, 8, v2
	global_load_dwordx4 v[96:99], v104, s[8:9]
	v_lshl_or_b32 v104, v70, 8, v2
	global_load_dwordx4 v[100:103], v104, s[8:9]
	s_waitcnt vmcnt(7)
	v_fma_mix_f32 v16, v57, v72, v16 op_sel_hi:[0,1,0]
	v_fma_mix_f32 v17, v57, v72, v17 op_sel:[0,1,0] op_sel_hi:[0,1,0]
	v_fma_mix_f32 v18, v57, v73, v18 op_sel_hi:[0,1,0]
	v_fma_mix_f32 v19, v57, v73, v19 op_sel:[0,1,0] op_sel_hi:[0,1,0]
	v_fma_mix_f32 v20, v57, v74, v20 op_sel_hi:[0,1,0]
	v_fma_mix_f32 v21, v57, v74, v21 op_sel:[0,1,0] op_sel_hi:[0,1,0]
	v_fma_mix_f32 v22, v57, v75, v22 op_sel_hi:[0,1,0]
	v_fma_mix_f32 v23, v57, v75, v23 op_sel:[0,1,0] op_sel_hi:[0,1,0]
	s_waitcnt vmcnt(6)
	v_fma_mix_f32 v16, v59, v76, v16 op_sel_hi:[0,1,0]
	v_fma_mix_f32 v17, v59, v76, v17 op_sel:[0,1,0] op_sel_hi:[0,1,0]
	v_fma_mix_f32 v18, v59, v77, v18 op_sel_hi:[0,1,0]
	v_fma_mix_f32 v19, v59, v77, v19 op_sel:[0,1,0] op_sel_hi:[0,1,0]
	v_fma_mix_f32 v20, v59, v78, v20 op_sel_hi:[0,1,0]
	v_fma_mix_f32 v21, v59, v78, v21 op_sel:[0,1,0] op_sel_hi:[0,1,0]
	v_fma_mix_f32 v22, v59, v79, v22 op_sel_hi:[0,1,0]
	v_fma_mix_f32 v23, v59, v79, v23 op_sel:[0,1,0] op_sel_hi:[0,1,0]
	s_waitcnt vmcnt(5)
	v_fma_mix_f32 v16, v61, v80, v16 op_sel_hi:[0,1,0]
	v_fma_mix_f32 v17, v61, v80, v17 op_sel:[0,1,0] op_sel_hi:[0,1,0]
	v_fma_mix_f32 v18, v61, v81, v18 op_sel_hi:[0,1,0]
	v_fma_mix_f32 v19, v61, v81, v19 op_sel:[0,1,0] op_sel_hi:[0,1,0]
	v_fma_mix_f32 v20, v61, v82, v20 op_sel_hi:[0,1,0]
	v_fma_mix_f32 v21, v61, v82, v21 op_sel:[0,1,0] op_sel_hi:[0,1,0]
	v_fma_mix_f32 v22, v61, v83, v22 op_sel_hi:[0,1,0]
	v_fma_mix_f32 v23, v61, v83, v23 op_sel:[0,1,0] op_sel_hi:[0,1,0]
	s_waitcnt vmcnt(4)
	v_fma_mix_f32 v16, v63, v84, v16 op_sel_hi:[0,1,0]
	v_fma_mix_f32 v17, v63, v84, v17 op_sel:[0,1,0] op_sel_hi:[0,1,0]
	v_fma_mix_f32 v18, v63, v85, v18 op_sel_hi:[0,1,0]
	v_fma_mix_f32 v19, v63, v85, v19 op_sel:[0,1,0] op_sel_hi:[0,1,0]
	v_fma_mix_f32 v20, v63, v86, v20 op_sel_hi:[0,1,0]
	v_fma_mix_f32 v21, v63, v86, v21 op_sel:[0,1,0] op_sel_hi:[0,1,0]
	v_fma_mix_f32 v22, v63, v87, v22 op_sel_hi:[0,1,0]
	v_fma_mix_f32 v23, v63, v87, v23 op_sel:[0,1,0] op_sel_hi:[0,1,0]
	s_waitcnt vmcnt(3)
	v_fma_mix_f32 v16, v65, v88, v16 op_sel_hi:[0,1,0]
	v_fma_mix_f32 v17, v65, v88, v17 op_sel:[0,1,0] op_sel_hi:[0,1,0]
	v_fma_mix_f32 v18, v65, v89, v18 op_sel_hi:[0,1,0]
	v_fma_mix_f32 v19, v65, v89, v19 op_sel:[0,1,0] op_sel_hi:[0,1,0]
	v_fma_mix_f32 v20, v65, v90, v20 op_sel_hi:[0,1,0]
	v_fma_mix_f32 v21, v65, v90, v21 op_sel:[0,1,0] op_sel_hi:[0,1,0]
	v_fma_mix_f32 v22, v65, v91, v22 op_sel_hi:[0,1,0]
	v_fma_mix_f32 v23, v65, v91, v23 op_sel:[0,1,0] op_sel_hi:[0,1,0]
	s_waitcnt vmcnt(2)
	v_fma_mix_f32 v16, v67, v92, v16 op_sel_hi:[0,1,0]
	v_fma_mix_f32 v17, v67, v92, v17 op_sel:[0,1,0] op_sel_hi:[0,1,0]
	v_fma_mix_f32 v18, v67, v93, v18 op_sel_hi:[0,1,0]
	v_fma_mix_f32 v19, v67, v93, v19 op_sel:[0,1,0] op_sel_hi:[0,1,0]
	v_fma_mix_f32 v20, v67, v94, v20 op_sel_hi:[0,1,0]
	v_fma_mix_f32 v21, v67, v94, v21 op_sel:[0,1,0] op_sel_hi:[0,1,0]
	v_fma_mix_f32 v22, v67, v95, v22 op_sel_hi:[0,1,0]
	v_fma_mix_f32 v23, v67, v95, v23 op_sel:[0,1,0] op_sel_hi:[0,1,0]
	s_waitcnt vmcnt(1)
	v_fma_mix_f32 v16, v69, v96, v16 op_sel_hi:[0,1,0]
	v_fma_mix_f32 v17, v69, v96, v17 op_sel:[0,1,0] op_sel_hi:[0,1,0]
	v_fma_mix_f32 v18, v69, v97, v18 op_sel_hi:[0,1,0]
	v_fma_mix_f32 v19, v69, v97, v19 op_sel:[0,1,0] op_sel_hi:[0,1,0]
	v_fma_mix_f32 v20, v69, v98, v20 op_sel_hi:[0,1,0]
	v_fma_mix_f32 v21, v69, v98, v21 op_sel:[0,1,0] op_sel_hi:[0,1,0]
	v_fma_mix_f32 v22, v69, v99, v22 op_sel_hi:[0,1,0]
	v_fma_mix_f32 v23, v69, v99, v23 op_sel:[0,1,0] op_sel_hi:[0,1,0]
	s_waitcnt vmcnt(0)
	v_fma_mix_f32 v16, v71, v100, v16 op_sel_hi:[0,1,0]
	v_fma_mix_f32 v17, v71, v100, v17 op_sel:[0,1,0] op_sel_hi:[0,1,0]
	v_fma_mix_f32 v18, v71, v101, v18 op_sel_hi:[0,1,0]
	v_fma_mix_f32 v19, v71, v101, v19 op_sel:[0,1,0] op_sel_hi:[0,1,0]
	v_fma_mix_f32 v20, v71, v102, v20 op_sel_hi:[0,1,0]
	v_fma_mix_f32 v21, v71, v102, v21 op_sel:[0,1,0] op_sel_hi:[0,1,0]
	v_fma_mix_f32 v22, v71, v103, v22 op_sel_hi:[0,1,0]
	v_fma_mix_f32 v23, v71, v103, v23 op_sel:[0,1,0] op_sel_hi:[0,1,0]

.Lsw_wskip1:
.Lsw_wk2:
	s_waitcnt vmcnt(0)
	v_lshrrev_b32_e32 v57, 13, v52
	v_cmp_eq_u32_e32 vcc, s55, v57
	v_cmp_lt_u32_e64 s[52:53], v1, v46
	s_and_b64 s[50:51], vcc, s[52:53]
	s_cmp_lg_u64 s[50:51], 0
	s_cbranch_scc0 .Lsw_wskip2
	v_lshrrev_b64 v[58:59], v6, s[50:51]
	v_lshrrev_b32_e32 v56, 5, v52
	v_not_b32_e32 v58, v58
	v_lshlrev_b32_e32 v56, 2, v56
	v_or_b32_e32 v58, 0x10000, v58
	ds_read_b32 v57, v56
	v_ffbl_b32_e32 v60, v58
	s_nop 0
	v_cmp_lt_u32_e32 vcc, v1, v60
	s_waitcnt lgkmcnt(0)
	v_mul_f32_e32 v59, v53, v57
	v_cndmask_b32_e32 v58, 0, v52, vcc
	v_cndmask_b32_e32 v59, 0, v59, vcc
	ds_write_b64 v4, v[58:59]
	v_add_u32_e32 v42, v42, v60
	v_sub_u32_e32 v46, v46, v60
	v_cmp_lt_u32_e32 vcc, v1, v46
	v_add_u32_e32 v56, v42, v1
	v_lshlrev_b32_e32 v56, 3, v56
	v_mov_b32_e32 v52, 0
	v_mov_b32_e32 v53, 0
	s_and_saveexec_b64 s[36:37], vcc
	global_load_dwordx2 v[52:53], v56, s[6:7]
	s_mov_b64 exec, s[36:37]
	v_readlane_b32 s40, v60, 0
	v_readlane_b32 s41, v60, 16
	v_readlane_b32 s42, v60, 32
	v_readlane_b32 s43, v60, 48
	s_nop 0
	s_max_u32 s40, s40, s41
	s_max_u32 s42, s42, s43
	s_max_u32 s40, s40, s42
	s_mov_b32 s58, s40

.Lsw_go2:
	s_add_u32 s60, s60, 1
	s_cmp_gt_u32 s40, 8
	s_addc_u32 s60, s60, 0
	ds_read_b128 v[56:59], v5 offset:0
	ds_read_b128 v[60:63], v5 offset:16
	ds_read_b128 v[64:67], v5 offset:32
	ds_read_b128 v[68:71], v5 offset:48
	s_waitcnt lgkmcnt(0)
	v_lshl_or_b32 v104, v56, 8, v2
	global_load_dwordx4 v[72:75], v104, s[8:9]
	v_lshl_or_b32 v104, v58, 8, v2
	global_load_dwordx4 v[76:79], v104, s[8:9]
	v_lshl_or_b32 v104, v60, 8, v2
	global_load_dwordx4 v[80:83], v104, s[8:9]
	v_lshl_or_b32 v104, v62, 8, v2
	global_load_dwordx4 v[84:87], v104, s[8:9]
	v_lshl_or_b32 v104, v64, 8, v2
	global_load_dwordx4 v[88:91], v104, s[8:9]
	v_lshl_or_b32 v104, v66, 8, v2
	global_load_dwordx4 v[92:95], v104, s[8:9]
	v_lshl_or_b32 v104, v68, 8, v2
	global_load_dwordx4 v[96:99], v104, s[8:9]
	v_lshl_or_b32 v104, v70, 8, v2
	global_load_dwordx4 v[100:103], v104, s[8:9]
	s_waitcnt vmcnt(7)
	v_fma_mix_f32 v24, v57, v72, v24 op_sel_hi:[0,1,0]
	v_fma_mix_f32 v25, v57, v72, v25 op_sel:[0,1,0] op_sel_hi:[0,1,0]
	v_fma_mix_f32 v26, v57, v73, v26 op_sel_hi:[0,1,0]
	v_fma_mix_f32 v27, v57, v73, v27 op_sel:[0,1,0] op_sel_hi:[0,1,0]
	v_fma_mix_f32 v28, v57, v74, v28 op_sel_hi:[0,1,0]
	v_fma_mix_f32 v29, v57, v74, v29 op_sel:[0,1,0] op_sel_hi:[0,1,0]
	v_fma_mix_f32 v30, v57, v75, v30 op_sel_hi:[0,1,0]
	v_fma_mix_f32 v31, v57, v75, v31 op_sel:[0,1,0] op_sel_hi:[0,1,0]
	s_waitcnt vmcnt(6)
	v_fma_mix_f32 v24, v59, v76, v24 op_sel_hi:[0,1,0]
	v_fma_mix_f32 v25, v59, v76, v25 op_sel:[0,1,0] op_sel_hi:[0,1,0]
	v_fma_mix_f32 v26, v59, v77, v26 op_sel_hi:[0,1,0]
	v_fma_mix_f32 v27, v59, v77, v27 op_sel:[0,1,0] op_sel_hi:[0,1,0]
	v_fma_mix_f32 v28, v59, v78, v28 op_sel_hi:[0,1,0]
	v_fma_mix_f32 v29, v59, v78, v29 op_sel:[0,1,0] op_sel_hi:[0,1,0]
	v_fma_mix_f32 v30, v59, v79, v30 op_sel_hi:[0,1,0]
	v_fma_mix_f32 v31, v59, v79, v31 op_sel:[0,1,0] op_sel_hi:[0,1,0]
	s_waitcnt vmcnt(5)
	v_fma_mix_f32 v24, v61, v80, v24 op_sel_hi:[0,1,0]
	v_fma_mix_f32 v25, v61, v80, v25 op_sel:[0,1,0] op_sel_hi:[0,1,0]
	v_fma_mix_f32 v26, v61, v81, v26 op_sel_hi:[0,1,0]
	v_fma_mix_f32 v27, v61, v81, v27 op_sel:[0,1,0] op_sel_hi:[0,1,0]
	v_fma_mix_f32 v28, v61, v82, v28 op_sel_hi:[0,1,0]
	v_fma_mix_f32 v29, v61, v82, v29 op_sel:[0,1,0] op_sel_hi:[0,1,0]
	v_fma_mix_f32 v30, v61, v83, v30 op_sel_hi:[0,1,0]
	v_fma_mix_f32 v31, v61, v83, v31 op_sel:[0,1,0] op_sel_hi:[0,1,0]
	s_waitcnt vmcnt(4)
	v_fma_mix_f32 v24, v63, v84, v24 op_sel_hi:[0,1,0]
	v_fma_mix_f32 v25, v63, v84, v25 op_sel:[0,1,0] op_sel_hi:[0,1,0]
	v_fma_mix_f32 v26, v63, v85, v26 op_sel_hi:[0,1,0]
	v_fma_mix_f32 v27, v63, v85, v27 op_sel:[0,1,0] op_sel_hi:[0,1,0]
	v_fma_mix_f32 v28, v63, v86, v28 op_sel_hi:[0,1,0]
	v_fma_mix_f32 v29, v63, v86, v29 op_sel:[0,1,0] op_sel_hi:[0,1,0]
	v_fma_mix_f32 v30, v63, v87, v30 op_sel_hi:[0,1,0]
	v_fma_mix_f32 v31, v63, v87, v31 op_sel:[0,1,0] op_sel_hi:[0,1,0]
	s_waitcnt vmcnt(3)
	v_fma_mix_f32 v24, v65, v88, v24 op_sel_hi:[0,1,0]
	v_fma_mix_f32 v25, v65, v88, v25 op_sel:[0,1,0] op_sel_hi:[0,1,0]
	v_fma_mix_f32 v26, v65, v89, v26 op_sel_hi:[0,1,0]
	v_fma_mix_f32 v27, v65, v89, v27 op_sel:[0,1,0] op_sel_hi:[0,1,0]
	v_fma_mix_f32 v28, v65, v90, v28 op_sel_hi:[0,1,0]
	v_fma_mix_f32 v29, v65, v90, v29 op_sel:[0,1,0] op_sel_hi:[0,1,0]
	v_fma_mix_f32 v30, v65, v91, v30 op_sel_hi:[0,1,0]
	v_fma_mix_f32 v31, v65, v91, v31 op_sel:[0,1,0] op_sel_hi:[0,1,0]
	s_waitcnt vmcnt(2)
	v_fma_mix_f32 v24, v67, v92, v24 op_sel_hi:[0,1,0]
	v_fma_mix_f32 v25, v67, v92, v25 op_sel:[0,1,0] op_sel_hi:[0,1,0]
	v_fma_mix_f32 v26, v67, v93, v26 op_sel_hi:[0,1,0]
	v_fma_mix_f32 v27, v67, v93, v27 op_sel:[0,1,0] op_sel_hi:[0,1,0]
	v_fma_mix_f32 v28, v67, v94, v28 op_sel_hi:[0,1,0]
	v_fma_mix_f32 v29, v67, v94, v29 op_sel:[0,1,0] op_sel_hi:[0,1,0]
	v_fma_mix_f32 v30, v67, v95, v30 op_sel_hi:[0,1,0]
	v_fma_mix_f32 v31, v67, v95, v31 op_sel:[0,1,0] op_sel_hi:[0,1,0]
	s_waitcnt vmcnt(1)
	v_fma_mix_f32 v24, v69, v96, v24 op_sel_hi:[0,1,0]
	v_fma_mix_f32 v25, v69, v96, v25 op_sel:[0,1,0] op_sel_hi:[0,1,0]
	v_fma_mix_f32 v26, v69, v97, v26 op_sel_hi:[0,1,0]
	v_fma_mix_f32 v27, v69, v97, v27 op_sel:[0,1,0] op_sel_hi:[0,1,0]
	v_fma_mix_f32 v28, v69, v98, v28 op_sel_hi:[0,1,0]
	v_fma_mix_f32 v29, v69, v98, v29 op_sel:[0,1,0] op_sel_hi:[0,1,0]
	v_fma_mix_f32 v30, v69, v99, v30 op_sel_hi:[0,1,0]
	v_fma_mix_f32 v31, v69, v99, v31 op_sel:[0,1,0] op_sel_hi:[0,1,0]
	s_waitcnt vmcnt(0)
	v_fma_mix_f32 v24, v71, v100, v24 op_sel_hi:[0,1,0]
	v_fma_mix_f32 v25, v71, v100, v25 op_sel:[0,1,0] op_sel_hi:[0,1,0]
	v_fma_mix_f32 v26, v71, v101, v26 op_sel_hi:[0,1,0]
	v_fma_mix_f32 v27, v71, v101, v27 op_sel:[0,1,0] op_sel_hi:[0,1,0]
	v_fma_mix_f32 v28, v71, v102, v28 op_sel_hi:[0,1,0]
	v_fma_mix_f32 v29, v71, v102, v29 op_sel:[0,1,0] op_sel_hi:[0,1,0]
	v_fma_mix_f32 v30, v71, v103, v30 op_sel_hi:[0,1,0]
	v_fma_mix_f32 v31, v71, v103, v31 op_sel:[0,1,0] op_sel_hi:[0,1,0]
	s_cmp_le_u32 s40, 8
	s_cbranch_scc1 .Lsw_wg2
	ds_read_b128 v[56:59], v5 offset:64
	ds_read_b128 v[60:63], v5 offset:80
	ds_read_b128 v[64:67], v5 offset:96
	ds_read_b128 v[68:71], v5 offset:112
	s_waitcnt lgkmcnt(0)
	v_lshl_or_b32 v104, v56, 8, v2
	global_load_dwordx4 v[72:75], v104, s[8:9]
	v_lshl_or_b32 v104, v58, 8, v2
	global_load_dwordx4 v[76:79], v104, s[8:9]
	v_lshl_or_b32 v104, v60, 8, v2
	global_load_dwordx4 v[80:83], v104, s[8:9]
	v_lshl_or_b32 v104, v62, 8, v2
	global_load_dwordx4 v[84:87], v104, s[8:9]
	v_lshl_or_b32 v104, v64, 8, v2
	global_load_dwordx4 v[88:91], v104, s[8:9]
	v_lshl_or_b32 v104, v66, 8, v2
	global_load_dwordx4 v[92:95], v104, s[8:9]
	v_lshl_or_b32 v104, v68, 8, v2
	global_load_dwordx4 v[96:99], v104, s[8:9]
	v_lshl_or_b32 v104, v70, 8, v2
	global_load_dwordx4 v[100:103], v104, s[8:9]
	s_waitcnt vmcnt(7)
	v_fma_mix_f32 v24, v57, v72, v24 op_sel_hi:[0,1,0]
	v_fma_mix_f32 v25, v57, v72, v25 op_sel:[0,1,0] op_sel_hi:[0,1,0]
	v_fma_mix_f32 v26, v57, v73, v26 op_sel_hi:[0,1,0]
	v_fma_mix_f32 v27, v57, v73, v27 op_sel:[0,1,0] op_sel_hi:[0,1,0]
	v_fma_mix_f32 v28, v57, v74, v28 op_sel_hi:[0,1,0]
	v_fma_mix_f32 v29, v57, v74, v29 op_sel:[0,1,0] op_sel_hi:[0,1,0]
	v_fma_mix_f32 v30, v57, v75, v30 op_sel_hi:[0,1,0]
	v_fma_mix_f32 v31, v57, v75, v31 op_sel:[0,1,0] op_sel_hi:[0,1,0]
	s_waitcnt vmcnt(6)
	v_fma_mix_f32 v24, v59, v76, v24 op_sel_hi:[0,1,0]
	v_fma_mix_f32 v25, v59, v76, v25 op_sel:[0,1,0] op_sel_hi:[0,1,0]
	v_fma_mix_f32 v26, v59, v77, v26 op_sel_hi:[0,1,0]
	v_fma_mix_f32 v27, v59, v77, v27 op_sel:[0,1,0] op_sel_hi:[0,1,0]
	v_fma_mix_f32 v28, v59, v78, v28 op_sel_hi:[0,1,0]
	v_fma_mix_f32 v29, v59, v78, v29 op_sel:[0,1,0] op_sel_hi:[0,1,0]
	v_fma_mix_f32 v30, v59, v79, v30 op_sel_hi:[0,1,0]
	v_fma_mix_f32 v31, v59, v79, v31 op_sel:[0,1,0] op_sel_hi:[0,1,0]
	s_waitcnt vmcnt(5)
	v_fma_mix_f32 v24, v61, v80, v24 op_sel_hi:[0,1,0]
	v_fma_mix_f32 v25, v61, v80, v25 op_sel:[0,1,0] op_sel_hi:[0,1,0]
	v_fma_mix_f32 v26, v61, v81, v26 op_sel_hi:[0,1,0]
	v_fma_mix_f32 v27, v61, v81, v27 op_sel:[0,1,0] op_sel_hi:[0,1,0]
	v_fma_mix_f32 v28, v61, v82, v28 op_sel_hi:[0,1,0]
	v_fma_mix_f32 v29, v61, v82, v29 op_sel:[0,1,0] op_sel_hi:[0,1,0]
	v_fma_mix_f32 v30, v61, v83, v30 op_sel_hi:[0,1,0]
	v_fma_mix_f32 v31, v61, v83, v31 op_sel:[0,1,0] op_sel_hi:[0,1,0]
	s_waitcnt vmcnt(4)
	v_fma_mix_f32 v24, v63, v84, v24 op_sel_hi:[0,1,0]
	v_fma_mix_f32 v25, v63, v84, v25 op_sel:[0,1,0] op_sel_hi:[0,1,0]
	v_fma_mix_f32 v26, v63, v85, v26 op_sel_hi:[0,1,0]
	v_fma_mix_f32 v27, v63, v85, v27 op_sel:[0,1,0] op_sel_hi:[0,1,0]
	v_fma_mix_f32 v28, v63, v86, v28 op_sel_hi:[0,1,0]
	v_fma_mix_f32 v29, v63, v86, v29 op_sel:[0,1,0] op_sel_hi:[0,1,0]
	v_fma_mix_f32 v30, v63, v87, v30 op_sel_hi:[0,1,0]
	v_fma_mix_f32 v31, v63, v87, v31 op_sel:[0,1,0] op_sel_hi:[0,1,0]
	s_waitcnt vmcnt(3)
	v_fma_mix_f32 v24, v65, v88, v24 op_sel_hi:[0,1,0]
	v_fma_mix_f32 v25, v65, v88, v25 op_sel:[0,1,0] op_sel_hi:[0,1,0]
	v_fma_mix_f32 v26, v65, v89, v26 op_sel_hi:[0,1,0]
	v_fma_mix_f32 v27, v65, v89, v27 op_sel:[0,1,0] op_sel_hi:[0,1,0]
	v_fma_mix_f32 v28, v65, v90, v28 op_sel_hi:[0,1,0]
	v_fma_mix_f32 v29, v65, v90, v29 op_sel:[0,1,0] op_sel_hi:[0,1,0]
	v_fma_mix_f32 v30, v65, v91, v30 op_sel_hi:[0,1,0]
	v_fma_mix_f32 v31, v65, v91, v31 op_sel:[0,1,0] op_sel_hi:[0,1,0]
	s_waitcnt vmcnt(2)
	v_fma_mix_f32 v24, v67, v92, v24 op_sel_hi:[0,1,0]
	v_fma_mix_f32 v25, v67, v92, v25 op_sel:[0,1,0] op_sel_hi:[0,1,0]
	v_fma_mix_f32 v26, v67, v93, v26 op_sel_hi:[0,1,0]
	v_fma_mix_f32 v27, v67, v93, v27 op_sel:[0,1,0] op_sel_hi:[0,1,0]
	v_fma_mix_f32 v28, v67, v94, v28 op_sel_hi:[0,1,0]
	v_fma_mix_f32 v29, v67, v94, v29 op_sel:[0,1,0] op_sel_hi:[0,1,0]
	v_fma_mix_f32 v30, v67, v95, v30 op_sel_hi:[0,1,0]
	v_fma_mix_f32 v31, v67, v95, v31 op_sel:[0,1,0] op_sel_hi:[0,1,0]
	s_waitcnt vmcnt(1)
	v_fma_mix_f32 v24, v69, v96, v24 op_sel_hi:[0,1,0]
	v_fma_mix_f32 v25, v69, v96, v25 op_sel:[0,1,0] op_sel_hi:[0,1,0]
	v_fma_mix_f32 v26, v69, v97, v26 op_sel_hi:[0,1,0]
	v_fma_mix_f32 v27, v69, v97, v27 op_sel:[0,1,0] op_sel_hi:[0,1,0]
	v_fma_mix_f32 v28, v69, v98, v28 op_sel_hi:[0,1,0]
	v_fma_mix_f32 v29, v69, v98, v29 op_sel:[0,1,0] op_sel_hi:[0,1,0]
	v_fma_mix_f32 v30, v69, v99, v30 op_sel_hi:[0,1,0]
	v_fma_mix_f32 v31, v69, v99, v31 op_sel:[0,1,0] op_sel_hi:[0,1,0]
	s_waitcnt vmcnt(0)
	v_fma_mix_f32 v24, v71, v100, v24 op_sel_hi:[0,1,0]
	v_fma_mix_f32 v25, v71, v100, v25 op_sel:[0,1,0] op_sel_hi:[0,1,0]
	v_fma_mix_f32 v26, v71, v101, v26 op_sel_hi:[0,1,0]
	v_fma_mix_f32 v27, v71, v101, v27 op_sel:[0,1,0] op_sel_hi:[0,1,0]
	v_fma_mix_f32 v28, v71, v102, v28 op_sel_hi:[0,1,0]
	v_fma_mix_f32 v29, v71, v102, v29 op_sel:[0,1,0] op_sel_hi:[0,1,0]
	v_fma_mix_f32 v30, v71, v103, v30 op_sel_hi:[0,1,0]
	v_fma_mix_f32 v31, v71, v103, v31 op_sel:[0,1,0] op_sel_hi:[0,1,0]

.Lsw_wskip2:
.Lsw_wk3:
	s_waitcnt vmcnt(0)
	v_lshrrev_b32_e32 v57, 13, v54
	v_cmp_eq_u32_e32 vcc, s55, v57
	v_cmp_lt_u32_e64 s[52:53], v1, v47
	s_and_b64 s[50:51], vcc, s[52:53]
	s_cmp_lg_u64 s[50:51], 0
	s_cbranch_scc0 .Lsw_wskip3
	v_lshrrev_b64 v[58:59], v6, s[50:51]
	v_lshrrev_b32_e32 v56, 5, v54
	v_not_b32_e32 v58, v58
	v_lshlrev_b32_e32 v56, 2, v56
	v_or_b32_e32 v58, 0x10000, v58
	ds_read_b32 v57, v56
	v_ffbl_b32_e32 v60, v58
	s_nop 0
	v_cmp_lt_u32_e32 vcc, v1, v60
	s_waitcnt lgkmcnt(0)
	v_mul_f32_e32 v59, v55, v57
	v_cndmask_b32_e32 v58, 0, v54, vcc
	v_cndmask_b32_e32 v59, 0, v59, vcc
	ds_write_b64 v4, v[58:59]
	v_add_u32_e32 v43, v43, v60
	v_sub_u32_e32 v47, v47, v60
	v_cmp_lt_u32_e32 vcc, v1, v47
	v_add_u32_e32 v56, v43, v1
	v_lshlrev_b32_e32 v56, 3, v56
	v_mov_b32_e32 v54, 0
	v_mov_b32_e32 v55, 0
	s_and_saveexec_b64 s[36:37], vcc
	global_load_dwordx2 v[54:55], v56, s[6:7]
	s_mov_b64 exec, s[36:37]
	v_readlane_b32 s40, v60, 0
	v_readlane_b32 s41, v60, 16
	v_readlane_b32 s42, v60, 32
	v_readlane_b32 s43, v60, 48
	s_nop 0
	s_max_u32 s40, s40, s41
	s_max_u32 s42, s42, s43
	s_max_u32 s40, s40, s42
	s_mov_b32 s58, s40

.Lsw_go3:
	s_add_u32 s60, s60, 1
	s_cmp_gt_u32 s40, 8
	s_addc_u32 s60, s60, 0
	ds_read_b128 v[56:59], v5 offset:0
	ds_read_b128 v[60:63], v5 offset:16
	ds_read_b128 v[64:67], v5 offset:32
	ds_read_b128 v[68:71], v5 offset:48
	s_waitcnt lgkmcnt(0)
	v_lshl_or_b32 v104, v56, 8, v2
	global_load_dwordx4 v[72:75], v104, s[8:9]
	v_lshl_or_b32 v104, v58, 8, v2
	global_load_dwordx4 v[76:79], v104, s[8:9]
	v_lshl_or_b32 v104, v60, 8, v2
	global_load_dwordx4 v[80:83], v104, s[8:9]
	v_lshl_or_b32 v104, v62, 8, v2
	global_load_dwordx4 v[84:87], v104, s[8:9]
	v_lshl_or_b32 v104, v64, 8, v2
	global_load_dwordx4 v[88:91], v104, s[8:9]
	v_lshl_or_b32 v104, v66, 8, v2
	global_load_dwordx4 v[92:95], v104, s[8:9]
	v_lshl_or_b32 v104, v68, 8, v2
	global_load_dwordx4 v[96:99], v104, s[8:9]
	v_lshl_or_b32 v104, v70, 8, v2
	global_load_dwordx4 v[100:103], v104, s[8:9]
	s_waitcnt vmcnt(7)
	v_fma_mix_f32 v32, v57, v72, v32 op_sel_hi:[0,1,0]
	v_fma_mix_f32 v33, v57, v72, v33 op_sel:[0,1,0] op_sel_hi:[0,1,0]
	v_fma_mix_f32 v34, v57, v73, v34 op_sel_hi:[0,1,0]
	v_fma_mix_f32 v35, v57, v73, v35 op_sel:[0,1,0] op_sel_hi:[0,1,0]
	v_fma_mix_f32 v36, v57, v74, v36 op_sel_hi:[0,1,0]
	v_fma_mix_f32 v37, v57, v74, v37 op_sel:[0,1,0] op_sel_hi:[0,1,0]
	v_fma_mix_f32 v38, v57, v75, v38 op_sel_hi:[0,1,0]
	v_fma_mix_f32 v39, v57, v75, v39 op_sel:[0,1,0] op_sel_hi:[0,1,0]
	s_waitcnt vmcnt(6)
	v_fma_mix_f32 v32, v59, v76, v32 op_sel_hi:[0,1,0]
	v_fma_mix_f32 v33, v59, v76, v33 op_sel:[0,1,0] op_sel_hi:[0,1,0]
	v_fma_mix_f32 v34, v59, v77, v34 op_sel_hi:[0,1,0]
	v_fma_mix_f32 v35, v59, v77, v35 op_sel:[0,1,0] op_sel_hi:[0,1,0]
	v_fma_mix_f32 v36, v59, v78, v36 op_sel_hi:[0,1,0]
	v_fma_mix_f32 v37, v59, v78, v37 op_sel:[0,1,0] op_sel_hi:[0,1,0]
	v_fma_mix_f32 v38, v59, v79, v38 op_sel_hi:[0,1,0]
	v_fma_mix_f32 v39, v59, v79, v39 op_sel:[0,1,0] op_sel_hi:[0,1,0]
	s_waitcnt vmcnt(5)
	v_fma_mix_f32 v32, v61, v80, v32 op_sel_hi:[0,1,0]
	v_fma_mix_f32 v33, v61, v80, v33 op_sel:[0,1,0] op_sel_hi:[0,1,0]
	v_fma_mix_f32 v34, v61, v81, v34 op_sel_hi:[0,1,0]
	v_fma_mix_f32 v35, v61, v81, v35 op_sel:[0,1,0] op_sel_hi:[0,1,0]
	v_fma_mix_f32 v36, v61, v82, v36 op_sel_hi:[0,1,0]
	v_fma_mix_f32 v37, v61, v82, v37 op_sel:[0,1,0] op_sel_hi:[0,1,0]
	v_fma_mix_f32 v38, v61, v83, v38 op_sel_hi:[0,1,0]
	v_fma_mix_f32 v39, v61, v83, v39 op_sel:[0,1,0] op_sel_hi:[0,1,0]
	s_waitcnt vmcnt(4)
	v_fma_mix_f32 v32, v63, v84, v32 op_sel_hi:[0,1,0]
	v_fma_mix_f32 v33, v63, v84, v33 op_sel:[0,1,0] op_sel_hi:[0,1,0]
	v_fma_mix_f32 v34, v63, v85, v34 op_sel_hi:[0,1,0]
	v_fma_mix_f32 v35, v63, v85, v35 op_sel:[0,1,0] op_sel_hi:[0,1,0]
	v_fma_mix_f32 v36, v63, v86, v36 op_sel_hi:[0,1,0]
	v_fma_mix_f32 v37, v63, v86, v37 op_sel:[0,1,0] op_sel_hi:[0,1,0]
	v_fma_mix_f32 v38, v63, v87, v38 op_sel_hi:[0,1,0]
	v_fma_mix_f32 v39, v63, v87, v39 op_sel:[0,1,0] op_sel_hi:[0,1,0]
	s_waitcnt vmcnt(3)
	v_fma_mix_f32 v32, v65, v88, v32 op_sel_hi:[0,1,0]
	v_fma_mix_f32 v33, v65, v88, v33 op_sel:[0,1,0] op_sel_hi:[0,1,0]
	v_fma_mix_f32 v34, v65, v89, v34 op_sel_hi:[0,1,0]
	v_fma_mix_f32 v35, v65, v89, v35 op_sel:[0,1,0] op_sel_hi:[0,1,0]
	v_fma_mix_f32 v36, v65, v90, v36 op_sel_hi:[0,1,0]
	v_fma_mix_f32 v37, v65, v90, v37 op_sel:[0,1,0] op_sel_hi:[0,1,0]
	v_fma_mix_f32 v38, v65, v91, v38 op_sel_hi:[0,1,0]
	v_fma_mix_f32 v39, v65, v91, v39 op_sel:[0,1,0] op_sel_hi:[0,1,0]
	s_waitcnt vmcnt(2)
	v_fma_mix_f32 v32, v67, v92, v32 op_sel_hi:[0,1,0]
	v_fma_mix_f32 v33, v67, v92, v33 op_sel:[0,1,0] op_sel_hi:[0,1,0]
	v_fma_mix_f32 v34, v67, v93, v34 op_sel_hi:[0,1,0]
	v_fma_mix_f32 v35, v67, v93, v35 op_sel:[0,1,0] op_sel_hi:[0,1,0]
	v_fma_mix_f32 v36, v67, v94, v36 op_sel_hi:[0,1,0]
	v_fma_mix_f32 v37, v67, v94, v37 op_sel:[0,1,0] op_sel_hi:[0,1,0]
	v_fma_mix_f32 v38, v67, v95, v38 op_sel_hi:[0,1,0]
	v_fma_mix_f32 v39, v67, v95, v39 op_sel:[0,1,0] op_sel_hi:[0,1,0]
	s_waitcnt vmcnt(1)
	v_fma_mix_f32 v32, v69, v96, v32 op_sel_hi:[0,1,0]
	v_fma_mix_f32 v33, v69, v96, v33 op_sel:[0,1,0] op_sel_hi:[0,1,0]
	v_fma_mix_f32 v34, v69, v97, v34 op_sel_hi:[0,1,0]
	v_fma_mix_f32 v35, v69, v97, v35 op_sel:[0,1,0] op_sel_hi:[0,1,0]
	v_fma_mix_f32 v36, v69, v98, v36 op_sel_hi:[0,1,0]
	v_fma_mix_f32 v37, v69, v98, v37 op_sel:[0,1,0] op_sel_hi:[0,1,0]
	v_fma_mix_f32 v38, v69, v99, v38 op_sel_hi:[0,1,0]
	v_fma_mix_f32 v39, v69, v99, v39 op_sel:[0,1,0] op_sel_hi:[0,1,0]
	s_waitcnt vmcnt(0)
	v_fma_mix_f32 v32, v71, v100, v32 op_sel_hi:[0,1,0]
	v_fma_mix_f32 v33, v71, v100, v33 op_sel:[0,1,0] op_sel_hi:[0,1,0]
	v_fma_mix_f32 v34, v71, v101, v34 op_sel_hi:[0,1,0]
	v_fma_mix_f32 v35, v71, v101, v35 op_sel:[0,1,0] op_sel_hi:[0,1,0]
	v_fma_mix_f32 v36, v71, v102, v36 op_sel_hi:[0,1,0]
	v_fma_mix_f32 v37, v71, v102, v37 op_sel:[0,1,0] op_sel_hi:[0,1,0]
	v_fma_mix_f32 v38, v71, v103, v38 op_sel_hi:[0,1,0]
	v_fma_mix_f32 v39, v71, v103, v39 op_sel:[0,1,0] op_sel_hi:[0,1,0]
	s_cmp_le_u32 s40, 8
	s_cbranch_scc1 .Lsw_wg3
	ds_read_b128 v[56:59], v5 offset:64
	ds_read_b128 v[60:63], v5 offset:80
	ds_read_b128 v[64:67], v5 offset:96
	ds_read_b128 v[68:71], v5 offset:112
	s_waitcnt lgkmcnt(0)
	v_lshl_or_b32 v104, v56, 8, v2
	global_load_dwordx4 v[72:75], v104, s[8:9]
	v_lshl_or_b32 v104, v58, 8, v2
	global_load_dwordx4 v[76:79], v104, s[8:9]
	v_lshl_or_b32 v104, v60, 8, v2
	global_load_dwordx4 v[80:83], v104, s[8:9]
	v_lshl_or_b32 v104, v62, 8, v2
	global_load_dwordx4 v[84:87], v104, s[8:9]
	v_lshl_or_b32 v104, v64, 8, v2
	global_load_dwordx4 v[88:91], v104, s[8:9]
	v_lshl_or_b32 v104, v66, 8, v2
	global_load_dwordx4 v[92:95], v104, s[8:9]
	v_lshl_or_b32 v104, v68, 8, v2
	global_load_dwordx4 v[96:99], v104, s[8:9]
	v_lshl_or_b32 v104, v70, 8, v2
	global_load_dwordx4 v[100:103], v104, s[8:9]
	s_waitcnt vmcnt(7)
	v_fma_mix_f32 v32, v57, v72, v32 op_sel_hi:[0,1,0]
	v_fma_mix_f32 v33, v57, v72, v33 op_sel:[0,1,0] op_sel_hi:[0,1,0]
	v_fma_mix_f32 v34, v57, v73, v34 op_sel_hi:[0,1,0]
	v_fma_mix_f32 v35, v57, v73, v35 op_sel:[0,1,0] op_sel_hi:[0,1,0]
	v_fma_mix_f32 v36, v57, v74, v36 op_sel_hi:[0,1,0]
	v_fma_mix_f32 v37, v57, v74, v37 op_sel:[0,1,0] op_sel_hi:[0,1,0]
	v_fma_mix_f32 v38, v57, v75, v38 op_sel_hi:[0,1,0]
	v_fma_mix_f32 v39, v57, v75, v39 op_sel:[0,1,0] op_sel_hi:[0,1,0]
	s_waitcnt vmcnt(6)
	v_fma_mix_f32 v32, v59, v76, v32 op_sel_hi:[0,1,0]
	v_fma_mix_f32 v33, v59, v76, v33 op_sel:[0,1,0] op_sel_hi:[0,1,0]
	v_fma_mix_f32 v34, v59, v77, v34 op_sel_hi:[0,1,0]
	v_fma_mix_f32 v35, v59, v77, v35 op_sel:[0,1,0] op_sel_hi:[0,1,0]
	v_fma_mix_f32 v36, v59, v78, v36 op_sel_hi:[0,1,0]
	v_fma_mix_f32 v37, v59, v78, v37 op_sel:[0,1,0] op_sel_hi:[0,1,0]
	v_fma_mix_f32 v38, v59, v79, v38 op_sel_hi:[0,1,0]
	v_fma_mix_f32 v39, v59, v79, v39 op_sel:[0,1,0] op_sel_hi:[0,1,0]
	s_waitcnt vmcnt(5)
	v_fma_mix_f32 v32, v61, v80, v32 op_sel_hi:[0,1,0]
	v_fma_mix_f32 v33, v61, v80, v33 op_sel:[0,1,0] op_sel_hi:[0,1,0]
	v_fma_mix_f32 v34, v61, v81, v34 op_sel_hi:[0,1,0]
	v_fma_mix_f32 v35, v61, v81, v35 op_sel:[0,1,0] op_sel_hi:[0,1,0]
	v_fma_mix_f32 v36, v61, v82, v36 op_sel_hi:[0,1,0]
	v_fma_mix_f32 v37, v61, v82, v37 op_sel:[0,1,0] op_sel_hi:[0,1,0]
	v_fma_mix_f32 v38, v61, v83, v38 op_sel_hi:[0,1,0]
	v_fma_mix_f32 v39, v61, v83, v39 op_sel:[0,1,0] op_sel_hi:[0,1,0]
	s_waitcnt vmcnt(4)
	v_fma_mix_f32 v32, v63, v84, v32 op_sel_hi:[0,1,0]
	v_fma_mix_f32 v33, v63, v84, v33 op_sel:[0,1,0] op_sel_hi:[0,1,0]
	v_fma_mix_f32 v34, v63, v85, v34 op_sel_hi:[0,1,0]
	v_fma_mix_f32 v35, v63, v85, v35 op_sel:[0,1,0] op_sel_hi:[0,1,0]
	v_fma_mix_f32 v36, v63, v86, v36 op_sel_hi:[0,1,0]
	v_fma_mix_f32 v37, v63, v86, v37 op_sel:[0,1,0] op_sel_hi:[0,1,0]
	v_fma_mix_f32 v38, v63, v87, v38 op_sel_hi:[0,1,0]
	v_fma_mix_f32 v39, v63, v87, v39 op_sel:[0,1,0] op_sel_hi:[0,1,0]
	s_waitcnt vmcnt(3)
	v_fma_mix_f32 v32, v65, v88, v32 op_sel_hi:[0,1,0]
	v_fma_mix_f32 v33, v65, v88, v33 op_sel:[0,1,0] op_sel_hi:[0,1,0]
	v_fma_mix_f32 v34, v65, v89, v34 op_sel_hi:[0,1,0]
	v_fma_mix_f32 v35, v65, v89, v35 op_sel:[0,1,0] op_sel_hi:[0,1,0]
	v_fma_mix_f32 v36, v65, v90, v36 op_sel_hi:[0,1,0]
	v_fma_mix_f32 v37, v65, v90, v37 op_sel:[0,1,0] op_sel_hi:[0,1,0]
	v_fma_mix_f32 v38, v65, v91, v38 op_sel_hi:[0,1,0]
	v_fma_mix_f32 v39, v65, v91, v39 op_sel:[0,1,0] op_sel_hi:[0,1,0]
	s_waitcnt vmcnt(2)
	v_fma_mix_f32 v32, v67, v92, v32 op_sel_hi:[0,1,0]
	v_fma_mix_f32 v33, v67, v92, v33 op_sel:[0,1,0] op_sel_hi:[0,1,0]
	v_fma_mix_f32 v34, v67, v93, v34 op_sel_hi:[0,1,0]
	v_fma_mix_f32 v35, v67, v93, v35 op_sel:[0,1,0] op_sel_hi:[0,1,0]
	v_fma_mix_f32 v36, v67, v94, v36 op_sel_hi:[0,1,0]
	v_fma_mix_f32 v37, v67, v94, v37 op_sel:[0,1,0] op_sel_hi:[0,1,0]
	v_fma_mix_f32 v38, v67, v95, v38 op_sel_hi:[0,1,0]
	v_fma_mix_f32 v39, v67, v95, v39 op_sel:[0,1,0] op_sel_hi:[0,1,0]
	s_waitcnt vmcnt(1)
	v_fma_mix_f32 v32, v69, v96, v32 op_sel_hi:[0,1,0]
	v_fma_mix_f32 v33, v69, v96, v33 op_sel:[0,1,0] op_sel_hi:[0,1,0]
	v_fma_mix_f32 v34, v69, v97, v34 op_sel_hi:[0,1,0]
	v_fma_mix_f32 v35, v69, v97, v35 op_sel:[0,1,0] op_sel_hi:[0,1,0]
	v_fma_mix_f32 v36, v69, v98, v36 op_sel_hi:[0,1,0]
	v_fma_mix_f32 v37, v69, v98, v37 op_sel:[0,1,0] op_sel_hi:[0,1,0]
	v_fma_mix_f32 v38, v69, v99, v38 op_sel_hi:[0,1,0]
	v_fma_mix_f32 v39, v69, v99, v39 op_sel:[0,1,0] op_sel_hi:[0,1,0]
	s_waitcnt vmcnt(0)
	v_fma_mix_f32 v32, v71, v100, v32 op_sel_hi:[0,1,0]
	v_fma_mix_f32 v33, v71, v100, v33 op_sel:[0,1,0] op_sel_hi:[0,1,0]
	v_fma_mix_f32 v34, v71, v101, v34 op_sel_hi:[0,1,0]
	v_fma_mix_f32 v35, v71, v101, v35 op_sel:[0,1,0] op_sel_hi:[0,1,0]
	v_fma_mix_f32 v36, v71, v102, v36 op_sel_hi:[0,1,0]
	v_fma_mix_f32 v37, v71, v102, v37 op_sel:[0,1,0] op_sel_hi:[0,1,0]
	v_fma_mix_f32 v38, v71, v103, v38 op_sel_hi:[0,1,0]
	v_fma_mix_f32 v39, v71, v103, v39 op_sel:[0,1,0] op_sel_hi:[0,1,0]

.Lsw_wskip3:
	s_add_u32 s55, s55, s56
	s_add_u32 s57, s57, 1
	s_cmp_lt_u32 s57, s54
	s_cbranch_scc1 .Lsw_win
	s_nop 1
	v_readlane_b32 s40, v44, 0
	v_readlane_b32 s41, v44, 16
	v_readlane_b32 s42, v44, 32
	v_readlane_b32 s43, v44, 48
	s_nop 0
	s_max_u32 s40, s40, s41
	s_max_u32 s42, s42, s43
	s_max_u32 s30, s40, s42
	v_readlane_b32 s40, v45, 0
	v_readlane_b32 s41, v45, 16
	v_readlane_b32 s42, v45, 32
	v_readlane_b32 s43, v45, 48
	s_nop 0
	s_max_u32 s40, s40, s41
	s_max_u32 s42, s42, s43
	s_max_u32 s31, s40, s42
	v_readlane_b32 s40, v46, 0
	v_readlane_b32 s41, v46, 16
	v_readlane_b32 s42, v46, 32
	v_readlane_b32 s43, v46, 48
	s_nop 0
	s_max_u32 s40, s40, s41
	s_max_u32 s42, s42, s43
	s_max_u32 s32, s40, s42
	v_readlane_b32 s40, v47, 0
	v_readlane_b32 s41, v47, 16
	v_readlane_b32 s42, v47, 32
	v_readlane_b32 s43, v47, 48
	s_nop 0
	s_max_u32 s40, s40, s41
	s_max_u32 s42, s42, s43
	s_max_u32 s33, s40, s42
	s_max_u32 s40, s30, s31
	s_max_u32 s41, s32, s33
	s_max_u32 s40, s40, s41
	s_add_u32 s40, s40, 15
	s_lshr_b32 s29, s40, 4
	s_mov_b32 s28, 0
	s_cmp_eq_u32 s29, 0
	s_cbranch_scc1 .Lsw_rounds_done
.Lsw_round:
	s_lshl_b32 s38, s28, 4
	s_add_u32 s39, s38, 16
	s_cmp_ge_u32 s38, s30
	s_cbranch_scc1 .Lsw_skip0
	s_waitcnt vmcnt(0)
	v_lshrrev_b32_e32 v56, 5, v48
	v_lshlrev_b32_e32 v56, 2, v56
	ds_read_b32 v57, v56
	v_mov_b32_e32 v58, v48
	s_waitcnt lgkmcnt(0)
	v_mul_f32_e32 v59, v49, v57
	ds_write_b64 v4, v[58:59]
	v_add_u32_e32 v56, s39, v1
	v_cmp_lt_u32_e32 vcc, v56, v44
	v_add_u32_e32 v56, v56, v40
	v_lshlrev_b32_e32 v56, 3, v56
	v_mov_b32_e32 v48, 0
	v_mov_b32_e32 v49, 0
	s_and_saveexec_b64 s[36:37], vcc
	global_load_dwordx2 v[48:49], v56, s[6:7]
	s_mov_b64 exec, s[36:37]
	s_sub_u32 s40, s30, s38
	ds_read_b128 v[56:59], v5 offset:0
	ds_read_b128 v[60:63], v5 offset:16
	ds_read_b128 v[64:67], v5 offset:32
	ds_read_b128 v[68:71], v5 offset:48
	s_waitcnt lgkmcnt(0)
	v_lshl_or_b32 v104, v56, 8, v2
	global_load_dwordx4 v[72:75], v104, s[8:9]
	v_lshl_or_b32 v104, v58, 8, v2
	global_load_dwordx4 v[76:79], v104, s[8:9]
	v_lshl_or_b32 v104, v60, 8, v2
	global_load_dwordx4 v[80:83], v104, s[8:9]
	v_lshl_or_b32 v104, v62, 8, v2
	global_load_dwordx4 v[84:87], v104, s[8:9]
	v_lshl_or_b32 v104, v64, 8, v2
	global_load_dwordx4 v[88:91], v104, s[8:9]
	v_lshl_or_b32 v104, v66, 8, v2
	global_load_dwordx4 v[92:95], v104, s[8:9]
	v_lshl_or_b32 v104, v68, 8, v2
	global_load_dwordx4 v[96:99], v104, s[8:9]
	v_lshl_or_b32 v104, v70, 8, v2
	global_load_dwordx4 v[100:103], v104, s[8:9]
	s_waitcnt vmcnt(7)
	v_fma_mix_f32 v8, v57, v72, v8 op_sel_hi:[0,1,0]
	v_fma_mix_f32 v9, v57, v72, v9 op_sel:[0,1,0] op_sel_hi:[0,1,0]
	v_fma_mix_f32 v10, v57, v73, v10 op_sel_hi:[0,1,0]
	v_fma_mix_f32 v11, v57, v73, v11 op_sel:[0,1,0] op_sel_hi:[0,1,0]
	v_fma_mix_f32 v12, v57, v74, v12 op_sel_hi:[0,1,0]
	v_fma_mix_f32 v13, v57, v74, v13 op_sel:[0,1,0] op_sel_hi:[0,1,0]
	v_fma_mix_f32 v14, v57, v75, v14 op_sel_hi:[0,1,0]
	v_fma_mix_f32 v15, v57, v75, v15 op_sel:[0,1,0] op_sel_hi:[0,1,0]
	s_waitcnt vmcnt(6)
	v_fma_mix_f32 v8, v59, v76, v8 op_sel_hi:[0,1,0]
	v_fma_mix_f32 v9, v59, v76, v9 op_sel:[0,1,0] op_sel_hi:[0,1,0]
	v_fma_mix_f32 v10, v59, v77, v10 op_sel_hi:[0,1,0]
	v_fma_mix_f32 v11, v59, v77, v11 op_sel:[0,1,0] op_sel_hi:[0,1,0]
	v_fma_mix_f32 v12, v59, v78, v12 op_sel_hi:[0,1,0]
	v_fma_mix_f32 v13, v59, v78, v13 op_sel:[0,1,0] op_sel_hi:[0,1,0]
	v_fma_mix_f32 v14, v59, v79, v14 op_sel_hi:[0,1,0]
	v_fma_mix_f32 v15, v59, v79, v15 op_sel:[0,1,0] op_sel_hi:[0,1,0]
	s_waitcnt vmcnt(5)
	v_fma_mix_f32 v8, v61, v80, v8 op_sel_hi:[0,1,0]
	v_fma_mix_f32 v9, v61, v80, v9 op_sel:[0,1,0] op_sel_hi:[0,1,0]
	v_fma_mix_f32 v10, v61, v81, v10 op_sel_hi:[0,1,0]
	v_fma_mix_f32 v11, v61, v81, v11 op_sel:[0,1,0] op_sel_hi:[0,1,0]
	v_fma_mix_f32 v12, v61, v82, v12 op_sel_hi:[0,1,0]
	v_fma_mix_f32 v13, v61, v82, v13 op_sel:[0,1,0] op_sel_hi:[0,1,0]
	v_fma_mix_f32 v14, v61, v83, v14 op_sel_hi:[0,1,0]
	v_fma_mix_f32 v15, v61, v83, v15 op_sel:[0,1,0] op_sel_hi:[0,1,0]
	s_waitcnt vmcnt(4)
	v_fma_mix_f32 v8, v63, v84, v8 op_sel_hi:[0,1,0]
	v_fma_mix_f32 v9, v63, v84, v9 op_sel:[0,1,0] op_sel_hi:[0,1,0]
	v_fma_mix_f32 v10, v63, v85, v10 op_sel_hi:[0,1,0]
	v_fma_mix_f32 v11, v63, v85, v11 op_sel:[0,1,0] op_sel_hi:[0,1,0]
	v_fma_mix_f32 v12, v63, v86, v12 op_sel_hi:[0,1,0]
	v_fma_mix_f32 v13, v63, v86, v13 op_sel:[0,1,0] op_sel_hi:[0,1,0]
	v_fma_mix_f32 v14, v63, v87, v14 op_sel_hi:[0,1,0]
	v_fma_mix_f32 v15, v63, v87, v15 op_sel:[0,1,0] op_sel_hi:[0,1,0]
	s_waitcnt vmcnt(3)
	v_fma_mix_f32 v8, v65, v88, v8 op_sel_hi:[0,1,0]
	v_fma_mix_f32 v9, v65, v88, v9 op_sel:[0,1,0] op_sel_hi:[0,1,0]
	v_fma_mix_f32 v10, v65, v89, v10 op_sel_hi:[0,1,0]
	v_fma_mix_f32 v11, v65, v89, v11 op_sel:[0,1,0] op_sel_hi:[0,1,0]
	v_fma_mix_f32 v12, v65, v90, v12 op_sel_hi:[0,1,0]
	v_fma_mix_f32 v13, v65, v90, v13 op_sel:[0,1,0] op_sel_hi:[0,1,0]
	v_fma_mix_f32 v14, v65, v91, v14 op_sel_hi:[0,1,0]
	v_fma_mix_f32 v15, v65, v91, v15 op_sel:[0,1,0] op_sel_hi:[0,1,0]
	s_waitcnt vmcnt(2)
	v_fma_mix_f32 v8, v67, v92, v8 op_sel_hi:[0,1,0]
	v_fma_mix_f32 v9, v67, v92, v9 op_sel:[0,1,0] op_sel_hi:[0,1,0]
	v_fma_mix_f32 v10, v67, v93, v10 op_sel_hi:[0,1,0]
	v_fma_mix_f32 v11, v67, v93, v11 op_sel:[0,1,0] op_sel_hi:[0,1,0]
	v_fma_mix_f32 v12, v67, v94, v12 op_sel_hi:[0,1,0]
	v_fma_mix_f32 v13, v67, v94, v13 op_sel:[0,1,0] op_sel_hi:[0,1,0]
	v_fma_mix_f32 v14, v67, v95, v14 op_sel_hi:[0,1,0]
	v_fma_mix_f32 v15, v67, v95, v15 op_sel:[0,1,0] op_sel_hi:[0,1,0]
	s_waitcnt vmcnt(1)
	v_fma_mix_f32 v8, v69, v96, v8 op_sel_hi:[0,1,0]
	v_fma_mix_f32 v9, v69, v96, v9 op_sel:[0,1,0] op_sel_hi:[0,1,0]
	v_fma_mix_f32 v10, v69, v97, v10 op_sel_hi:[0,1,0]
	v_fma_mix_f32 v11, v69, v97, v11 op_sel:[0,1,0] op_sel_hi:[0,1,0]
	v_fma_mix_f32 v12, v69, v98, v12 op_sel_hi:[0,1,0]
	v_fma_mix_f32 v13, v69, v98, v13 op_sel:[0,1,0] op_sel_hi:[0,1,0]
	v_fma_mix_f32 v14, v69, v99, v14 op_sel_hi:[0,1,0]
	v_fma_mix_f32 v15, v69, v99, v15 op_sel:[0,1,0] op_sel_hi:[0,1,0]
	s_waitcnt vmcnt(0)
	v_fma_mix_f32 v8, v71, v100, v8 op_sel_hi:[0,1,0]
	v_fma_mix_f32 v9, v71, v100, v9 op_sel:[0,1,0] op_sel_hi:[0,1,0]
	v_fma_mix_f32 v10, v71, v101, v10 op_sel_hi:[0,1,0]
	v_fma_mix_f32 v11, v71, v101, v11 op_sel:[0,1,0] op_sel_hi:[0,1,0]
	v_fma_mix_f32 v12, v71, v102, v12 op_sel_hi:[0,1,0]
	v_fma_mix_f32 v13, v71, v102, v13 op_sel:[0,1,0] op_sel_hi:[0,1,0]
	v_fma_mix_f32 v14, v71, v103, v14 op_sel_hi:[0,1,0]
	v_fma_mix_f32 v15, v71, v103, v15 op_sel:[0,1,0] op_sel_hi:[0,1,0]
	s_cmp_le_u32 s40, 8
	s_cbranch_scc1 .Lsw_skip0
	ds_read_b128 v[56:59], v5 offset:64
	ds_read_b128 v[60:63], v5 offset:80
	ds_read_b128 v[64:67], v5 offset:96
	ds_read_b128 v[68:71], v5 offset:112
	s_waitcnt lgkmcnt(0)
	v_lshl_or_b32 v104, v56, 8, v2
	global_load_dwordx4 v[72:75], v104, s[8:9]
	v_lshl_or_b32 v104, v58, 8, v2
	global_load_dwordx4 v[76:79], v104, s[8:9]
	v_lshl_or_b32 v104, v60, 8, v2
	global_load_dwordx4 v[80:83], v104, s[8:9]
	v_lshl_or_b32 v104, v62, 8, v2
	global_load_dwordx4 v[84:87], v104, s[8:9]
	v_lshl_or_b32 v104, v64, 8, v2
	global_load_dwordx4 v[88:91], v104, s[8:9]
	v_lshl_or_b32 v104, v66, 8, v2
	global_load_dwordx4 v[92:95], v104, s[8:9]
	v_lshl_or_b32 v104, v68, 8, v2
	global_load_dwordx4 v[96:99], v104, s[8:9]
	v_lshl_or_b32 v104, v70, 8, v2
	global_load_dwordx4 v[100:103], v104, s[8:9]
	s_waitcnt vmcnt(7)
	v_fma_mix_f32 v8, v57, v72, v8 op_sel_hi:[0,1,0]
	v_fma_mix_f32 v9, v57, v72, v9 op_sel:[0,1,0] op_sel_hi:[0,1,0]
	v_fma_mix_f32 v10, v57, v73, v10 op_sel_hi:[0,1,0]
	v_fma_mix_f32 v11, v57, v73, v11 op_sel:[0,1,0] op_sel_hi:[0,1,0]
	v_fma_mix_f32 v12, v57, v74, v12 op_sel_hi:[0,1,0]
	v_fma_mix_f32 v13, v57, v74, v13 op_sel:[0,1,0] op_sel_hi:[0,1,0]
	v_fma_mix_f32 v14, v57, v75, v14 op_sel_hi:[0,1,0]
	v_fma_mix_f32 v15, v57, v75, v15 op_sel:[0,1,0] op_sel_hi:[0,1,0]
	s_waitcnt vmcnt(6)
	v_fma_mix_f32 v8, v59, v76, v8 op_sel_hi:[0,1,0]
	v_fma_mix_f32 v9, v59, v76, v9 op_sel:[0,1,0] op_sel_hi:[0,1,0]
	v_fma_mix_f32 v10, v59, v77, v10 op_sel_hi:[0,1,0]
	v_fma_mix_f32 v11, v59, v77, v11 op_sel:[0,1,0] op_sel_hi:[0,1,0]
	v_fma_mix_f32 v12, v59, v78, v12 op_sel_hi:[0,1,0]
	v_fma_mix_f32 v13, v59, v78, v13 op_sel:[0,1,0] op_sel_hi:[0,1,0]
	v_fma_mix_f32 v14, v59, v79, v14 op_sel_hi:[0,1,0]
	v_fma_mix_f32 v15, v59, v79, v15 op_sel:[0,1,0] op_sel_hi:[0,1,0]
	s_waitcnt vmcnt(5)
	v_fma_mix_f32 v8, v61, v80, v8 op_sel_hi:[0,1,0]
	v_fma_mix_f32 v9, v61, v80, v9 op_sel:[0,1,0] op_sel_hi:[0,1,0]
	v_fma_mix_f32 v10, v61, v81, v10 op_sel_hi:[0,1,0]
	v_fma_mix_f32 v11, v61, v81, v11 op_sel:[0,1,0] op_sel_hi:[0,1,0]
	v_fma_mix_f32 v12, v61, v82, v12 op_sel_hi:[0,1,0]
	v_fma_mix_f32 v13, v61, v82, v13 op_sel:[0,1,0] op_sel_hi:[0,1,0]
	v_fma_mix_f32 v14, v61, v83, v14 op_sel_hi:[0,1,0]
	v_fma_mix_f32 v15, v61, v83, v15 op_sel:[0,1,0] op_sel_hi:[0,1,0]
	s_waitcnt vmcnt(4)
	v_fma_mix_f32 v8, v63, v84, v8 op_sel_hi:[0,1,0]
	v_fma_mix_f32 v9, v63, v84, v9 op_sel:[0,1,0] op_sel_hi:[0,1,0]
	v_fma_mix_f32 v10, v63, v85, v10 op_sel_hi:[0,1,0]
	v_fma_mix_f32 v11, v63, v85, v11 op_sel:[0,1,0] op_sel_hi:[0,1,0]
	v_fma_mix_f32 v12, v63, v86, v12 op_sel_hi:[0,1,0]
	v_fma_mix_f32 v13, v63, v86, v13 op_sel:[0,1,0] op_sel_hi:[0,1,0]
	v_fma_mix_f32 v14, v63, v87, v14 op_sel_hi:[0,1,0]
	v_fma_mix_f32 v15, v63, v87, v15 op_sel:[0,1,0] op_sel_hi:[0,1,0]
	s_waitcnt vmcnt(3)
	v_fma_mix_f32 v8, v65, v88, v8 op_sel_hi:[0,1,0]
	v_fma_mix_f32 v9, v65, v88, v9 op_sel:[0,1,0] op_sel_hi:[0,1,0]
	v_fma_mix_f32 v10, v65, v89, v10 op_sel_hi:[0,1,0]
	v_fma_mix_f32 v11, v65, v89, v11 op_sel:[0,1,0] op_sel_hi:[0,1,0]
	v_fma_mix_f32 v12, v65, v90, v12 op_sel_hi:[0,1,0]
	v_fma_mix_f32 v13, v65, v90, v13 op_sel:[0,1,0] op_sel_hi:[0,1,0]
	v_fma_mix_f32 v14, v65, v91, v14 op_sel_hi:[0,1,0]
	v_fma_mix_f32 v15, v65, v91, v15 op_sel:[0,1,0] op_sel_hi:[0,1,0]
	s_waitcnt vmcnt(2)
	v_fma_mix_f32 v8, v67, v92, v8 op_sel_hi:[0,1,0]
	v_fma_mix_f32 v9, v67, v92, v9 op_sel:[0,1,0] op_sel_hi:[0,1,0]
	v_fma_mix_f32 v10, v67, v93, v10 op_sel_hi:[0,1,0]
	v_fma_mix_f32 v11, v67, v93, v11 op_sel:[0,1,0] op_sel_hi:[0,1,0]
	v_fma_mix_f32 v12, v67, v94, v12 op_sel_hi:[0,1,0]
	v_fma_mix_f32 v13, v67, v94, v13 op_sel:[0,1,0] op_sel_hi:[0,1,0]
	v_fma_mix_f32 v14, v67, v95, v14 op_sel_hi:[0,1,0]
	v_fma_mix_f32 v15, v67, v95, v15 op_sel:[0,1,0] op_sel_hi:[0,1,0]
	s_waitcnt vmcnt(1)
	v_fma_mix_f32 v8, v69, v96, v8 op_sel_hi:[0,1,0]
	v_fma_mix_f32 v9, v69, v96, v9 op_sel:[0,1,0] op_sel_hi:[0,1,0]
	v_fma_mix_f32 v10, v69, v97, v10 op_sel_hi:[0,1,0]
	v_fma_mix_f32 v11, v69, v97, v11 op_sel:[0,1,0] op_sel_hi:[0,1,0]
	v_fma_mix_f32 v12, v69, v98, v12 op_sel_hi:[0,1,0]
	v_fma_mix_f32 v13, v69, v98, v13 op_sel:[0,1,0] op_sel_hi:[0,1,0]
	v_fma_mix_f32 v14, v69, v99, v14 op_sel_hi:[0,1,0]
	v_fma_mix_f32 v15, v69, v99, v15 op_sel:[0,1,0] op_sel_hi:[0,1,0]
	s_waitcnt vmcnt(0)
	v_fma_mix_f32 v8, v71, v100, v8 op_sel_hi:[0,1,0]
	v_fma_mix_f32 v9, v71, v100, v9 op_sel:[0,1,0] op_sel_hi:[0,1,0]
	v_fma_mix_f32 v10, v71, v101, v10 op_sel_hi:[0,1,0]
	v_fma_mix_f32 v11, v71, v101, v11 op_sel:[0,1,0] op_sel_hi:[0,1,0]
	v_fma_mix_f32 v12, v71, v102, v12 op_sel_hi:[0,1,0]
	v_fma_mix_f32 v13, v71, v102, v13 op_sel:[0,1,0] op_sel_hi:[0,1,0]
	v_fma_mix_f32 v14, v71, v103, v14 op_sel_hi:[0,1,0]
	v_fma_mix_f32 v15, v71, v103, v15 op_sel:[0,1,0] op_sel_hi:[0,1,0]
.Lsw_skip0:
	s_cmp_ge_u32 s38, s31
	s_cbranch_scc1 .Lsw_skip1
	s_waitcnt vmcnt(0)
	v_lshrrev_b32_e32 v56, 5, v50
	v_lshlrev_b32_e32 v56, 2, v56
	ds_read_b32 v57, v56
	v_mov_b32_e32 v58, v50
	s_waitcnt lgkmcnt(0)
	v_mul_f32_e32 v59, v51, v57
	ds_write_b64 v4, v[58:59]
	v_add_u32_e32 v56, s39, v1
	v_cmp_lt_u32_e32 vcc, v56, v45
	v_add_u32_e32 v56, v56, v41
	v_lshlrev_b32_e32 v56, 3, v56
	v_mov_b32_e32 v50, 0
	v_mov_b32_e32 v51, 0
	s_and_saveexec_b64 s[36:37], vcc
	global_load_dwordx2 v[50:51], v56, s[6:7]
	s_mov_b64 exec, s[36:37]
	s_sub_u32 s40, s31, s38
	ds_read_b128 v[56:59], v5 offset:0
	ds_read_b128 v[60:63], v5 offset:16
	ds_read_b128 v[64:67], v5 offset:32
	ds_read_b128 v[68:71], v5 offset:48
	s_waitcnt lgkmcnt(0)
	v_lshl_or_b32 v104, v56, 8, v2
	global_load_dwordx4 v[72:75], v104, s[8:9]
	v_lshl_or_b32 v104, v58, 8, v2
	global_load_dwordx4 v[76:79], v104, s[8:9]
	v_lshl_or_b32 v104, v60, 8, v2
	global_load_dwordx4 v[80:83], v104, s[8:9]
	v_lshl_or_b32 v104, v62, 8, v2
	global_load_dwordx4 v[84:87], v104, s[8:9]
	v_lshl_or_b32 v104, v64, 8, v2
	global_load_dwordx4 v[88:91], v104, s[8:9]
	v_lshl_or_b32 v104, v66, 8, v2
	global_load_dwordx4 v[92:95], v104, s[8:9]
	v_lshl_or_b32 v104, v68, 8, v2
	global_load_dwordx4 v[96:99], v104, s[8:9]
	v_lshl_or_b32 v104, v70, 8, v2
	global_load_dwordx4 v[100:103], v104, s[8:9]
	s_waitcnt vmcnt(7)
	v_fma_mix_f32 v16, v57, v72, v16 op_sel_hi:[0,1,0]
	v_fma_mix_f32 v17, v57, v72, v17 op_sel:[0,1,0] op_sel_hi:[0,1,0]
	v_fma_mix_f32 v18, v57, v73, v18 op_sel_hi:[0,1,0]
	v_fma_mix_f32 v19, v57, v73, v19 op_sel:[0,1,0] op_sel_hi:[0,1,0]
	v_fma_mix_f32 v20, v57, v74, v20 op_sel_hi:[0,1,0]
	v_fma_mix_f32 v21, v57, v74, v21 op_sel:[0,1,0] op_sel_hi:[0,1,0]
	v_fma_mix_f32 v22, v57, v75, v22 op_sel_hi:[0,1,0]
	v_fma_mix_f32 v23, v57, v75, v23 op_sel:[0,1,0] op_sel_hi:[0,1,0]
	s_waitcnt vmcnt(6)
	v_fma_mix_f32 v16, v59, v76, v16 op_sel_hi:[0,1,0]
	v_fma_mix_f32 v17, v59, v76, v17 op_sel:[0,1,0] op_sel_hi:[0,1,0]
	v_fma_mix_f32 v18, v59, v77, v18 op_sel_hi:[0,1,0]
	v_fma_mix_f32 v19, v59, v77, v19 op_sel:[0,1,0] op_sel_hi:[0,1,0]
	v_fma_mix_f32 v20, v59, v78, v20 op_sel_hi:[0,1,0]
	v_fma_mix_f32 v21, v59, v78, v21 op_sel:[0,1,0] op_sel_hi:[0,1,0]
	v_fma_mix_f32 v22, v59, v79, v22 op_sel_hi:[0,1,0]
	v_fma_mix_f32 v23, v59, v79, v23 op_sel:[0,1,0] op_sel_hi:[0,1,0]
	s_waitcnt vmcnt(5)
	v_fma_mix_f32 v16, v61, v80, v16 op_sel_hi:[0,1,0]
	v_fma_mix_f32 v17, v61, v80, v17 op_sel:[0,1,0] op_sel_hi:[0,1,0]
	v_fma_mix_f32 v18, v61, v81, v18 op_sel_hi:[0,1,0]
	v_fma_mix_f32 v19, v61, v81, v19 op_sel:[0,1,0] op_sel_hi:[0,1,0]
	v_fma_mix_f32 v20, v61, v82, v20 op_sel_hi:[0,1,0]
	v_fma_mix_f32 v21, v61, v82, v21 op_sel:[0,1,0] op_sel_hi:[0,1,0]
	v_fma_mix_f32 v22, v61, v83, v22 op_sel_hi:[0,1,0]
	v_fma_mix_f32 v23, v61, v83, v23 op_sel:[0,1,0] op_sel_hi:[0,1,0]
	s_waitcnt vmcnt(4)
	v_fma_mix_f32 v16, v63, v84, v16 op_sel_hi:[0,1,0]
	v_fma_mix_f32 v17, v63, v84, v17 op_sel:[0,1,0] op_sel_hi:[0,1,0]
	v_fma_mix_f32 v18, v63, v85, v18 op_sel_hi:[0,1,0]
	v_fma_mix_f32 v19, v63, v85, v19 op_sel:[0,1,0] op_sel_hi:[0,1,0]
	v_fma_mix_f32 v20, v63, v86, v20 op_sel_hi:[0,1,0]
	v_fma_mix_f32 v21, v63, v86, v21 op_sel:[0,1,0] op_sel_hi:[0,1,0]
	v_fma_mix_f32 v22, v63, v87, v22 op_sel_hi:[0,1,0]
	v_fma_mix_f32 v23, v63, v87, v23 op_sel:[0,1,0] op_sel_hi:[0,1,0]
	s_waitcnt vmcnt(3)
	v_fma_mix_f32 v16, v65, v88, v16 op_sel_hi:[0,1,0]
	v_fma_mix_f32 v17, v65, v88, v17 op_sel:[0,1,0] op_sel_hi:[0,1,0]
	v_fma_mix_f32 v18, v65, v89, v18 op_sel_hi:[0,1,0]
	v_fma_mix_f32 v19, v65, v89, v19 op_sel:[0,1,0] op_sel_hi:[0,1,0]
	v_fma_mix_f32 v20, v65, v90, v20 op_sel_hi:[0,1,0]
	v_fma_mix_f32 v21, v65, v90, v21 op_sel:[0,1,0] op_sel_hi:[0,1,0]
	v_fma_mix_f32 v22, v65, v91, v22 op_sel_hi:[0,1,0]
	v_fma_mix_f32 v23, v65, v91, v23 op_sel:[0,1,0] op_sel_hi:[0,1,0]
	s_waitcnt vmcnt(2)
	v_fma_mix_f32 v16, v67, v92, v16 op_sel_hi:[0,1,0]
	v_fma_mix_f32 v17, v67, v92, v17 op_sel:[0,1,0] op_sel_hi:[0,1,0]
	v_fma_mix_f32 v18, v67, v93, v18 op_sel_hi:[0,1,0]
	v_fma_mix_f32 v19, v67, v93, v19 op_sel:[0,1,0] op_sel_hi:[0,1,0]
	v_fma_mix_f32 v20, v67, v94, v20 op_sel_hi:[0,1,0]
	v_fma_mix_f32 v21, v67, v94, v21 op_sel:[0,1,0] op_sel_hi:[0,1,0]
	v_fma_mix_f32 v22, v67, v95, v22 op_sel_hi:[0,1,0]
	v_fma_mix_f32 v23, v67, v95, v23 op_sel:[0,1,0] op_sel_hi:[0,1,0]
	s_waitcnt vmcnt(1)
	v_fma_mix_f32 v16, v69, v96, v16 op_sel_hi:[0,1,0]
	v_fma_mix_f32 v17, v69, v96, v17 op_sel:[0,1,0] op_sel_hi:[0,1,0]
	v_fma_mix_f32 v18, v69, v97, v18 op_sel_hi:[0,1,0]
	v_fma_mix_f32 v19, v69, v97, v19 op_sel:[0,1,0] op_sel_hi:[0,1,0]
	v_fma_mix_f32 v20, v69, v98, v20 op_sel_hi:[0,1,0]
	v_fma_mix_f32 v21, v69, v98, v21 op_sel:[0,1,0] op_sel_hi:[0,1,0]
	v_fma_mix_f32 v22, v69, v99, v22 op_sel_hi:[0,1,0]
	v_fma_mix_f32 v23, v69, v99, v23 op_sel:[0,1,0] op_sel_hi:[0,1,0]
	s_waitcnt vmcnt(0)
	v_fma_mix_f32 v16, v71, v100, v16 op_sel_hi:[0,1,0]
	v_fma_mix_f32 v17, v71, v100, v17 op_sel:[0,1,0] op_sel_hi:[0,1,0]
	v_fma_mix_f32 v18, v71, v101, v18 op_sel_hi:[0,1,0]
	v_fma_mix_f32 v19, v71, v101, v19 op_sel:[0,1,0] op_sel_hi:[0,1,0]
	v_fma_mix_f32 v20, v71, v102, v20 op_sel_hi:[0,1,0]
	v_fma_mix_f32 v21, v71, v102, v21 op_sel:[0,1,0] op_sel_hi:[0,1,0]
	v_fma_mix_f32 v22, v71, v103, v22 op_sel_hi:[0,1,0]
	v_fma_mix_f32 v23, v71, v103, v23 op_sel:[0,1,0] op_sel_hi:[0,1,0]
	s_cmp_le_u32 s40, 8
	s_cbranch_scc1 .Lsw_skip1
	ds_read_b128 v[56:59], v5 offset:64
	ds_read_b128 v[60:63], v5 offset:80
	ds_read_b128 v[64:67], v5 offset:96
	ds_read_b128 v[68:71], v5 offset:112
	s_waitcnt lgkmcnt(0)
	v_lshl_or_b32 v104, v56, 8, v2
	global_load_dwordx4 v[72:75], v104, s[8:9]
	v_lshl_or_b32 v104, v58, 8, v2
	global_load_dwordx4 v[76:79], v104, s[8:9]
	v_lshl_or_b32 v104, v60, 8, v2
	global_load_dwordx4 v[80:83], v104, s[8:9]
	v_lshl_or_b32 v104, v62, 8, v2
	global_load_dwordx4 v[84:87], v104, s[8:9]
	v_lshl_or_b32 v104, v64, 8, v2
	global_load_dwordx4 v[88:91], v104, s[8:9]
	v_lshl_or_b32 v104, v66, 8, v2
	global_load_dwordx4 v[92:95], v104, s[8:9]
	v_lshl_or_b32 v104, v68, 8, v2
	global_load_dwordx4 v[96:99], v104, s[8:9]
	v_lshl_or_b32 v104, v70, 8, v2
	global_load_dwordx4 v[100:103], v104, s[8:9]
	s_waitcnt vmcnt(7)
	v_fma_mix_f32 v16, v57, v72, v16 op_sel_hi:[0,1,0]
	v_fma_mix_f32 v17, v57, v72, v17 op_sel:[0,1,0] op_sel_hi:[0,1,0]
	v_fma_mix_f32 v18, v57, v73, v18 op_sel_hi:[0,1,0]
	v_fma_mix_f32 v19, v57, v73, v19 op_sel:[0,1,0] op_sel_hi:[0,1,0]
	v_fma_mix_f32 v20, v57, v74, v20 op_sel_hi:[0,1,0]
	v_fma_mix_f32 v21, v57, v74, v21 op_sel:[0,1,0] op_sel_hi:[0,1,0]
	v_fma_mix_f32 v22, v57, v75, v22 op_sel_hi:[0,1,0]
	v_fma_mix_f32 v23, v57, v75, v23 op_sel:[0,1,0] op_sel_hi:[0,1,0]
	s_waitcnt vmcnt(6)
	v_fma_mix_f32 v16, v59, v76, v16 op_sel_hi:[0,1,0]
	v_fma_mix_f32 v17, v59, v76, v17 op_sel:[0,1,0] op_sel_hi:[0,1,0]
	v_fma_mix_f32 v18, v59, v77, v18 op_sel_hi:[0,1,0]
	v_fma_mix_f32 v19, v59, v77, v19 op_sel:[0,1,0] op_sel_hi:[0,1,0]
	v_fma_mix_f32 v20, v59, v78, v20 op_sel_hi:[0,1,0]
	v_fma_mix_f32 v21, v59, v78, v21 op_sel:[0,1,0] op_sel_hi:[0,1,0]
	v_fma_mix_f32 v22, v59, v79, v22 op_sel_hi:[0,1,0]
	v_fma_mix_f32 v23, v59, v79, v23 op_sel:[0,1,0] op_sel_hi:[0,1,0]
	s_waitcnt vmcnt(5)
	v_fma_mix_f32 v16, v61, v80, v16 op_sel_hi:[0,1,0]
	v_fma_mix_f32 v17, v61, v80, v17 op_sel:[0,1,0] op_sel_hi:[0,1,0]
	v_fma_mix_f32 v18, v61, v81, v18 op_sel_hi:[0,1,0]
	v_fma_mix_f32 v19, v61, v81, v19 op_sel:[0,1,0] op_sel_hi:[0,1,0]
	v_fma_mix_f32 v20, v61, v82, v20 op_sel_hi:[0,1,0]
	v_fma_mix_f32 v21, v61, v82, v21 op_sel:[0,1,0] op_sel_hi:[0,1,0]
	v_fma_mix_f32 v22, v61, v83, v22 op_sel_hi:[0,1,0]
	v_fma_mix_f32 v23, v61, v83, v23 op_sel:[0,1,0] op_sel_hi:[0,1,0]
	s_waitcnt vmcnt(4)
	v_fma_mix_f32 v16, v63, v84, v16 op_sel_hi:[0,1,0]
	v_fma_mix_f32 v17, v63, v84, v17 op_sel:[0,1,0] op_sel_hi:[0,1,0]
	v_fma_mix_f32 v18, v63, v85, v18 op_sel_hi:[0,1,0]
	v_fma_mix_f32 v19, v63, v85, v19 op_sel:[0,1,0] op_sel_hi:[0,1,0]
	v_fma_mix_f32 v20, v63, v86, v20 op_sel_hi:[0,1,0]
	v_fma_mix_f32 v21, v63, v86, v21 op_sel:[0,1,0] op_sel_hi:[0,1,0]
	v_fma_mix_f32 v22, v63, v87, v22 op_sel_hi:[0,1,0]
	v_fma_mix_f32 v23, v63, v87, v23 op_sel:[0,1,0] op_sel_hi:[0,1,0]
	s_waitcnt vmcnt(3)
	v_fma_mix_f32 v16, v65, v88, v16 op_sel_hi:[0,1,0]
	v_fma_mix_f32 v17, v65, v88, v17 op_sel:[0,1,0] op_sel_hi:[0,1,0]
	v_fma_mix_f32 v18, v65, v89, v18 op_sel_hi:[0,1,0]
	v_fma_mix_f32 v19, v65, v89, v19 op_sel:[0,1,0] op_sel_hi:[0,1,0]
	v_fma_mix_f32 v20, v65, v90, v20 op_sel_hi:[0,1,0]
	v_fma_mix_f32 v21, v65, v90, v21 op_sel:[0,1,0] op_sel_hi:[0,1,0]
	v_fma_mix_f32 v22, v65, v91, v22 op_sel_hi:[0,1,0]
	v_fma_mix_f32 v23, v65, v91, v23 op_sel:[0,1,0] op_sel_hi:[0,1,0]
	s_waitcnt vmcnt(2)
	v_fma_mix_f32 v16, v67, v92, v16 op_sel_hi:[0,1,0]
	v_fma_mix_f32 v17, v67, v92, v17 op_sel:[0,1,0] op_sel_hi:[0,1,0]
	v_fma_mix_f32 v18, v67, v93, v18 op_sel_hi:[0,1,0]
	v_fma_mix_f32 v19, v67, v93, v19 op_sel:[0,1,0] op_sel_hi:[0,1,0]
	v_fma_mix_f32 v20, v67, v94, v20 op_sel_hi:[0,1,0]
	v_fma_mix_f32 v21, v67, v94, v21 op_sel:[0,1,0] op_sel_hi:[0,1,0]
	v_fma_mix_f32 v22, v67, v95, v22 op_sel_hi:[0,1,0]
	v_fma_mix_f32 v23, v67, v95, v23 op_sel:[0,1,0] op_sel_hi:[0,1,0]
	s_waitcnt vmcnt(1)
	v_fma_mix_f32 v16, v69, v96, v16 op_sel_hi:[0,1,0]
	v_fma_mix_f32 v17, v69, v96, v17 op_sel:[0,1,0] op_sel_hi:[0,1,0]
	v_fma_mix_f32 v18, v69, v97, v18 op_sel_hi:[0,1,0]
	v_fma_mix_f32 v19, v69, v97, v19 op_sel:[0,1,0] op_sel_hi:[0,1,0]
	v_fma_mix_f32 v20, v69, v98, v20 op_sel_hi:[0,1,0]
	v_fma_mix_f32 v21, v69, v98, v21 op_sel:[0,1,0] op_sel_hi:[0,1,0]
	v_fma_mix_f32 v22, v69, v99, v22 op_sel_hi:[0,1,0]
	v_fma_mix_f32 v23, v69, v99, v23 op_sel:[0,1,0] op_sel_hi:[0,1,0]
	s_waitcnt vmcnt(0)
	v_fma_mix_f32 v16, v71, v100, v16 op_sel_hi:[0,1,0]
	v_fma_mix_f32 v17, v71, v100, v17 op_sel:[0,1,0] op_sel_hi:[0,1,0]
	v_fma_mix_f32 v18, v71, v101, v18 op_sel_hi:[0,1,0]
	v_fma_mix_f32 v19, v71, v101, v19 op_sel:[0,1,0] op_sel_hi:[0,1,0]
	v_fma_mix_f32 v20, v71, v102, v20 op_sel_hi:[0,1,0]
	v_fma_mix_f32 v21, v71, v102, v21 op_sel:[0,1,0] op_sel_hi:[0,1,0]
	v_fma_mix_f32 v22, v71, v103, v22 op_sel_hi:[0,1,0]
	v_fma_mix_f32 v23, v71, v103, v23 op_sel:[0,1,0] op_sel_hi:[0,1,0]
.Lsw_skip1:
	s_cmp_ge_u32 s38, s32
	s_cbranch_scc1 .Lsw_skip2
	s_waitcnt vmcnt(0)
	v_lshrrev_b32_e32 v56, 5, v52
	v_lshlrev_b32_e32 v56, 2, v56
	ds_read_b32 v57, v56
	v_mov_b32_e32 v58, v52
	s_waitcnt lgkmcnt(0)
	v_mul_f32_e32 v59, v53, v57
	ds_write_b64 v4, v[58:59]
	v_add_u32_e32 v56, s39, v1
	v_cmp_lt_u32_e32 vcc, v56, v46
	v_add_u32_e32 v56, v56, v42
	v_lshlrev_b32_e32 v56, 3, v56
	v_mov_b32_e32 v52, 0
	v_mov_b32_e32 v53, 0
	s_and_saveexec_b64 s[36:37], vcc
	global_load_dwordx2 v[52:53], v56, s[6:7]
	s_mov_b64 exec, s[36:37]
	s_sub_u32 s40, s32, s38
	ds_read_b128 v[56:59], v5 offset:0
	ds_read_b128 v[60:63], v5 offset:16
	ds_read_b128 v[64:67], v5 offset:32
	ds_read_b128 v[68:71], v5 offset:48
	s_waitcnt lgkmcnt(0)
	v_lshl_or_b32 v104, v56, 8, v2
	global_load_dwordx4 v[72:75], v104, s[8:9]
	v_lshl_or_b32 v104, v58, 8, v2
	global_load_dwordx4 v[76:79], v104, s[8:9]
	v_lshl_or_b32 v104, v60, 8, v2
	global_load_dwordx4 v[80:83], v104, s[8:9]
	v_lshl_or_b32 v104, v62, 8, v2
	global_load_dwordx4 v[84:87], v104, s[8:9]
	v_lshl_or_b32 v104, v64, 8, v2
	global_load_dwordx4 v[88:91], v104, s[8:9]
	v_lshl_or_b32 v104, v66, 8, v2
	global_load_dwordx4 v[92:95], v104, s[8:9]
	v_lshl_or_b32 v104, v68, 8, v2
	global_load_dwordx4 v[96:99], v104, s[8:9]
	v_lshl_or_b32 v104, v70, 8, v2
	global_load_dwordx4 v[100:103], v104, s[8:9]
	s_waitcnt vmcnt(7)
	v_fma_mix_f32 v24, v57, v72, v24 op_sel_hi:[0,1,0]
	v_fma_mix_f32 v25, v57, v72, v25 op_sel:[0,1,0] op_sel_hi:[0,1,0]
	v_fma_mix_f32 v26, v57, v73, v26 op_sel_hi:[0,1,0]
	v_fma_mix_f32 v27, v57, v73, v27 op_sel:[0,1,0] op_sel_hi:[0,1,0]
	v_fma_mix_f32 v28, v57, v74, v28 op_sel_hi:[0,1,0]
	v_fma_mix_f32 v29, v57, v74, v29 op_sel:[0,1,0] op_sel_hi:[0,1,0]
	v_fma_mix_f32 v30, v57, v75, v30 op_sel_hi:[0,1,0]
	v_fma_mix_f32 v31, v57, v75, v31 op_sel:[0,1,0] op_sel_hi:[0,1,0]
	s_waitcnt vmcnt(6)
	v_fma_mix_f32 v24, v59, v76, v24 op_sel_hi:[0,1,0]
	v_fma_mix_f32 v25, v59, v76, v25 op_sel:[0,1,0] op_sel_hi:[0,1,0]
	v_fma_mix_f32 v26, v59, v77, v26 op_sel_hi:[0,1,0]
	v_fma_mix_f32 v27, v59, v77, v27 op_sel:[0,1,0] op_sel_hi:[0,1,0]
	v_fma_mix_f32 v28, v59, v78, v28 op_sel_hi:[0,1,0]
	v_fma_mix_f32 v29, v59, v78, v29 op_sel:[0,1,0] op_sel_hi:[0,1,0]
	v_fma_mix_f32 v30, v59, v79, v30 op_sel_hi:[0,1,0]
	v_fma_mix_f32 v31, v59, v79, v31 op_sel:[0,1,0] op_sel_hi:[0,1,0]
	s_waitcnt vmcnt(5)
	v_fma_mix_f32 v24, v61, v80, v24 op_sel_hi:[0,1,0]
	v_fma_mix_f32 v25, v61, v80, v25 op_sel:[0,1,0] op_sel_hi:[0,1,0]
	v_fma_mix_f32 v26, v61, v81, v26 op_sel_hi:[0,1,0]
	v_fma_mix_f32 v27, v61, v81, v27 op_sel:[0,1,0] op_sel_hi:[0,1,0]
	v_fma_mix_f32 v28, v61, v82, v28 op_sel_hi:[0,1,0]
	v_fma_mix_f32 v29, v61, v82, v29 op_sel:[0,1,0] op_sel_hi:[0,1,0]
	v_fma_mix_f32 v30, v61, v83, v30 op_sel_hi:[0,1,0]
	v_fma_mix_f32 v31, v61, v83, v31 op_sel:[0,1,0] op_sel_hi:[0,1,0]
	s_waitcnt vmcnt(4)
	v_fma_mix_f32 v24, v63, v84, v24 op_sel_hi:[0,1,0]
	v_fma_mix_f32 v25, v63, v84, v25 op_sel:[0,1,0] op_sel_hi:[0,1,0]
	v_fma_mix_f32 v26, v63, v85, v26 op_sel_hi:[0,1,0]
	v_fma_mix_f32 v27, v63, v85, v27 op_sel:[0,1,0] op_sel_hi:[0,1,0]
	v_fma_mix_f32 v28, v63, v86, v28 op_sel_hi:[0,1,0]
	v_fma_mix_f32 v29, v63, v86, v29 op_sel:[0,1,0] op_sel_hi:[0,1,0]
	v_fma_mix_f32 v30, v63, v87, v30 op_sel_hi:[0,1,0]
	v_fma_mix_f32 v31, v63, v87, v31 op_sel:[0,1,0] op_sel_hi:[0,1,0]
	s_waitcnt vmcnt(3)
	v_fma_mix_f32 v24, v65, v88, v24 op_sel_hi:[0,1,0]
	v_fma_mix_f32 v25, v65, v88, v25 op_sel:[0,1,0] op_sel_hi:[0,1,0]
	v_fma_mix_f32 v26, v65, v89, v26 op_sel_hi:[0,1,0]
	v_fma_mix_f32 v27, v65, v89, v27 op_sel:[0,1,0] op_sel_hi:[0,1,0]
	v_fma_mix_f32 v28, v65, v90, v28 op_sel_hi:[0,1,0]
	v_fma_mix_f32 v29, v65, v90, v29 op_sel:[0,1,0] op_sel_hi:[0,1,0]
	v_fma_mix_f32 v30, v65, v91, v30 op_sel_hi:[0,1,0]
	v_fma_mix_f32 v31, v65, v91, v31 op_sel:[0,1,0] op_sel_hi:[0,1,0]
	s_waitcnt vmcnt(2)
	v_fma_mix_f32 v24, v67, v92, v24 op_sel_hi:[0,1,0]
	v_fma_mix_f32 v25, v67, v92, v25 op_sel:[0,1,0] op_sel_hi:[0,1,0]
	v_fma_mix_f32 v26, v67, v93, v26 op_sel_hi:[0,1,0]
	v_fma_mix_f32 v27, v67, v93, v27 op_sel:[0,1,0] op_sel_hi:[0,1,0]
	v_fma_mix_f32 v28, v67, v94, v28 op_sel_hi:[0,1,0]
	v_fma_mix_f32 v29, v67, v94, v29 op_sel:[0,1,0] op_sel_hi:[0,1,0]
	v_fma_mix_f32 v30, v67, v95, v30 op_sel_hi:[0,1,0]
	v_fma_mix_f32 v31, v67, v95, v31 op_sel:[0,1,0] op_sel_hi:[0,1,0]
	s_waitcnt vmcnt(1)
	v_fma_mix_f32 v24, v69, v96, v24 op_sel_hi:[0,1,0]
	v_fma_mix_f32 v25, v69, v96, v25 op_sel:[0,1,0] op_sel_hi:[0,1,0]
	v_fma_mix_f32 v26, v69, v97, v26 op_sel_hi:[0,1,0]
	v_fma_mix_f32 v27, v69, v97, v27 op_sel:[0,1,0] op_sel_hi:[0,1,0]
	v_fma_mix_f32 v28, v69, v98, v28 op_sel_hi:[0,1,0]
	v_fma_mix_f32 v29, v69, v98, v29 op_sel:[0,1,0] op_sel_hi:[0,1,0]
	v_fma_mix_f32 v30, v69, v99, v30 op_sel_hi:[0,1,0]
	v_fma_mix_f32 v31, v69, v99, v31 op_sel:[0,1,0] op_sel_hi:[0,1,0]
	s_waitcnt vmcnt(0)
	v_fma_mix_f32 v24, v71, v100, v24 op_sel_hi:[0,1,0]
	v_fma_mix_f32 v25, v71, v100, v25 op_sel:[0,1,0] op_sel_hi:[0,1,0]
	v_fma_mix_f32 v26, v71, v101, v26 op_sel_hi:[0,1,0]
	v_fma_mix_f32 v27, v71, v101, v27 op_sel:[0,1,0] op_sel_hi:[0,1,0]
	v_fma_mix_f32 v28, v71, v102, v28 op_sel_hi:[0,1,0]
	v_fma_mix_f32 v29, v71, v102, v29 op_sel:[0,1,0] op_sel_hi:[0,1,0]
	v_fma_mix_f32 v30, v71, v103, v30 op_sel_hi:[0,1,0]
	v_fma_mix_f32 v31, v71, v103, v31 op_sel:[0,1,0] op_sel_hi:[0,1,0]
	s_cmp_le_u32 s40, 8
	s_cbranch_scc1 .Lsw_skip2
	ds_read_b128 v[56:59], v5 offset:64
	ds_read_b128 v[60:63], v5 offset:80
	ds_read_b128 v[64:67], v5 offset:96
	ds_read_b128 v[68:71], v5 offset:112
	s_waitcnt lgkmcnt(0)
	v_lshl_or_b32 v104, v56, 8, v2
	global_load_dwordx4 v[72:75], v104, s[8:9]
	v_lshl_or_b32 v104, v58, 8, v2
	global_load_dwordx4 v[76:79], v104, s[8:9]
	v_lshl_or_b32 v104, v60, 8, v2
	global_load_dwordx4 v[80:83], v104, s[8:9]
	v_lshl_or_b32 v104, v62, 8, v2
	global_load_dwordx4 v[84:87], v104, s[8:9]
	v_lshl_or_b32 v104, v64, 8, v2
	global_load_dwordx4 v[88:91], v104, s[8:9]
	v_lshl_or_b32 v104, v66, 8, v2
	global_load_dwordx4 v[92:95], v104, s[8:9]
	v_lshl_or_b32 v104, v68, 8, v2
	global_load_dwordx4 v[96:99], v104, s[8:9]
	v_lshl_or_b32 v104, v70, 8, v2
	global_load_dwordx4 v[100:103], v104, s[8:9]
	s_waitcnt vmcnt(7)
	v_fma_mix_f32 v24, v57, v72, v24 op_sel_hi:[0,1,0]
	v_fma_mix_f32 v25, v57, v72, v25 op_sel:[0,1,0] op_sel_hi:[0,1,0]
	v_fma_mix_f32 v26, v57, v73, v26 op_sel_hi:[0,1,0]
	v_fma_mix_f32 v27, v57, v73, v27 op_sel:[0,1,0] op_sel_hi:[0,1,0]
	v_fma_mix_f32 v28, v57, v74, v28 op_sel_hi:[0,1,0]
	v_fma_mix_f32 v29, v57, v74, v29 op_sel:[0,1,0] op_sel_hi:[0,1,0]
	v_fma_mix_f32 v30, v57, v75, v30 op_sel_hi:[0,1,0]
	v_fma_mix_f32 v31, v57, v75, v31 op_sel:[0,1,0] op_sel_hi:[0,1,0]
	s_waitcnt vmcnt(6)
	v_fma_mix_f32 v24, v59, v76, v24 op_sel_hi:[0,1,0]
	v_fma_mix_f32 v25, v59, v76, v25 op_sel:[0,1,0] op_sel_hi:[0,1,0]
	v_fma_mix_f32 v26, v59, v77, v26 op_sel_hi:[0,1,0]
	v_fma_mix_f32 v27, v59, v77, v27 op_sel:[0,1,0] op_sel_hi:[0,1,0]
	v_fma_mix_f32 v28, v59, v78, v28 op_sel_hi:[0,1,0]
	v_fma_mix_f32 v29, v59, v78, v29 op_sel:[0,1,0] op_sel_hi:[0,1,0]
	v_fma_mix_f32 v30, v59, v79, v30 op_sel_hi:[0,1,0]
	v_fma_mix_f32 v31, v59, v79, v31 op_sel:[0,1,0] op_sel_hi:[0,1,0]
	s_waitcnt vmcnt(5)
	v_fma_mix_f32 v24, v61, v80, v24 op_sel_hi:[0,1,0]
	v_fma_mix_f32 v25, v61, v80, v25 op_sel:[0,1,0] op_sel_hi:[0,1,0]
	v_fma_mix_f32 v26, v61, v81, v26 op_sel_hi:[0,1,0]
	v_fma_mix_f32 v27, v61, v81, v27 op_sel:[0,1,0] op_sel_hi:[0,1,0]
	v_fma_mix_f32 v28, v61, v82, v28 op_sel_hi:[0,1,0]
	v_fma_mix_f32 v29, v61, v82, v29 op_sel:[0,1,0] op_sel_hi:[0,1,0]
	v_fma_mix_f32 v30, v61, v83, v30 op_sel_hi:[0,1,0]
	v_fma_mix_f32 v31, v61, v83, v31 op_sel:[0,1,0] op_sel_hi:[0,1,0]
	s_waitcnt vmcnt(4)
	v_fma_mix_f32 v24, v63, v84, v24 op_sel_hi:[0,1,0]
	v_fma_mix_f32 v25, v63, v84, v25 op_sel:[0,1,0] op_sel_hi:[0,1,0]
	v_fma_mix_f32 v26, v63, v85, v26 op_sel_hi:[0,1,0]
	v_fma_mix_f32 v27, v63, v85, v27 op_sel:[0,1,0] op_sel_hi:[0,1,0]
	v_fma_mix_f32 v28, v63, v86, v28 op_sel_hi:[0,1,0]
	v_fma_mix_f32 v29, v63, v86, v29 op_sel:[0,1,0] op_sel_hi:[0,1,0]
	v_fma_mix_f32 v30, v63, v87, v30 op_sel_hi:[0,1,0]
	v_fma_mix_f32 v31, v63, v87, v31 op_sel:[0,1,0] op_sel_hi:[0,1,0]
	s_waitcnt vmcnt(3)
	v_fma_mix_f32 v24, v65, v88, v24 op_sel_hi:[0,1,0]
	v_fma_mix_f32 v25, v65, v88, v25 op_sel:[0,1,0] op_sel_hi:[0,1,0]
	v_fma_mix_f32 v26, v65, v89, v26 op_sel_hi:[0,1,0]
	v_fma_mix_f32 v27, v65, v89, v27 op_sel:[0,1,0] op_sel_hi:[0,1,0]
	v_fma_mix_f32 v28, v65, v90, v28 op_sel_hi:[0,1,0]
	v_fma_mix_f32 v29, v65, v90, v29 op_sel:[0,1,0] op_sel_hi:[0,1,0]
	v_fma_mix_f32 v30, v65, v91, v30 op_sel_hi:[0,1,0]
	v_fma_mix_f32 v31, v65, v91, v31 op_sel:[0,1,0] op_sel_hi:[0,1,0]
	s_waitcnt vmcnt(2)
	v_fma_mix_f32 v24, v67, v92, v24 op_sel_hi:[0,1,0]
	v_fma_mix_f32 v25, v67, v92, v25 op_sel:[0,1,0] op_sel_hi:[0,1,0]
	v_fma_mix_f32 v26, v67, v93, v26 op_sel_hi:[0,1,0]
	v_fma_mix_f32 v27, v67, v93, v27 op_sel:[0,1,0] op_sel_hi:[0,1,0]
	v_fma_mix_f32 v28, v67, v94, v28 op_sel_hi:[0,1,0]
	v_fma_mix_f32 v29, v67, v94, v29 op_sel:[0,1,0] op_sel_hi:[0,1,0]
	v_fma_mix_f32 v30, v67, v95, v30 op_sel_hi:[0,1,0]
	v_fma_mix_f32 v31, v67, v95, v31 op_sel:[0,1,0] op_sel_hi:[0,1,0]
	s_waitcnt vmcnt(1)
	v_fma_mix_f32 v24, v69, v96, v24 op_sel_hi:[0,1,0]
	v_fma_mix_f32 v25, v69, v96, v25 op_sel:[0,1,0] op_sel_hi:[0,1,0]
	v_fma_mix_f32 v26, v69, v97, v26 op_sel_hi:[0,1,0]
	v_fma_mix_f32 v27, v69, v97, v27 op_sel:[0,1,0] op_sel_hi:[0,1,0]
	v_fma_mix_f32 v28, v69, v98, v28 op_sel_hi:[0,1,0]
	v_fma_mix_f32 v29, v69, v98, v29 op_sel:[0,1,0] op_sel_hi:[0,1,0]
	v_fma_mix_f32 v30, v69, v99, v30 op_sel_hi:[0,1,0]
	v_fma_mix_f32 v31, v69, v99, v31 op_sel:[0,1,0] op_sel_hi:[0,1,0]
	s_waitcnt vmcnt(0)
	v_fma_mix_f32 v24, v71, v100, v24 op_sel_hi:[0,1,0]
	v_fma_mix_f32 v25, v71, v100, v25 op_sel:[0,1,0] op_sel_hi:[0,1,0]
	v_fma_mix_f32 v26, v71, v101, v26 op_sel_hi:[0,1,0]
	v_fma_mix_f32 v27, v71, v101, v27 op_sel:[0,1,0] op_sel_hi:[0,1,0]
	v_fma_mix_f32 v28, v71, v102, v28 op_sel_hi:[0,1,0]
	v_fma_mix_f32 v29, v71, v102, v29 op_sel:[0,1,0] op_sel_hi:[0,1,0]
	v_fma_mix_f32 v30, v71, v103, v30 op_sel_hi:[0,1,0]
	v_fma_mix_f32 v31, v71, v103, v31 op_sel:[0,1,0] op_sel_hi:[0,1,0]
.Lsw_skip2:
	s_cmp_ge_u32 s38, s33
	s_cbranch_scc1 .Lsw_skip3
	s_waitcnt vmcnt(0)
	v_lshrrev_b32_e32 v56, 5, v54
	v_lshlrev_b32_e32 v56, 2, v56
	ds_read_b32 v57, v56
	v_mov_b32_e32 v58, v54
	s_waitcnt lgkmcnt(0)
	v_mul_f32_e32 v59, v55, v57
	ds_write_b64 v4, v[58:59]
	v_add_u32_e32 v56, s39, v1
	v_cmp_lt_u32_e32 vcc, v56, v47
	v_add_u32_e32 v56, v56, v43
	v_lshlrev_b32_e32 v56, 3, v56
	v_mov_b32_e32 v54, 0
	v_mov_b32_e32 v55, 0
	s_and_saveexec_b64 s[36:37], vcc
	global_load_dwordx2 v[54:55], v56, s[6:7]
	s_mov_b64 exec, s[36:37]
	s_sub_u32 s40, s33, s38
	ds_read_b128 v[56:59], v5 offset:0
	ds_read_b128 v[60:63], v5 offset:16
	ds_read_b128 v[64:67], v5 offset:32
	ds_read_b128 v[68:71], v5 offset:48
	s_waitcnt lgkmcnt(0)
	v_lshl_or_b32 v104, v56, 8, v2
	global_load_dwordx4 v[72:75], v104, s[8:9]
	v_lshl_or_b32 v104, v58, 8, v2
	global_load_dwordx4 v[76:79], v104, s[8:9]
	v_lshl_or_b32 v104, v60, 8, v2
	global_load_dwordx4 v[80:83], v104, s[8:9]
	v_lshl_or_b32 v104, v62, 8, v2
	global_load_dwordx4 v[84:87], v104, s[8:9]
	v_lshl_or_b32 v104, v64, 8, v2
	global_load_dwordx4 v[88:91], v104, s[8:9]
	v_lshl_or_b32 v104, v66, 8, v2
	global_load_dwordx4 v[92:95], v104, s[8:9]
	v_lshl_or_b32 v104, v68, 8, v2
	global_load_dwordx4 v[96:99], v104, s[8:9]
	v_lshl_or_b32 v104, v70, 8, v2
	global_load_dwordx4 v[100:103], v104, s[8:9]
	s_waitcnt vmcnt(7)
	v_fma_mix_f32 v32, v57, v72, v32 op_sel_hi:[0,1,0]
	v_fma_mix_f32 v33, v57, v72, v33 op_sel:[0,1,0] op_sel_hi:[0,1,0]
	v_fma_mix_f32 v34, v57, v73, v34 op_sel_hi:[0,1,0]
	v_fma_mix_f32 v35, v57, v73, v35 op_sel:[0,1,0] op_sel_hi:[0,1,0]
	v_fma_mix_f32 v36, v57, v74, v36 op_sel_hi:[0,1,0]
	v_fma_mix_f32 v37, v57, v74, v37 op_sel:[0,1,0] op_sel_hi:[0,1,0]
	v_fma_mix_f32 v38, v57, v75, v38 op_sel_hi:[0,1,0]
	v_fma_mix_f32 v39, v57, v75, v39 op_sel:[0,1,0] op_sel_hi:[0,1,0]
	s_waitcnt vmcnt(6)
	v_fma_mix_f32 v32, v59, v76, v32 op_sel_hi:[0,1,0]
	v_fma_mix_f32 v33, v59, v76, v33 op_sel:[0,1,0] op_sel_hi:[0,1,0]
	v_fma_mix_f32 v34, v59, v77, v34 op_sel_hi:[0,1,0]
	v_fma_mix_f32 v35, v59, v77, v35 op_sel:[0,1,0] op_sel_hi:[0,1,0]
	v_fma_mix_f32 v36, v59, v78, v36 op_sel_hi:[0,1,0]
	v_fma_mix_f32 v37, v59, v78, v37 op_sel:[0,1,0] op_sel_hi:[0,1,0]
	v_fma_mix_f32 v38, v59, v79, v38 op_sel_hi:[0,1,0]
	v_fma_mix_f32 v39, v59, v79, v39 op_sel:[0,1,0] op_sel_hi:[0,1,0]
	s_waitcnt vmcnt(5)
	v_fma_mix_f32 v32, v61, v80, v32 op_sel_hi:[0,1,0]
	v_fma_mix_f32 v33, v61, v80, v33 op_sel:[0,1,0] op_sel_hi:[0,1,0]
	v_fma_mix_f32 v34, v61, v81, v34 op_sel_hi:[0,1,0]
	v_fma_mix_f32 v35, v61, v81, v35 op_sel:[0,1,0] op_sel_hi:[0,1,0]
	v_fma_mix_f32 v36, v61, v82, v36 op_sel_hi:[0,1,0]
	v_fma_mix_f32 v37, v61, v82, v37 op_sel:[0,1,0] op_sel_hi:[0,1,0]
	v_fma_mix_f32 v38, v61, v83, v38 op_sel_hi:[0,1,0]
	v_fma_mix_f32 v39, v61, v83, v39 op_sel:[0,1,0] op_sel_hi:[0,1,0]
	s_waitcnt vmcnt(4)
	v_fma_mix_f32 v32, v63, v84, v32 op_sel_hi:[0,1,0]
	v_fma_mix_f32 v33, v63, v84, v33 op_sel:[0,1,0] op_sel_hi:[0,1,0]
	v_fma_mix_f32 v34, v63, v85, v34 op_sel_hi:[0,1,0]
	v_fma_mix_f32 v35, v63, v85, v35 op_sel:[0,1,0] op_sel_hi:[0,1,0]
	v_fma_mix_f32 v36, v63, v86, v36 op_sel_hi:[0,1,0]
	v_fma_mix_f32 v37, v63, v86, v37 op_sel:[0,1,0] op_sel_hi:[0,1,0]
	v_fma_mix_f32 v38, v63, v87, v38 op_sel_hi:[0,1,0]
	v_fma_mix_f32 v39, v63, v87, v39 op_sel:[0,1,0] op_sel_hi:[0,1,0]
	s_waitcnt vmcnt(3)
	v_fma_mix_f32 v32, v65, v88, v32 op_sel_hi:[0,1,0]
	v_fma_mix_f32 v33, v65, v88, v33 op_sel:[0,1,0] op_sel_hi:[0,1,0]
	v_fma_mix_f32 v34, v65, v89, v34 op_sel_hi:[0,1,0]
	v_fma_mix_f32 v35, v65, v89, v35 op_sel:[0,1,0] op_sel_hi:[0,1,0]
	v_fma_mix_f32 v36, v65, v90, v36 op_sel_hi:[0,1,0]
	v_fma_mix_f32 v37, v65, v90, v37 op_sel:[0,1,0] op_sel_hi:[0,1,0]
	v_fma_mix_f32 v38, v65, v91, v38 op_sel_hi:[0,1,0]
	v_fma_mix_f32 v39, v65, v91, v39 op_sel:[0,1,0] op_sel_hi:[0,1,0]
	s_waitcnt vmcnt(2)
	v_fma_mix_f32 v32, v67, v92, v32 op_sel_hi:[0,1,0]
	v_fma_mix_f32 v33, v67, v92, v33 op_sel:[0,1,0] op_sel_hi:[0,1,0]
	v_fma_mix_f32 v34, v67, v93, v34 op_sel_hi:[0,1,0]
	v_fma_mix_f32 v35, v67, v93, v35 op_sel:[0,1,0] op_sel_hi:[0,1,0]
	v_fma_mix_f32 v36, v67, v94, v36 op_sel_hi:[0,1,0]
	v_fma_mix_f32 v37, v67, v94, v37 op_sel:[0,1,0] op_sel_hi:[0,1,0]
	v_fma_mix_f32 v38, v67, v95, v38 op_sel_hi:[0,1,0]
	v_fma_mix_f32 v39, v67, v95, v39 op_sel:[0,1,0] op_sel_hi:[0,1,0]
	s_waitcnt vmcnt(1)
	v_fma_mix_f32 v32, v69, v96, v32 op_sel_hi:[0,1,0]
	v_fma_mix_f32 v33, v69, v96, v33 op_sel:[0,1,0] op_sel_hi:[0,1,0]
	v_fma_mix_f32 v34, v69, v97, v34 op_sel_hi:[0,1,0]
	v_fma_mix_f32 v35, v69, v97, v35 op_sel:[0,1,0] op_sel_hi:[0,1,0]
	v_fma_mix_f32 v36, v69, v98, v36 op_sel_hi:[0,1,0]
	v_fma_mix_f32 v37, v69, v98, v37 op_sel:[0,1,0] op_sel_hi:[0,1,0]
	v_fma_mix_f32 v38, v69, v99, v38 op_sel_hi:[0,1,0]
	v_fma_mix_f32 v39, v69, v99, v39 op_sel:[0,1,0] op_sel_hi:[0,1,0]
	s_waitcnt vmcnt(0)
	v_fma_mix_f32 v32, v71, v100, v32 op_sel_hi:[0,1,0]
	v_fma_mix_f32 v33, v71, v100, v33 op_sel:[0,1,0] op_sel_hi:[0,1,0]
	v_fma_mix_f32 v34, v71, v101, v34 op_sel_hi:[0,1,0]
	v_fma_mix_f32 v35, v71, v101, v35 op_sel:[0,1,0] op_sel_hi:[0,1,0]
	v_fma_mix_f32 v36, v71, v102, v36 op_sel_hi:[0,1,0]
	v_fma_mix_f32 v37, v71, v102, v37 op_sel:[0,1,0] op_sel_hi:[0,1,0]
	v_fma_mix_f32 v38, v71, v103, v38 op_sel_hi:[0,1,0]
	v_fma_mix_f32 v39, v71, v103, v39 op_sel:[0,1,0] op_sel_hi:[0,1,0]
	s_cmp_le_u32 s40, 8
	s_cbranch_scc1 .Lsw_skip3
	ds_read_b128 v[56:59], v5 offset:64
	ds_read_b128 v[60:63], v5 offset:80
	ds_read_b128 v[64:67], v5 offset:96
	ds_read_b128 v[68:71], v5 offset:112
	s_waitcnt lgkmcnt(0)
	v_lshl_or_b32 v104, v56, 8, v2
	global_load_dwordx4 v[72:75], v104, s[8:9]
	v_lshl_or_b32 v104, v58, 8, v2
	global_load_dwordx4 v[76:79], v104, s[8:9]
	v_lshl_or_b32 v104, v60, 8, v2
	global_load_dwordx4 v[80:83], v104, s[8:9]
	v_lshl_or_b32 v104, v62, 8, v2
	global_load_dwordx4 v[84:87], v104, s[8:9]
	v_lshl_or_b32 v104, v64, 8, v2
	global_load_dwordx4 v[88:91], v104, s[8:9]
	v_lshl_or_b32 v104, v66, 8, v2
	global_load_dwordx4 v[92:95], v104, s[8:9]
	v_lshl_or_b32 v104, v68, 8, v2
	global_load_dwordx4 v[96:99], v104, s[8:9]
	v_lshl_or_b32 v104, v70, 8, v2
	global_load_dwordx4 v[100:103], v104, s[8:9]
	s_waitcnt vmcnt(7)
	v_fma_mix_f32 v32, v57, v72, v32 op_sel_hi:[0,1,0]
	v_fma_mix_f32 v33, v57, v72, v33 op_sel:[0,1,0] op_sel_hi:[0,1,0]
	v_fma_mix_f32 v34, v57, v73, v34 op_sel_hi:[0,1,0]
	v_fma_mix_f32 v35, v57, v73, v35 op_sel:[0,1,0] op_sel_hi:[0,1,0]
	v_fma_mix_f32 v36, v57, v74, v36 op_sel_hi:[0,1,0]
	v_fma_mix_f32 v37, v57, v74, v37 op_sel:[0,1,0] op_sel_hi:[0,1,0]
	v_fma_mix_f32 v38, v57, v75, v38 op_sel_hi:[0,1,0]
	v_fma_mix_f32 v39, v57, v75, v39 op_sel:[0,1,0] op_sel_hi:[0,1,0]
	s_waitcnt vmcnt(6)
	v_fma_mix_f32 v32, v59, v76, v32 op_sel_hi:[0,1,0]
	v_fma_mix_f32 v33, v59, v76, v33 op_sel:[0,1,0] op_sel_hi:[0,1,0]
	v_fma_mix_f32 v34, v59, v77, v34 op_sel_hi:[0,1,0]
	v_fma_mix_f32 v35, v59, v77, v35 op_sel:[0,1,0] op_sel_hi:[0,1,0]
	v_fma_mix_f32 v36, v59, v78, v36 op_sel_hi:[0,1,0]
	v_fma_mix_f32 v37, v59, v78, v37 op_sel:[0,1,0] op_sel_hi:[0,1,0]
	v_fma_mix_f32 v38, v59, v79, v38 op_sel_hi:[0,1,0]
	v_fma_mix_f32 v39, v59, v79, v39 op_sel:[0,1,0] op_sel_hi:[0,1,0]
	s_waitcnt vmcnt(5)
	v_fma_mix_f32 v32, v61, v80, v32 op_sel_hi:[0,1,0]
	v_fma_mix_f32 v33, v61, v80, v33 op_sel:[0,1,0] op_sel_hi:[0,1,0]
	v_fma_mix_f32 v34, v61, v81, v34 op_sel_hi:[0,1,0]
	v_fma_mix_f32 v35, v61, v81, v35 op_sel:[0,1,0] op_sel_hi:[0,1,0]
	v_fma_mix_f32 v36, v61, v82, v36 op_sel_hi:[0,1,0]
	v_fma_mix_f32 v37, v61, v82, v37 op_sel:[0,1,0] op_sel_hi:[0,1,0]
	v_fma_mix_f32 v38, v61, v83, v38 op_sel_hi:[0,1,0]
	v_fma_mix_f32 v39, v61, v83, v39 op_sel:[0,1,0] op_sel_hi:[0,1,0]
	s_waitcnt vmcnt(4)
	v_fma_mix_f32 v32, v63, v84, v32 op_sel_hi:[0,1,0]
	v_fma_mix_f32 v33, v63, v84, v33 op_sel:[0,1,0] op_sel_hi:[0,1,0]
	v_fma_mix_f32 v34, v63, v85, v34 op_sel_hi:[0,1,0]
	v_fma_mix_f32 v35, v63, v85, v35 op_sel:[0,1,0] op_sel_hi:[0,1,0]
	v_fma_mix_f32 v36, v63, v86, v36 op_sel_hi:[0,1,0]
	v_fma_mix_f32 v37, v63, v86, v37 op_sel:[0,1,0] op_sel_hi:[0,1,0]
	v_fma_mix_f32 v38, v63, v87, v38 op_sel_hi:[0,1,0]
	v_fma_mix_f32 v39, v63, v87, v39 op_sel:[0,1,0] op_sel_hi:[0,1,0]
	s_waitcnt vmcnt(3)
	v_fma_mix_f32 v32, v65, v88, v32 op_sel_hi:[0,1,0]
	v_fma_mix_f32 v33, v65, v88, v33 op_sel:[0,1,0] op_sel_hi:[0,1,0]
	v_fma_mix_f32 v34, v65, v89, v34 op_sel_hi:[0,1,0]
	v_fma_mix_f32 v35, v65, v89, v35 op_sel:[0,1,0] op_sel_hi:[0,1,0]
	v_fma_mix_f32 v36, v65, v90, v36 op_sel_hi:[0,1,0]
	v_fma_mix_f32 v37, v65, v90, v37 op_sel:[0,1,0] op_sel_hi:[0,1,0]
	v_fma_mix_f32 v38, v65, v91, v38 op_sel_hi:[0,1,0]
	v_fma_mix_f32 v39, v65, v91, v39 op_sel:[0,1,0] op_sel_hi:[0,1,0]
	s_waitcnt vmcnt(2)
	v_fma_mix_f32 v32, v67, v92, v32 op_sel_hi:[0,1,0]
	v_fma_mix_f32 v33, v67, v92, v33 op_sel:[0,1,0] op_sel_hi:[0,1,0]
	v_fma_mix_f32 v34, v67, v93, v34 op_sel_hi:[0,1,0]
	v_fma_mix_f32 v35, v67, v93, v35 op_sel:[0,1,0] op_sel_hi:[0,1,0]
	v_fma_mix_f32 v36, v67, v94, v36 op_sel_hi:[0,1,0]
	v_fma_mix_f32 v37, v67, v94, v37 op_sel:[0,1,0] op_sel_hi:[0,1,0]
	v_fma_mix_f32 v38, v67, v95, v38 op_sel_hi:[0,1,0]
	v_fma_mix_f32 v39, v67, v95, v39 op_sel:[0,1,0] op_sel_hi:[0,1,0]
	s_waitcnt vmcnt(1)
	v_fma_mix_f32 v32, v69, v96, v32 op_sel_hi:[0,1,0]
	v_fma_mix_f32 v33, v69, v96, v33 op_sel:[0,1,0] op_sel_hi:[0,1,0]
	v_fma_mix_f32 v34, v69, v97, v34 op_sel_hi:[0,1,0]
	v_fma_mix_f32 v35, v69, v97, v35 op_sel:[0,1,0] op_sel_hi:[0,1,0]
	v_fma_mix_f32 v36, v69, v98, v36 op_sel_hi:[0,1,0]
	v_fma_mix_f32 v37, v69, v98, v37 op_sel:[0,1,0] op_sel_hi:[0,1,0]
	v_fma_mix_f32 v38, v69, v99, v38 op_sel_hi:[0,1,0]
	v_fma_mix_f32 v39, v69, v99, v39 op_sel:[0,1,0] op_sel_hi:[0,1,0]
	s_waitcnt vmcnt(0)
	v_fma_mix_f32 v32, v71, v100, v32 op_sel_hi:[0,1,0]
	v_fma_mix_f32 v33, v71, v100, v33 op_sel:[0,1,0] op_sel_hi:[0,1,0]
	v_fma_mix_f32 v34, v71, v101, v34 op_sel_hi:[0,1,0]
	v_fma_mix_f32 v35, v71, v101, v35 op_sel:[0,1,0] op_sel_hi:[0,1,0]
	v_fma_mix_f32 v36, v71, v102, v36 op_sel_hi:[0,1,0]
	v_fma_mix_f32 v37, v71, v102, v37 op_sel:[0,1,0] op_sel_hi:[0,1,0]
	v_fma_mix_f32 v38, v71, v103, v38 op_sel_hi:[0,1,0]
	v_fma_mix_f32 v39, v71, v103, v39 op_sel:[0,1,0] op_sel_hi:[0,1,0]
.Lsw_skip3:
	s_add_u32 s28, s28, 1
	s_cmp_lt_u32 s28, s29
	s_cbranch_scc1 .Lsw_round
.Lsw_rounds_done:
	s_waitcnt vmcnt(0)
	s_lshr_b32 s40, s26, 1
	s_lshl_b32 s40, s40, 2
	s_and_b32 s41, s26, 1
	s_add_u32 s40, s40, s41
	s_lshl_b32 s40, s40, 1
	s_lshl_b32 s40, s40, 9
	s_add_u32 s40, s40, s2
	s_sub_u32 s41, s27, s40
	s_sub_u32 s41, s41, 1
	s_cmp_lt_u32 s40, s27
	s_cselect_b64 s[42:43], -1, 0
	v_lshl_add_u32 v106, s41, 5, v3
	v_cmp_gt_i32_e32 vcc, s18, v106
	s_and_b64 s[44:45], vcc, s[42:43]
	s_nop 1
	v_cndmask_b32_e32 v107, 0, v106, vcc
	v_lshlrev_b32_e32 v108, 8, v107
	v_or_b32_e32 v108, v108, v2
	v_lshlrev_b32_e32 v109, 2, v107
	v_lshrrev_b32_e32 v110, 5, v107
	v_lshlrev_b32_e32 v110, 2, v110
	s_mov_b64 s[36:37], exec
	s_and_b64 exec, exec, s[42:43]
	global_load_dwordx4 v[72:75], v108, s[12:13]
	global_load_dword v88, v109, s[16:17]
	global_load_dword v92, v110, s[14:15]
	s_mov_b64 exec, s[36:37]
	s_lshr_b32 s40, s26, 1
	s_lshl_b32 s40, s40, 2
	s_and_b32 s41, s26, 1
	s_add_u32 s40, s40, s41
	s_lshl_b32 s40, s40, 1
	s_or_b32 s40, s40, 1
	s_lshl_b32 s40, s40, 9
	s_add_u32 s40, s40, s2
	s_sub_u32 s41, s27, s40
	s_sub_u32 s41, s41, 1
	s_cmp_lt_u32 s40, s27
	s_cselect_b64 s[42:43], -1, 0
	v_lshl_add_u32 v106, s41, 5, v3
	v_cmp_gt_i32_e32 vcc, s18, v106
	s_and_b64 s[46:47], vcc, s[42:43]
	s_nop 1
	v_cndmask_b32_e32 v107, 0, v106, vcc
	v_lshlrev_b32_e32 v108, 8, v107
	v_or_b32_e32 v108, v108, v2
	v_lshlrev_b32_e32 v109, 2, v107
	v_lshrrev_b32_e32 v110, 5, v107
	v_lshlrev_b32_e32 v110, 2, v110
	s_mov_b64 s[36:37], exec
	s_and_b64 exec, exec, s[42:43]
	global_load_dwordx4 v[76:79], v108, s[12:13]
	global_load_dword v89, v109, s[16:17]
	global_load_dword v93, v110, s[14:15]
	s_mov_b64 exec, s[36:37]
	s_lshr_b32 s40, s26, 1
	s_lshl_b32 s40, s40, 2
	s_and_b32 s41, s26, 1
	s_add_u32 s40, s40, s41
	s_add_u32 s40, s40, 2
	s_lshl_b32 s40, s40, 1
	s_lshl_b32 s40, s40, 9
	s_add_u32 s40, s40, s2
	s_sub_u32 s41, s27, s40
	s_sub_u32 s41, s41, 1
	s_cmp_lt_u32 s40, s27
	s_cselect_b64 s[42:43], -1, 0
	v_lshl_add_u32 v106, s41, 5, v3
	v_cmp_gt_i32_e32 vcc, s18, v106
	s_and_b64 s[48:49], vcc, s[42:43]
	s_nop 1
	v_cndmask_b32_e32 v107, 0, v106, vcc
	v_lshlrev_b32_e32 v108, 8, v107
	v_or_b32_e32 v108, v108, v2
	v_lshlrev_b32_e32 v109, 2, v107
	v_lshrrev_b32_e32 v110, 5, v107
	v_lshlrev_b32_e32 v110, 2, v110
	s_mov_b64 s[36:37], exec
	s_and_b64 exec, exec, s[42:43]
	global_load_dwordx4 v[80:83], v108, s[12:13]
	global_load_dword v90, v109, s[16:17]
	global_load_dword v94, v110, s[14:15]
	s_mov_b64 exec, s[36:37]
	s_lshr_b32 s40, s26, 1
	s_lshl_b32 s40, s40, 2
	s_and_b32 s41, s26, 1
	s_add_u32 s40, s40, s41
	s_add_u32 s40, s40, 2
	s_lshl_b32 s40, s40, 1
	s_or_b32 s40, s40, 1
	s_lshl_b32 s40, s40, 9
	s_add_u32 s40, s40, s2
	s_sub_u32 s41, s27, s40
	s_sub_u32 s41, s41, 1
	s_cmp_lt_u32 s40, s27
	s_cselect_b64 s[42:43], -1, 0
	v_lshl_add_u32 v106, s41, 5, v3
	v_cmp_gt_i32_e32 vcc, s18, v106
	s_and_b64 s[50:51], vcc, s[42:43]
	s_nop 1
	v_cndmask_b32_e32 v107, 0, v106, vcc
	v_lshlrev_b32_e32 v108, 8, v107
	v_or_b32_e32 v108, v108, v2
	v_lshlrev_b32_e32 v109, 2, v107
	v_lshrrev_b32_e32 v110, 5, v107
	v_lshlrev_b32_e32 v110, 2, v110
	s_mov_b64 s[36:37], exec
	s_and_b64 exec, exec, s[42:43]
	global_load_dwordx4 v[84:87], v108, s[12:13]
	global_load_dword v91, v109, s[16:17]
	global_load_dword v95, v110, s[14:15]
	s_mov_b64 exec, s[36:37]
	s_waitcnt vmcnt(0)
	s_lshr_b32 s40, s26, 1
	s_lshl_b32 s40, s40, 2
	s_and_b32 s41, s26, 1
	s_add_u32 s40, s40, s41
	s_lshl_b32 s40, s40, 1
	s_lshl_b32 s40, s40, 9
	s_add_u32 s40, s40, s2
	s_sub_u32 s41, s27, s40
	s_sub_u32 s41, s41, 1
	s_cmp_lt_u32 s40, s27
	s_cselect_b64 s[42:43], -1, 0
	s_cmp_lt_u32 s40, s27
	s_cbranch_scc0 .Lsw_epi_skip0
	v_lshl_add_u32 v106, s41, 5, v3
	v_mul_f32_e32 v56, v8, v8
	v_fmac_f32_e32 v56, v9, v9
	v_fmac_f32_e32 v56, v10, v10
	v_fmac_f32_e32 v56, v11, v11
	v_fmac_f32_e32 v56, v12, v12
	v_fmac_f32_e32 v56, v13, v13
	v_fmac_f32_e32 v56, v14, v14
	v_fmac_f32_e32 v56, v15, v15
	v_max_f32_e64 v57, |v8|, |v9|
	v_max3_f32 v57, v57, |v10|, |v11|
	v_max3_f32 v57, v57, |v12|, |v13|
	v_max3_f32 v57, v57, |v14|, |v15|
	v_fma_mix_f32 v58, v8, v72, 0 op_sel_hi:[0,1,0]
	v_fma_mix_f32 v58, v9, v72, v58 op_sel:[0,1,0] op_sel_hi:[0,1,0]
	v_fma_mix_f32 v58, v10, v73, v58 op_sel_hi:[0,1,0]
	v_fma_mix_f32 v58, v11, v73, v58 op_sel:[0,1,0] op_sel_hi:[0,1,0]
	v_fma_mix_f32 v58, v12, v74, v58 op_sel_hi:[0,1,0]
	v_fma_mix_f32 v58, v13, v74, v58 op_sel:[0,1,0] op_sel_hi:[0,1,0]
	v_fma_mix_f32 v58, v14, v75, v58 op_sel_hi:[0,1,0]
	v_fma_mix_f32 v58, v15, v75, v58 op_sel:[0,1,0] op_sel_hi:[0,1,0]
	s_nop 1
	v_add_f32_dpp v56, v56, v56 quad_perm:[1,0,3,2] row_mask:0xf bank_mask:0xf
	v_add_f32_dpp v58, v58, v58 quad_perm:[1,0,3,2] row_mask:0xf bank_mask:0xf
	v_max_f32_dpp v57, v57, v57 quad_perm:[1,0,3,2] row_mask:0xf bank_mask:0xf
	v_add_f32_dpp v56, v56, v56 quad_perm:[2,3,0,1] row_mask:0xf bank_mask:0xf
	v_add_f32_dpp v58, v58, v58 quad_perm:[2,3,0,1] row_mask:0xf bank_mask:0xf
	v_max_f32_dpp v57, v57, v57 quad_perm:[2,3,0,1] row_mask:0xf bank_mask:0xf
	v_add_f32_dpp v56, v56, v56 row_half_mirror row_mask:0xf bank_mask:0xf
	v_add_f32_dpp v58, v58, v58 row_half_mirror row_mask:0xf bank_mask:0xf
	v_max_f32_dpp v57, v57, v57 row_half_mirror row_mask:0xf bank_mask:0xf
	v_add_f32_dpp v56, v56, v56 row_mirror row_mask:0xf bank_mask:0xf
	v_add_f32_dpp v58, v58, v58 row_mirror row_mask:0xf bank_mask:0xf
	v_max_f32_dpp v57, v57, v57 row_mirror row_mask:0xf bank_mask:0xf
	v_sqrt_f32_e32 v59, v56
	v_mul_f32_e32 v60, v58, v92
	v_max_f32_e32 v59, 0x322bcc77, v59
	v_mul_f32_e32 v61, v59, v88
	v_rcp_f32_e32 v61, v61
	s_nop 0
	v_mul_f32_e32 v60, v60, v61
	v_mul_f32_e64 v62, |v60|, v57
	v_cndmask_b32_e64 v62, 0, v62, s[44:45]
	s_nop 1
	v_readlane_b32 s40, v62, 0
	v_readlane_b32 s42, v62, 16
	v_readlane_b32 s52, v62, 32
	v_readlane_b32 s53, v62, 48
	s_nop 0
	s_max_u32 s40, s40, s42
	s_max_u32 s52, s52, s53
	s_max_u32 s40, s40, s52
	v_mov_b32_e32 v63, s40
	v_lshrrev_b32_e32 v64, 6, v0
	v_lshlrev_b32_e32 v64, 2, v64
	ds_write_b32 v64, v63 offset:36864
	s_waitcnt lgkmcnt(0)
	s_barrier
	v_mov_b32_e32 v64, 0
	ds_read_b128 v[64:67], v64 offset:36864
	v_mov_b32_e32 v68, 0
	ds_read_b128 v[68:71], v68 offset:36880
	s_waitcnt lgkmcnt(0)
	v_max3_f32 v96, v64, v65, v66
	v_max3_f32 v96, v96, v67, v68
	v_max3_f32 v96, v96, v69, v70
	v_max_f32_e32 v96, v96, v71
	v_cmp_lt_f32_e32 vcc, 0, v96
	s_nop 1
	v_cndmask_b32_e32 v96, 1.0, v96, vcc
	v_rcp_f32_e32 v97, v96
	s_nop 0
	v_mul_f32_e32 v98, v60, v97
	v_mul_f32_e32 v99, 0x43800000, v98
	v_mul_f32_e32 v112, v8, v98
	v_mul_f32_e32 v113, v9, v98
	v_mul_f32_e32 v114, v10, v98
	v_mul_f32_e32 v115, v11, v98
	v_mul_f32_e32 v116, v12, v98
	v_mul_f32_e32 v117, v13, v98
	v_mul_f32_e32 v118, v14, v98
	v_mul_f32_e32 v119, v15, v98
	v_cvt_pk_f16_f32 v100, v112, v113
	v_cvt_pk_f16_f32 v101, v114, v115
	v_cvt_pk_f16_f32 v102, v116, v117
	v_cvt_pk_f16_f32 v103, v118, v119
	v_mul_f32_e32 v112, v8, v99
	v_mul_f32_e32 v113, v9, v99
	v_mul_f32_e32 v114, v10, v99
	v_mul_f32_e32 v115, v11, v99
	v_mul_f32_e32 v116, v12, v99
	v_mul_f32_e32 v117, v13, v99
	v_mul_f32_e32 v118, v14, v99
	v_mul_f32_e32 v119, v15, v99
	v_mov_b32_e32 v104, 0
	v_mov_b32_e32 v105, 0
	v_cvt_pk_fp8_f32 v104, v112, v113
	v_cvt_pk_fp8_f32 v105, v116, v117
	v_cvt_pk_fp8_f32 v104, v114, v115 op_sel:[0,0,1]
	v_cvt_pk_fp8_f32 v105, v118, v119 op_sel:[0,0,1]
	v_lshlrev_b32_e32 v108, 8, v106
	v_or_b32_e32 v108, v108, v2
	v_lshlrev_b32_e32 v109, 7, v106
	v_lshl_or_b32 v109, v1, 3, v109
	s_mov_b64 s[36:37], exec
	s_and_b64 exec, exec, s[44:45]
	global_store_dwordx4 v108, v[100:103], s[20:21]
	global_store_dwordx2 v109, v[104:105], s[22:23]
	s_mov_b64 exec, s[36:37]
	v_cmp_eq_u32_e32 vcc, 0, v0
	v_mul_f32_e32 v110, 0x3b800000, v96
	s_lshl_b32 s40, s41, 2
	v_mov_b32_e32 v111, s40
	s_and_saveexec_b64 s[36:37], vcc
	global_store_dword v111, v110, s[24:25]
	s_mov_b64 exec, s[36:37]
.Lsw_epi_skip0:
	s_lshr_b32 s40, s26, 1
	s_lshl_b32 s40, s40, 2
	s_and_b32 s41, s26, 1
	s_add_u32 s40, s40, s41
	s_lshl_b32 s40, s40, 1
	s_or_b32 s40, s40, 1
	s_lshl_b32 s40, s40, 9
	s_add_u32 s40, s40, s2
	s_sub_u32 s41, s27, s40
	s_sub_u32 s41, s41, 1
	s_cmp_lt_u32 s40, s27
	s_cselect_b64 s[42:43], -1, 0
	s_cmp_lt_u32 s40, s27
	s_cbranch_scc0 .Lsw_epi_skip1
	v_lshl_add_u32 v106, s41, 5, v3
	v_mul_f32_e32 v56, v16, v16
	v_fmac_f32_e32 v56, v17, v17
	v_fmac_f32_e32 v56, v18, v18
	v_fmac_f32_e32 v56, v19, v19
	v_fmac_f32_e32 v56, v20, v20
	v_fmac_f32_e32 v56, v21, v21
	v_fmac_f32_e32 v56, v22, v22
	v_fmac_f32_e32 v56, v23, v23
	v_max_f32_e64 v57, |v16|, |v17|
	v_max3_f32 v57, v57, |v18|, |v19|
	v_max3_f32 v57, v57, |v20|, |v21|
	v_max3_f32 v57, v57, |v22|, |v23|
	v_fma_mix_f32 v58, v16, v76, 0 op_sel_hi:[0,1,0]
	v_fma_mix_f32 v58, v17, v76, v58 op_sel:[0,1,0] op_sel_hi:[0,1,0]
	v_fma_mix_f32 v58, v18, v77, v58 op_sel_hi:[0,1,0]
	v_fma_mix_f32 v58, v19, v77, v58 op_sel:[0,1,0] op_sel_hi:[0,1,0]
	v_fma_mix_f32 v58, v20, v78, v58 op_sel_hi:[0,1,0]
	v_fma_mix_f32 v58, v21, v78, v58 op_sel:[0,1,0] op_sel_hi:[0,1,0]
	v_fma_mix_f32 v58, v22, v79, v58 op_sel_hi:[0,1,0]
	v_fma_mix_f32 v58, v23, v79, v58 op_sel:[0,1,0] op_sel_hi:[0,1,0]
	s_nop 1
	v_add_f32_dpp v56, v56, v56 quad_perm:[1,0,3,2] row_mask:0xf bank_mask:0xf
	v_add_f32_dpp v58, v58, v58 quad_perm:[1,0,3,2] row_mask:0xf bank_mask:0xf
	v_max_f32_dpp v57, v57, v57 quad_perm:[1,0,3,2] row_mask:0xf bank_mask:0xf
	v_add_f32_dpp v56, v56, v56 quad_perm:[2,3,0,1] row_mask:0xf bank_mask:0xf
	v_add_f32_dpp v58, v58, v58 quad_perm:[2,3,0,1] row_mask:0xf bank_mask:0xf
	v_max_f32_dpp v57, v57, v57 quad_perm:[2,3,0,1] row_mask:0xf bank_mask:0xf
	v_add_f32_dpp v56, v56, v56 row_half_mirror row_mask:0xf bank_mask:0xf
	v_add_f32_dpp v58, v58, v58 row_half_mirror row_mask:0xf bank_mask:0xf
	v_max_f32_dpp v57, v57, v57 row_half_mirror row_mask:0xf bank_mask:0xf
	v_add_f32_dpp v56, v56, v56 row_mirror row_mask:0xf bank_mask:0xf
	v_add_f32_dpp v58, v58, v58 row_mirror row_mask:0xf bank_mask:0xf
	v_max_f32_dpp v57, v57, v57 row_mirror row_mask:0xf bank_mask:0xf
	v_sqrt_f32_e32 v59, v56
	v_mul_f32_e32 v60, v58, v93
	v_max_f32_e32 v59, 0x322bcc77, v59
	v_mul_f32_e32 v61, v59, v89
	v_rcp_f32_e32 v61, v61
	s_nop 0
	v_mul_f32_e32 v60, v60, v61
	v_mul_f32_e64 v62, |v60|, v57
	v_cndmask_b32_e64 v62, 0, v62, s[46:47]
	s_nop 1
	v_readlane_b32 s40, v62, 0
	v_readlane_b32 s42, v62, 16
	v_readlane_b32 s52, v62, 32
	v_readlane_b32 s53, v62, 48
	s_nop 0
	s_max_u32 s40, s40, s42
	s_max_u32 s52, s52, s53
	s_max_u32 s40, s40, s52
	v_mov_b32_e32 v63, s40
	v_lshrrev_b32_e32 v64, 6, v0
	v_lshlrev_b32_e32 v64, 2, v64
	ds_write_b32 v64, v63 offset:36896
	s_waitcnt lgkmcnt(0)
	s_barrier
	v_mov_b32_e32 v64, 0
	ds_read_b128 v[64:67], v64 offset:36896
	v_mov_b32_e32 v68, 0
	ds_read_b128 v[68:71], v68 offset:36912
	s_waitcnt lgkmcnt(0)
	v_max3_f32 v96, v64, v65, v66
	v_max3_f32 v96, v96, v67, v68
	v_max3_f32 v96, v96, v69, v70
	v_max_f32_e32 v96, v96, v71
	v_cmp_lt_f32_e32 vcc, 0, v96
	s_nop 1
	v_cndmask_b32_e32 v96, 1.0, v96, vcc
	v_rcp_f32_e32 v97, v96
	s_nop 0
	v_mul_f32_e32 v98, v60, v97
	v_mul_f32_e32 v99, 0x43800000, v98
	v_mul_f32_e32 v112, v16, v98
	v_mul_f32_e32 v113, v17, v98
	v_mul_f32_e32 v114, v18, v98
	v_mul_f32_e32 v115, v19, v98
	v_mul_f32_e32 v116, v20, v98
	v_mul_f32_e32 v117, v21, v98
	v_mul_f32_e32 v118, v22, v98
	v_mul_f32_e32 v119, v23, v98
	v_cvt_pk_f16_f32 v100, v112, v113
	v_cvt_pk_f16_f32 v101, v114, v115
	v_cvt_pk_f16_f32 v102, v116, v117
	v_cvt_pk_f16_f32 v103, v118, v119
	v_mul_f32_e32 v112, v16, v99
	v_mul_f32_e32 v113, v17, v99
	v_mul_f32_e32 v114, v18, v99
	v_mul_f32_e32 v115, v19, v99
	v_mul_f32_e32 v116, v20, v99
	v_mul_f32_e32 v117, v21, v99
	v_mul_f32_e32 v118, v22, v99
	v_mul_f32_e32 v119, v23, v99
	v_mov_b32_e32 v104, 0
	v_mov_b32_e32 v105, 0
	v_cvt_pk_fp8_f32 v104, v112, v113
	v_cvt_pk_fp8_f32 v105, v116, v117
	v_cvt_pk_fp8_f32 v104, v114, v115 op_sel:[0,0,1]
	v_cvt_pk_fp8_f32 v105, v118, v119 op_sel:[0,0,1]
	v_lshlrev_b32_e32 v108, 8, v106
	v_or_b32_e32 v108, v108, v2
	v_lshlrev_b32_e32 v109, 7, v106
	v_lshl_or_b32 v109, v1, 3, v109
	s_mov_b64 s[36:37], exec
	s_and_b64 exec, exec, s[46:47]
	global_store_dwordx4 v108, v[100:103], s[20:21]
	global_store_dwordx2 v109, v[104:105], s[22:23]
	s_mov_b64 exec, s[36:37]
	v_cmp_eq_u32_e32 vcc, 0, v0
	v_mul_f32_e32 v110, 0x3b800000, v96
	s_lshl_b32 s40, s41, 2
	v_mov_b32_e32 v111, s40
	s_and_saveexec_b64 s[36:37], vcc
	global_store_dword v111, v110, s[24:25]
	s_mov_b64 exec, s[36:37]
.Lsw_epi_skip1:
	s_lshr_b32 s40, s26, 1
	s_lshl_b32 s40, s40, 2
	s_and_b32 s41, s26, 1
	s_add_u32 s40, s40, s41
	s_add_u32 s40, s40, 2
	s_lshl_b32 s40, s40, 1
	s_lshl_b32 s40, s40, 9
	s_add_u32 s40, s40, s2
	s_sub_u32 s41, s27, s40
	s_sub_u32 s41, s41, 1
	s_cmp_lt_u32 s40, s27
	s_cselect_b64 s[42:43], -1, 0
	s_cmp_lt_u32 s40, s27
	s_cbranch_scc0 .Lsw_epi_skip2
	v_lshl_add_u32 v106, s41, 5, v3
	v_mul_f32_e32 v56, v24, v24
	v_fmac_f32_e32 v56, v25, v25
	v_fmac_f32_e32 v56, v26, v26
	v_fmac_f32_e32 v56, v27, v27
	v_fmac_f32_e32 v56, v28, v28
	v_fmac_f32_e32 v56, v29, v29
	v_fmac_f32_e32 v56, v30, v30
	v_fmac_f32_e32 v56, v31, v31
	v_max_f32_e64 v57, |v24|, |v25|
	v_max3_f32 v57, v57, |v26|, |v27|
	v_max3_f32 v57, v57, |v28|, |v29|
	v_max3_f32 v57, v57, |v30|, |v31|
	v_fma_mix_f32 v58, v24, v80, 0 op_sel_hi:[0,1,0]
	v_fma_mix_f32 v58, v25, v80, v58 op_sel:[0,1,0] op_sel_hi:[0,1,0]
	v_fma_mix_f32 v58, v26, v81, v58 op_sel_hi:[0,1,0]
	v_fma_mix_f32 v58, v27, v81, v58 op_sel:[0,1,0] op_sel_hi:[0,1,0]
	v_fma_mix_f32 v58, v28, v82, v58 op_sel_hi:[0,1,0]
	v_fma_mix_f32 v58, v29, v82, v58 op_sel:[0,1,0] op_sel_hi:[0,1,0]
	v_fma_mix_f32 v58, v30, v83, v58 op_sel_hi:[0,1,0]
	v_fma_mix_f32 v58, v31, v83, v58 op_sel:[0,1,0] op_sel_hi:[0,1,0]
	s_nop 1
	v_add_f32_dpp v56, v56, v56 quad_perm:[1,0,3,2] row_mask:0xf bank_mask:0xf
	v_add_f32_dpp v58, v58, v58 quad_perm:[1,0,3,2] row_mask:0xf bank_mask:0xf
	v_max_f32_dpp v57, v57, v57 quad_perm:[1,0,3,2] row_mask:0xf bank_mask:0xf
	v_add_f32_dpp v56, v56, v56 quad_perm:[2,3,0,1] row_mask:0xf bank_mask:0xf
	v_add_f32_dpp v58, v58, v58 quad_perm:[2,3,0,1] row_mask:0xf bank_mask:0xf
	v_max_f32_dpp v57, v57, v57 quad_perm:[2,3,0,1] row_mask:0xf bank_mask:0xf
	v_add_f32_dpp v56, v56, v56 row_half_mirror row_mask:0xf bank_mask:0xf
	v_add_f32_dpp v58, v58, v58 row_half_mirror row_mask:0xf bank_mask:0xf
	v_max_f32_dpp v57, v57, v57 row_half_mirror row_mask:0xf bank_mask:0xf
	v_add_f32_dpp v56, v56, v56 row_mirror row_mask:0xf bank_mask:0xf
	v_add_f32_dpp v58, v58, v58 row_mirror row_mask:0xf bank_mask:0xf
	v_max_f32_dpp v57, v57, v57 row_mirror row_mask:0xf bank_mask:0xf
	v_sqrt_f32_e32 v59, v56
	v_mul_f32_e32 v60, v58, v94
	v_max_f32_e32 v59, 0x322bcc77, v59
	v_mul_f32_e32 v61, v59, v90
	v_rcp_f32_e32 v61, v61
	s_nop 0
	v_mul_f32_e32 v60, v60, v61
	v_mul_f32_e64 v62, |v60|, v57
	v_cndmask_b32_e64 v62, 0, v62, s[48:49]
	s_nop 1
	v_readlane_b32 s40, v62, 0
	v_readlane_b32 s42, v62, 16
	v_readlane_b32 s52, v62, 32
	v_readlane_b32 s53, v62, 48
	s_nop 0
	s_max_u32 s40, s40, s42
	s_max_u32 s52, s52, s53
	s_max_u32 s40, s40, s52
	v_mov_b32_e32 v63, s40
	v_lshrrev_b32_e32 v64, 6, v0
	v_lshlrev_b32_e32 v64, 2, v64
	ds_write_b32 v64, v63 offset:36864
	s_waitcnt lgkmcnt(0)
	s_barrier
	v_mov_b32_e32 v64, 0
	ds_read_b128 v[64:67], v64 offset:36864
	v_mov_b32_e32 v68, 0
	ds_read_b128 v[68:71], v68 offset:36880
	s_waitcnt lgkmcnt(0)
	v_max3_f32 v96, v64, v65, v66
	v_max3_f32 v96, v96, v67, v68
	v_max3_f32 v96, v96, v69, v70
	v_max_f32_e32 v96, v96, v71
	v_cmp_lt_f32_e32 vcc, 0, v96
	s_nop 1
	v_cndmask_b32_e32 v96, 1.0, v96, vcc
	v_rcp_f32_e32 v97, v96
	s_nop 0
	v_mul_f32_e32 v98, v60, v97
	v_mul_f32_e32 v99, 0x43800000, v98
	v_mul_f32_e32 v112, v24, v98
	v_mul_f32_e32 v113, v25, v98
	v_mul_f32_e32 v114, v26, v98
	v_mul_f32_e32 v115, v27, v98
	v_mul_f32_e32 v116, v28, v98
	v_mul_f32_e32 v117, v29, v98
	v_mul_f32_e32 v118, v30, v98
	v_mul_f32_e32 v119, v31, v98
	v_cvt_pk_f16_f32 v100, v112, v113
	v_cvt_pk_f16_f32 v101, v114, v115
	v_cvt_pk_f16_f32 v102, v116, v117
	v_cvt_pk_f16_f32 v103, v118, v119
	v_mul_f32_e32 v112, v24, v99
	v_mul_f32_e32 v113, v25, v99
	v_mul_f32_e32 v114, v26, v99
	v_mul_f32_e32 v115, v27, v99
	v_mul_f32_e32 v116, v28, v99
	v_mul_f32_e32 v117, v29, v99
	v_mul_f32_e32 v118, v30, v99
	v_mul_f32_e32 v119, v31, v99
	v_mov_b32_e32 v104, 0
	v_mov_b32_e32 v105, 0
	v_cvt_pk_fp8_f32 v104, v112, v113
	v_cvt_pk_fp8_f32 v105, v116, v117
	v_cvt_pk_fp8_f32 v104, v114, v115 op_sel:[0,0,1]
	v_cvt_pk_fp8_f32 v105, v118, v119 op_sel:[0,0,1]
	v_lshlrev_b32_e32 v108, 8, v106
	v_or_b32_e32 v108, v108, v2
	v_lshlrev_b32_e32 v109, 7, v106
	v_lshl_or_b32 v109, v1, 3, v109
	s_mov_b64 s[36:37], exec
	s_and_b64 exec, exec, s[48:49]
	global_store_dwordx4 v108, v[100:103], s[20:21]
	global_store_dwordx2 v109, v[104:105], s[22:23]
	s_mov_b64 exec, s[36:37]
	v_cmp_eq_u32_e32 vcc, 0, v0
	v_mul_f32_e32 v110, 0x3b800000, v96
	s_lshl_b32 s40, s41, 2
	v_mov_b32_e32 v111, s40
	s_and_saveexec_b64 s[36:37], vcc
	global_store_dword v111, v110, s[24:25]
	s_mov_b64 exec, s[36:37]
.Lsw_epi_skip2:
	s_lshr_b32 s40, s26, 1
	s_lshl_b32 s40, s40, 2
	s_and_b32 s41, s26, 1
	s_add_u32 s40, s40, s41
	s_add_u32 s40, s40, 2
	s_lshl_b32 s40, s40, 1
	s_or_b32 s40, s40, 1
	s_lshl_b32 s40, s40, 9
	s_add_u32 s40, s40, s2
	s_sub_u32 s41, s27, s40
	s_sub_u32 s41, s41, 1
	s_cmp_lt_u32 s40, s27
	s_cselect_b64 s[42:43], -1, 0
	s_cmp_lt_u32 s40, s27
	s_cbranch_scc0 .Lsw_epi_skip3
	v_lshl_add_u32 v106, s41, 5, v3
	v_mul_f32_e32 v56, v32, v32
	v_fmac_f32_e32 v56, v33, v33
	v_fmac_f32_e32 v56, v34, v34
	v_fmac_f32_e32 v56, v35, v35
	v_fmac_f32_e32 v56, v36, v36
	v_fmac_f32_e32 v56, v37, v37
	v_fmac_f32_e32 v56, v38, v38
	v_fmac_f32_e32 v56, v39, v39
	v_max_f32_e64 v57, |v32|, |v33|
	v_max3_f32 v57, v57, |v34|, |v35|
	v_max3_f32 v57, v57, |v36|, |v37|
	v_max3_f32 v57, v57, |v38|, |v39|
	v_fma_mix_f32 v58, v32, v84, 0 op_sel_hi:[0,1,0]
	v_fma_mix_f32 v58, v33, v84, v58 op_sel:[0,1,0] op_sel_hi:[0,1,0]
	v_fma_mix_f32 v58, v34, v85, v58 op_sel_hi:[0,1,0]
	v_fma_mix_f32 v58, v35, v85, v58 op_sel:[0,1,0] op_sel_hi:[0,1,0]
	v_fma_mix_f32 v58, v36, v86, v58 op_sel_hi:[0,1,0]
	v_fma_mix_f32 v58, v37, v86, v58 op_sel:[0,1,0] op_sel_hi:[0,1,0]
	v_fma_mix_f32 v58, v38, v87, v58 op_sel_hi:[0,1,0]
	v_fma_mix_f32 v58, v39, v87, v58 op_sel:[0,1,0] op_sel_hi:[0,1,0]
	s_nop 1
	v_add_f32_dpp v56, v56, v56 quad_perm:[1,0,3,2] row_mask:0xf bank_mask:0xf
	v_add_f32_dpp v58, v58, v58 quad_perm:[1,0,3,2] row_mask:0xf bank_mask:0xf
	v_max_f32_dpp v57, v57, v57 quad_perm:[1,0,3,2] row_mask:0xf bank_mask:0xf
	v_add_f32_dpp v56, v56, v56 quad_perm:[2,3,0,1] row_mask:0xf bank_mask:0xf
	v_add_f32_dpp v58, v58, v58 quad_perm:[2,3,0,1] row_mask:0xf bank_mask:0xf
	v_max_f32_dpp v57, v57, v57 quad_perm:[2,3,0,1] row_mask:0xf bank_mask:0xf
	v_add_f32_dpp v56, v56, v56 row_half_mirror row_mask:0xf bank_mask:0xf
	v_add_f32_dpp v58, v58, v58 row_half_mirror row_mask:0xf bank_mask:0xf
	v_max_f32_dpp v57, v57, v57 row_half_mirror row_mask:0xf bank_mask:0xf
	v_add_f32_dpp v56, v56, v56 row_mirror row_mask:0xf bank_mask:0xf
	v_add_f32_dpp v58, v58, v58 row_mirror row_mask:0xf bank_mask:0xf
	v_max_f32_dpp v57, v57, v57 row_mirror row_mask:0xf bank_mask:0xf
	v_sqrt_f32_e32 v59, v56
	v_mul_f32_e32 v60, v58, v95
	v_max_f32_e32 v59, 0x322bcc77, v59
	v_mul_f32_e32 v61, v59, v91
	v_rcp_f32_e32 v61, v61
	s_nop 0
	v_mul_f32_e32 v60, v60, v61
	v_mul_f32_e64 v62, |v60|, v57
	v_cndmask_b32_e64 v62, 0, v62, s[50:51]
	s_nop 1
	v_readlane_b32 s40, v62, 0
	v_readlane_b32 s42, v62, 16
	v_readlane_b32 s52, v62, 32
	v_readlane_b32 s53, v62, 48
	s_nop 0
	s_max_u32 s40, s40, s42
	s_max_u32 s52, s52, s53
	s_max_u32 s40, s40, s52
	v_mov_b32_e32 v63, s40
	v_lshrrev_b32_e32 v64, 6, v0
	v_lshlrev_b32_e32 v64, 2, v64
	ds_write_b32 v64, v63 offset:36896
	s_waitcnt lgkmcnt(0)
	s_barrier
	v_mov_b32_e32 v64, 0
	ds_read_b128 v[64:67], v64 offset:36896
	v_mov_b32_e32 v68, 0
	ds_read_b128 v[68:71], v68 offset:36912
	s_waitcnt lgkmcnt(0)
	v_max3_f32 v96, v64, v65, v66
	v_max3_f32 v96, v96, v67, v68
	v_max3_f32 v96, v96, v69, v70
	v_max_f32_e32 v96, v96, v71
	v_cmp_lt_f32_e32 vcc, 0, v96
	s_nop 1
	v_cndmask_b32_e32 v96, 1.0, v96, vcc
	v_rcp_f32_e32 v97, v96
	s_nop 0
	v_mul_f32_e32 v98, v60, v97
	v_mul_f32_e32 v99, 0x43800000, v98
	v_mul_f32_e32 v112, v32, v98
	v_mul_f32_e32 v113, v33, v98
	v_mul_f32_e32 v114, v34, v98
	v_mul_f32_e32 v115, v35, v98
	v_mul_f32_e32 v116, v36, v98
	v_mul_f32_e32 v117, v37, v98
	v_mul_f32_e32 v118, v38, v98
	v_mul_f32_e32 v119, v39, v98
	v_cvt_pk_f16_f32 v100, v112, v113
	v_cvt_pk_f16_f32 v101, v114, v115
	v_cvt_pk_f16_f32 v102, v116, v117
	v_cvt_pk_f16_f32 v103, v118, v119
	v_mul_f32_e32 v112, v32, v99
	v_mul_f32_e32 v113, v33, v99
	v_mul_f32_e32 v114, v34, v99
	v_mul_f32_e32 v115, v35, v99
	v_mul_f32_e32 v116, v36, v99
	v_mul_f32_e32 v117, v37, v99
	v_mul_f32_e32 v118, v38, v99
	v_mul_f32_e32 v119, v39, v99
	v_mov_b32_e32 v104, 0
	v_mov_b32_e32 v105, 0
	v_cvt_pk_fp8_f32 v104, v112, v113
	v_cvt_pk_fp8_f32 v105, v116, v117
	v_cvt_pk_fp8_f32 v104, v114, v115 op_sel:[0,0,1]
	v_cvt_pk_fp8_f32 v105, v118, v119 op_sel:[0,0,1]
	v_lshlrev_b32_e32 v108, 8, v106
	v_or_b32_e32 v108, v108, v2
	v_lshlrev_b32_e32 v109, 7, v106
	v_lshl_or_b32 v109, v1, 3, v109
	s_mov_b64 s[36:37], exec
	s_and_b64 exec, exec, s[50:51]
	global_store_dwordx4 v108, v[100:103], s[20:21]
	global_store_dwordx2 v109, v[104:105], s[22:23]
	s_mov_b64 exec, s[36:37]
	v_cmp_eq_u32_e32 vcc, 0, v0
	v_mul_f32_e32 v110, 0x3b800000, v96
	s_lshl_b32 s40, s41, 2
	v_mov_b32_e32 v111, s40
	s_and_saveexec_b64 s[36:37], vcc
	global_store_dword v111, v110, s[24:25]
	s_mov_b64 exec, s[36:37]
.Lsw_epi_skip3:
	s_barrier
	s_add_u32 s26, s26, 1
	s_cmp_lt_u32 s26, s35
	s_cbranch_scc1 .Lsw_sweep

	.amdhsa_kernel _Z6k_spmmILb0ELi0EEvPKiPK15HIP_vector_typeIiLj2EEPKvPKfPKDF16_S9_S9_iPfPDF16_PhSC_PKhS9_SG_S9_S9_i
		.amdhsa_group_segment_fixed_size 36928
		.amdhsa_private_segment_fixed_size 0
		.amdhsa_kernarg_size 400
		.amdhsa_user_sgpr_count 2
		.amdhsa_user_sgpr_dispatch_ptr 0
		.amdhsa_user_sgpr_queue_ptr 0
		.amdhsa_user_sgpr_kernarg_segment_ptr 1
		.amdhsa_user_sgpr_dispatch_id 0
		.amdhsa_user_sgpr_kernarg_preload_length 0
		.amdhsa_user_sgpr_kernarg_preload_offset 0
		.amdhsa_user_sgpr_private_segment_size 0
		.amdhsa_uses_dynamic_stack 0
		.amdhsa_enable_private_segment 0
		.amdhsa_system_sgpr_workgroup_id_x 1
		.amdhsa_system_sgpr_workgroup_id_y 0
		.amdhsa_system_sgpr_workgroup_id_z 0
		.amdhsa_system_sgpr_workgroup_info 0
		.amdhsa_system_vgpr_workitem_id 0
		.amdhsa_next_free_vgpr 128
		.amdhsa_next_free_sgpr 64
		.amdhsa_accum_offset 128
		.amdhsa_reserve_vcc 1
		.amdhsa_float_round_mode_32 0
		.amdhsa_float_round_mode_16_64 0
		.amdhsa_float_denorm_mode_32 3
		.amdhsa_float_denorm_mode_16_64 3
		.amdhsa_dx10_clamp 1
		.amdhsa_ieee_mode 1
		.amdhsa_fp16_overflow 0
		.amdhsa_tg_split 0
		.amdhsa_exception_fp_ieee_invalid_op 0
		.amdhsa_exception_fp_denorm_src 0
		.amdhsa_exception_fp_ieee_div_zero 0
		.amdhsa_exception_fp_ieee_overflow 0
		.amdhsa_exception_fp_ieee_underflow 0
		.amdhsa_exception_fp_ieee_inexact 0
		.amdhsa_exception_int_div_zero 0
	.end_amdhsa_kernel

amdhsa.kernels:
  - .agpr_count:     0
    .args:
      - .actual_access:  read_only
        .address_space:  global
        .offset:         0
        .size:           8
        .value_kind:     global_buffer
      - .actual_access:  write_only
        .address_space:  global
        .offset:         8
        .size:           8
        .value_kind:     global_buffer
      - .offset:         16
        .size:           4
        .value_kind:     by_value
      - .offset:         20
        .size:           4
        .value_kind:     by_value
    .group_segment_fixed_size: 8192
    .kernarg_segment_align: 8
    .kernarg_segment_size: 24
    .language:       OpenCL C
    .language_version:
      - 2
      - 0
    .max_flat_workgroup_size: 1024
    .name:           _Z7k_bhistPKiPiii
    .private_segment_fixed_size: 0
    .sgpr_count:     24
    .sgpr_spill_count: 0
    .symbol:         _Z7k_bhistPKiPiii.kd
    .uniform_work_group_size: 1
    .uses_dynamic_stack: false
    .vgpr_count:     50
    .vgpr_spill_count: 0
    .wavefront_size: 64
  - .agpr_count:     0
    .args:
      - .address_space:  global
        .offset:         0
        .size:           8
        .value_kind:     global_buffer
      - .actual_access:  write_only
        .address_space:  global
        .offset:         8
        .size:           8
        .value_kind:     global_buffer
      - .offset:         16
        .size:           4
        .value_kind:     by_value
      - .offset:         20
        .size:           4
        .value_kind:     by_value
      - .offset:         24
        .size:           4
        .value_kind:     by_value
      - .actual_access:  read_only
        .address_space:  global
        .offset:         32
        .size:           8
        .value_kind:     global_buffer
      - .actual_access:  read_only
        .address_space:  global
        .offset:         40
        .size:           8
        .value_kind:     global_buffer
      - .offset:         48
        .size:           4
        .value_kind:     by_value
      - .offset:         52
        .size:           4
        .value_kind:     by_value
      - .actual_access:  write_only
        .address_space:  global
        .offset:         56
        .size:           8
        .value_kind:     global_buffer
      - .actual_access:  write_only
        .address_space:  global
        .offset:         64
        .size:           8
        .value_kind:     global_buffer
      - .actual_access:  write_only
        .address_space:  global
        .offset:         72
        .size:           8
        .value_kind:     global_buffer
    .group_segment_fixed_size: 4160
    .kernarg_segment_align: 8
    .kernarg_segment_size: 80
    .language:       OpenCL C
    .language_version:
      - 2
      - 0
    .max_flat_workgroup_size: 1024
    .name:           _Z12k_bscan_prepPiS_iiiPKfS1_iiPDF16_PfS3_
    .private_segment_fixed_size: 0
    .sgpr_count:     24
    .sgpr_spill_count: 0
    .symbol:         _Z12k_bscan_prepPiS_iiiPKfS1_iiPDF16_PfS3_.kd
    .uniform_work_group_size: 1
    .uses_dynamic_stack: false
    .vgpr_count:     28
    .vgpr_spill_count: 0
    .wavefront_size: 64
  - .agpr_count:     0
    .args:
      - .actual_access:  read_only
        .address_space:  global
        .offset:         0
        .size:           8
        .value_kind:     global_buffer
      - .actual_access:  read_only
        .address_space:  global
        .offset:         8
        .size:           8
        .value_kind:     global_buffer
      - .actual_access:  read_only
        .address_space:  global
        .offset:         16
        .size:           8
        .value_kind:     global_buffer
      - .actual_access:  read_only
        .address_space:  global
        .offset:         24
        .size:           8
        .value_kind:     global_buffer
      - .actual_access:  read_only
        .address_space:  global
        .offset:         32
        .size:           8
        .value_kind:     global_buffer
      - .actual_access:  write_only
        .address_space:  global
        .offset:         40
        .size:           8
        .value_kind:     global_buffer
      - .actual_access:  write_only
        .address_space:  global
        .offset:         48
        .size:           8
        .value_kind:     global_buffer
      - .offset:         56
        .size:           4
        .value_kind:     by_value
      - .offset:         60
        .size:           4
        .value_kind:     by_value
      - .offset:         64
        .size:           4
        .value_kind:     by_value
      - .offset:         72
        .size:           4
        .value_kind:     hidden_block_count_x
      - .offset:         76
        .size:           4
        .value_kind:     hidden_block_count_y
      - .offset:         80
        .size:           4
        .value_kind:     hidden_block_count_z
      - .offset:         84
        .size:           2
        .value_kind:     hidden_group_size_x
      - .offset:         86
        .size:           2
        .value_kind:     hidden_group_size_y
      - .offset:         88
        .size:           2
        .value_kind:     hidden_group_size_z
      - .offset:         90
        .size:           2
        .value_kind:     hidden_remainder_x
      - .offset:         92
        .size:           2
        .value_kind:     hidden_remainder_y
      - .offset:         94
        .size:           2
        .value_kind:     hidden_remainder_z
      - .offset:         112
        .size:           8
        .value_kind:     hidden_global_offset_x
      - .offset:         120
        .size:           8
        .value_kind:     hidden_global_offset_y
      - .offset:         128
        .size:           8
        .value_kind:     hidden_global_offset_z
      - .offset:         136
        .size:           2
        .value_kind:     hidden_grid_dims
    .group_segment_fixed_size: 154816
    .kernarg_segment_align: 8
    .kernarg_segment_size: 328
    .language:       OpenCL C
    .language_version:
      - 2
      - 0
    .max_flat_workgroup_size: 1024
    .name:           _Z4k_l1PKiS0_PKfS0_S0_PiP15HIP_vector_typeIiLj2EEiii
    .private_segment_fixed_size: 0
    .sgpr_count:     92
    .sgpr_spill_count: 0
    .symbol:         _Z4k_l1PKiS0_PKfS0_S0_PiP15HIP_vector_typeIiLj2EEiii.kd
    .uniform_work_group_size: 1
    .uses_dynamic_stack: false
    .vgpr_count:     128
    .vgpr_spill_count: 0
    .wavefront_size: 64
  - .agpr_count:     0
    .args:
      - .actual_access:  read_only
        .address_space:  global
        .offset:         0
        .size:           8
        .value_kind:     global_buffer
      - .actual_access:  read_only
        .address_space:  global
        .offset:         8
        .size:           8
        .value_kind:     global_buffer
      - .actual_access:  write_only
        .address_space:  global
        .offset:         16
        .size:           8
        .value_kind:     global_buffer
      - .actual_access:  write_only
        .address_space:  global
        .offset:         24
        .size:           8
        .value_kind:     global_buffer
      - .offset:         32
        .size:           4
        .value_kind:     by_value
      - .offset:         36
        .size:           4
        .value_kind:     by_value
      - .offset:         40
        .size:           4
        .value_kind:     hidden_block_count_x
      - .offset:         44
        .size:           4
        .value_kind:     hidden_block_count_y
      - .offset:         48
        .size:           4
        .value_kind:     hidden_block_count_z
      - .offset:         52
        .size:           2
        .value_kind:     hidden_group_size_x
      - .offset:         54
        .size:           2
        .value_kind:     hidden_group_size_y
      - .offset:         56
        .size:           2
        .value_kind:     hidden_group_size_z
      - .offset:         58
        .size:           2
        .value_kind:     hidden_remainder_x
      - .offset:         60
        .size:           2
        .value_kind:     hidden_remainder_y
      - .offset:         62
        .size:           2
        .value_kind:     hidden_remainder_z
      - .offset:         80
        .size:           8
        .value_kind:     hidden_global_offset_x
      - .offset:         88
        .size:           8
        .value_kind:     hidden_global_offset_y
      - .offset:         96
        .size:           8
        .value_kind:     hidden_global_offset_z
      - .offset:         104
        .size:           2
        .value_kind:     hidden_grid_dims
    .group_segment_fixed_size: 147520
    .kernarg_segment_align: 8
    .kernarg_segment_size: 296
    .language:       OpenCL C
    .language_version:
      - 2
      - 0
    .max_flat_workgroup_size: 1024
    .name:           _Z4k_l2PK15HIP_vector_typeIiLj2EEPKiPiPS0_ii
    .private_segment_fixed_size: 0
    .sgpr_count:     56
    .sgpr_spill_count: 0
    .symbol:         _Z4k_l2PK15HIP_vector_typeIiLj2EEPKiPiPS0_ii.kd
    .uniform_work_group_size: 1
    .uses_dynamic_stack: false
    .vgpr_count:     96
    .vgpr_spill_count: 0
    .wavefront_size: 64
  - .agpr_count:     0
    .args:
      - .actual_access:  read_only
        .address_space:  global
        .offset:         0
        .size:           8
        .value_kind:     global_buffer
      - .actual_access:  read_only
        .address_space:  global
        .offset:         8
        .size:           8
        .value_kind:     global_buffer
      - .actual_access:  read_only
        .address_space:  global
        .offset:         16
        .size:           8
        .value_kind:     global_buffer
      - .actual_access:  read_only
        .address_space:  global
        .offset:         24
        .size:           8
        .value_kind:     global_buffer
      - .actual_access:  read_only
        .address_space:  global
        .offset:         32
        .size:           8
        .value_kind:     global_buffer
      - .actual_access:  read_only
        .address_space:  global
        .offset:         40
        .size:           8
        .value_kind:     global_buffer
      - .actual_access:  read_only
        .address_space:  global
        .offset:         48
        .size:           8
        .value_kind:     global_buffer
      - .offset:         56
        .size:           4
        .value_kind:     by_value
      - .actual_access:  read_only
        .address_space:  global
        .offset:         64
        .size:           8
        .value_kind:     global_buffer
      - .actual_access:  write_only
        .address_space:  global
        .offset:         72
        .size:           8
        .value_kind:     global_buffer
      - .actual_access:  write_only
        .address_space:  global
        .offset:         80
        .size:           8
        .value_kind:     global_buffer
      - .actual_access:  write_only
        .address_space:  global
        .offset:         88
        .size:           8
        .value_kind:     global_buffer
      - .actual_access:  read_only
        .address_space:  global
        .offset:         96
        .size:           8
        .value_kind:     global_buffer
      - .actual_access:  read_only
        .address_space:  global
        .offset:         104
        .size:           8
        .value_kind:     global_buffer
      - .actual_access:  read_only
        .address_space:  global
        .offset:         112
        .size:           8
        .value_kind:     global_buffer
      - .actual_access:  read_only
        .address_space:  global
        .offset:         120
        .size:           8
        .value_kind:     global_buffer
      - .actual_access:  read_only
        .address_space:  global
        .offset:         128
        .size:           8
        .value_kind:     global_buffer
      - .offset:         136
        .size:           4
        .value_kind:     by_value
      - .offset:         144
        .size:           4
        .value_kind:     hidden_block_count_x
      - .offset:         148
        .size:           4
        .value_kind:     hidden_block_count_y
      - .offset:         152
        .size:           4
        .value_kind:     hidden_block_count_z
      - .offset:         156
        .size:           2
        .value_kind:     hidden_group_size_x
      - .offset:         158
        .size:           2
        .value_kind:     hidden_group_size_y
      - .offset:         160
        .size:           2
        .value_kind:     hidden_group_size_z
      - .offset:         162
        .size:           2
        .value_kind:     hidden_remainder_x
      - .offset:         164
        .size:           2
        .value_kind:     hidden_remainder_y
      - .offset:         166
        .size:           2
        .value_kind:     hidden_remainder_z
      - .offset:         184
        .size:           8
        .value_kind:     hidden_global_offset_x
      - .offset:         192
        .size:           8
        .value_kind:     hidden_global_offset_y
      - .offset:         200
        .size:           8
        .value_kind:     hidden_global_offset_z
      - .offset:         208
        .size:           2
        .value_kind:     hidden_grid_dims
    .group_segment_fixed_size: 36928
    .kernarg_segment_align: 8
    .kernarg_segment_size: 400
    .language:       OpenCL C
    .language_version:
      - 2
      - 0
    .max_flat_workgroup_size: 512
    .name:           _Z6k_spmmILb0ELi0EEvPKiPK15HIP_vector_typeIiLj2EEPKvPKfPKDF16_S9_S9_iPfPDF16_PhSC_PKhS9_SG_S9_S9_i
    .private_segment_fixed_size: 0
    .sgpr_count:     70
    .sgpr_spill_count: 0
    .symbol:         _Z6k_spmmILb0ELi0EEvPKiPK15HIP_vector_typeIiLj2EEPKvPKfPKDF16_S9_S9_iPfPDF16_PhSC_PKhS9_SG_S9_S9_i.kd
    .uniform_work_group_size: 1
    .uses_dynamic_stack: false
    .vgpr_count:     128
    .vgpr_spill_count: 0
    .wavefront_size: 64
  - .agpr_count:     0
    .args:
      - .actual_access:  read_only
        .address_space:  global
        .offset:         0
        .size:           8
        .value_kind:     global_buffer
      - .actual_access:  read_only
        .address_space:  global
        .offset:         8
        .size:           8
        .value_kind:     global_buffer
      - .actual_access:  read_only
        .address_space:  global
        .offset:         16
        .size:           8
        .value_kind:     global_buffer
      - .actual_access:  read_only
        .address_space:  global
        .offset:         24
        .size:           8
        .value_kind:     global_buffer
      - .actual_access:  read_only
        .address_space:  global
        .offset:         32
        .size:           8
        .value_kind:     global_buffer
      - .actual_access:  read_only
        .address_space:  global
        .offset:         40
        .size:           8
        .value_kind:     global_buffer
      - .actual_access:  read_only
        .address_space:  global
        .offset:         48
        .size:           8
        .value_kind:     global_buffer
      - .offset:         56
        .size:           4
        .value_kind:     by_value
      - .actual_access:  read_only
        .address_space:  global
        .offset:         64
        .size:           8
        .value_kind:     global_buffer
      - .actual_access:  read_only
        .address_space:  global
        .offset:         72
        .size:           8
        .value_kind:     global_buffer
      - .actual_access:  write_only
        .address_space:  global
        .offset:         80
        .size:           8
        .value_kind:     global_buffer
      - .actual_access:  write_only
        .address_space:  global
        .offset:         88
        .size:           8
        .value_kind:     global_buffer
      - .actual_access:  read_only
        .address_space:  global
        .offset:         96
        .size:           8
        .value_kind:     global_buffer
      - .actual_access:  read_only
        .address_space:  global
        .offset:         104
        .size:           8
        .value_kind:     global_buffer
      - .actual_access:  read_only
        .address_space:  global
        .offset:         112
        .size:           8
        .value_kind:     global_buffer
      - .actual_access:  read_only
        .address_space:  global
        .offset:         120
        .size:           8
        .value_kind:     global_buffer
      - .actual_access:  read_only
        .address_space:  global
        .offset:         128
        .size:           8
        .value_kind:     global_buffer
      - .offset:         136
        .size:           4
        .value_kind:     by_value
      - .offset:         144
        .size:           4
        .value_kind:     hidden_block_count_x
      - .offset:         148
        .size:           4
        .value_kind:     hidden_block_count_y
      - .offset:         152
        .size:           4
        .value_kind:     hidden_block_count_z
      - .offset:         156
        .size:           2
        .value_kind:     hidden_group_size_x
      - .offset:         158
        .size:           2
        .value_kind:     hidden_group_size_y
      - .offset:         160
        .size:           2
        .value_kind:     hidden_group_size_z
      - .offset:         162
        .size:           2
        .value_kind:     hidden_remainder_x
      - .offset:         164
        .size:           2
        .value_kind:     hidden_remainder_y
      - .offset:         166
        .size:           2
        .value_kind:     hidden_remainder_z
      - .offset:         184
        .size:           8
        .value_kind:     hidden_global_offset_x
      - .offset:         192
        .size:           8
        .value_kind:     hidden_global_offset_y
      - .offset:         200
        .size:           8
        .value_kind:     hidden_global_offset_z
      - .offset:         208
        .size:           2
        .value_kind:     hidden_grid_dims
    .group_segment_fixed_size: 16416
    .kernarg_segment_align: 8
    .kernarg_segment_size: 400
    .language:       OpenCL C
    .language_version:
      - 2
      - 0
    .max_flat_workgroup_size: 512
    .name:           _Z6k_spmmILb1ELi1EEvPKiPK15HIP_vector_typeIiLj2EEPKvPKfPKDF16_S9_S9_iPfPDF16_PhSC_PKhS9_SG_S9_S9_i
    .private_segment_fixed_size: 0
    .sgpr_count:     36
    .sgpr_spill_count: 0
    .symbol:         _Z6k_spmmILb1ELi1EEvPKiPK15HIP_vector_typeIiLj2EEPKvPKfPKDF16_S9_S9_iPfPDF16_PhSC_PKhS9_SG_S9_S9_i.kd
    .uniform_work_group_size: 1
    .uses_dynamic_stack: false
    .vgpr_count:     64
    .vgpr_spill_count: 0
    .wavefront_size: 64
  - .agpr_count:     0
    .args:
      - .actual_access:  read_only
        .address_space:  global
        .offset:         0
        .size:           8
        .value_kind:     global_buffer
      - .actual_access:  read_only
        .address_space:  global
        .offset:         8
        .size:           8
        .value_kind:     global_buffer
      - .actual_access:  read_only
        .address_space:  global
        .offset:         16
        .size:           8
        .value_kind:     global_buffer
      - .actual_access:  read_only
        .address_space:  global
        .offset:         24
        .size:           8
        .value_kind:     global_buffer
      - .actual_access:  read_only
        .address_space:  global
        .offset:         32
        .size:           8
        .value_kind:     global_buffer
      - .actual_access:  read_only
        .address_space:  global
        .offset:         40
        .size:           8
        .value_kind:     global_buffer
      - .actual_access:  read_only
        .address_space:  global
        .offset:         48
        .size:           8
        .value_kind:     global_buffer
      - .offset:         56
        .size:           4
        .value_kind:     by_value
      - .actual_access:  write_only
        .address_space:  global
        .offset:         64
        .size:           8
        .value_kind:     global_buffer
      - .actual_access:  read_only
        .address_space:  global
        .offset:         72
        .size:           8
        .value_kind:     global_buffer
      - .actual_access:  read_only
        .address_space:  global
        .offset:         80
        .size:           8
        .value_kind:     global_buffer
      - .actual_access:  read_only
        .address_space:  global
        .offset:         88
        .size:           8
        .value_kind:     global_buffer
      - .actual_access:  read_only
        .address_space:  global
        .offset:         96
        .size:           8
        .value_kind:     global_buffer
      - .actual_access:  read_only
        .address_space:  global
        .offset:         104
        .size:           8
        .value_kind:     global_buffer
      - .actual_access:  read_only
        .address_space:  global
        .offset:         112
        .size:           8
        .value_kind:     global_buffer
      - .actual_access:  read_only
        .address_space:  global
        .offset:         120
        .size:           8
        .value_kind:     global_buffer
      - .actual_access:  read_only
        .address_space:  global
        .offset:         128
        .size:           8
        .value_kind:     global_buffer
      - .offset:         136
        .size:           4
        .value_kind:     by_value
      - .offset:         144
        .size:           4
        .value_kind:     hidden_block_count_x
      - .offset:         148
        .size:           4
        .value_kind:     hidden_block_count_y
      - .offset:         152
        .size:           4
        .value_kind:     hidden_block_count_z
      - .offset:         156
        .size:           2
        .value_kind:     hidden_group_size_x
      - .offset:         158
        .size:           2
        .value_kind:     hidden_group_size_y
      - .offset:         160
        .size:           2
        .value_kind:     hidden_group_size_z
      - .offset:         162
        .size:           2
        .value_kind:     hidden_remainder_x
      - .offset:         164
        .size:           2
        .value_kind:     hidden_remainder_y
      - .offset:         166
        .size:           2
        .value_kind:     hidden_remainder_z
      - .offset:         184
        .size:           8
        .value_kind:     hidden_global_offset_x
      - .offset:         192
        .size:           8
        .value_kind:     hidden_global_offset_y
      - .offset:         200
        .size:           8
        .value_kind:     hidden_global_offset_z
      - .offset:         208
        .size:           2
        .value_kind:     hidden_grid_dims
    .group_segment_fixed_size: 16384
    .kernarg_segment_align: 8
    .kernarg_segment_size: 400
    .language:       OpenCL C
    .language_version:
      - 2
      - 0
    .max_flat_workgroup_size: 512
    .name:           _Z6k_spmmILb1ELi2EEvPKiPK15HIP_vector_typeIiLj2EEPKvPKfPKDF16_S9_S9_iPfPDF16_PhSC_PKhS9_SG_S9_S9_i
    .private_segment_fixed_size: 0
    .sgpr_count:     42
    .sgpr_spill_count: 0
    .symbol:         _Z6k_spmmILb1ELi2EEvPKiPK15HIP_vector_typeIiLj2EEPKvPKfPKDF16_S9_S9_iPfPDF16_PhSC_PKhS9_SG_S9_S9_i.kd
    .uniform_work_group_size: 1
    .uses_dynamic_stack: false
    .vgpr_count:     64
    .vgpr_spill_count: 0
    .wavefront_size: 64
